# icache warm chains: one touch point per 128-byte line (instruction cache lines are 128 B), halves every chain
# speedup vs baseline: 1.0334x; 1.0319x over previous
.LBB0_5:
	s_andn2_b64 vcc, exec, s[6:7]
	s_cbranch_vccnz .LBB0_38
	s_add_i32 s3, s2, 0xffffff3c
	v_lshl_or_b32 v2, s3, 10, v0
	s_cmp_gt_u32 s3, 7
	s_mov_b64 s[6:7], -1
	s_cbranch_scc0 .LBB0_30
	s_load_dwordx2 s[6:7], s[0:1], 0x48
	s_cmp_gt_u32 s3, 9
	s_mov_b64 s[8:9], -1
	s_cbranch_scc0 .LBB0_27
	s_movk_i32 s8, 0x2900
	v_cmp_gt_u32_e32 vcc, s8, v2
	s_and_saveexec_b64 s[8:9], vcc
	s_cbranch_execz .LBB0_26
	s_load_dwordx2 s[10:11], s[0:1], 0x38
	v_add_u32_e32 v1, 0xffffd800, v2
	v_lshlrev_b32_e32 v4, 1, v0
	v_lshrrev_b32_e32 v1, 3, v1
	v_and_b32_e32 v4, 0x60, v4

.Lw0b2:
	v_and_b32_e32 v1, 0x1ffffff8, v1
	v_and_b32_e32 v3, 15, v0
	v_add_u32_e32 v4, v1, v4
	v_cmp_gt_u32_e32 vcc, 2, v3
	v_mov_b32_e32 v1, 0
	v_lshl_or_b32 v4, v4, 1, v3
	v_mov_b32_e32 v3, 0
	s_and_saveexec_b64 s[12:13], vcc
	s_cbranch_execz .LBB0_11
	v_mov_b32_e32 v5, 0
	s_waitcnt lgkmcnt(0)
	v_lshl_add_u64 v[6:7], v[4:5], 2, s[10:11]
	global_load_dword v3, v[6:7], off
	s_waitcnt vmcnt(0)
	v_cvt_f16_f32_e32 v3, v3

.Lw0b3:
	v_mov_b32_e32 v6, 0
	v_mov_b32_e32 v7, 0
	s_and_saveexec_b64 s[12:13], vcc
	s_cbranch_execz .LBB0_15
	v_mov_b32_e32 v5, 0
	s_waitcnt lgkmcnt(0)
	v_lshl_add_u64 v[8:9], v[4:5], 2, s[10:11]
	global_load_dword v5, v[8:9], off offset:16
	s_waitcnt vmcnt(0)
	v_cvt_f16_f32_e32 v7, v5

.LBB0_17:
	s_or_b64 exec, exec, s[12:13]
	v_mov_b32_e32 v8, 0
	v_mov_b32_e32 v9, 0
	s_and_saveexec_b64 s[12:13], vcc
	s_cbranch_execz .LBB0_19
	v_mov_b32_e32 v5, 0
	s_waitcnt lgkmcnt(0)
	v_lshl_add_u64 v[10:11], v[4:5], 2, s[10:11]

.Lw0b4:
	global_load_dword v5, v[10:11], off offset:32
	s_waitcnt vmcnt(0)
	v_cvt_f16_f32_e32 v9, v5

.LBB0_23:
	s_or_b64 exec, exec, s[12:13]
	s_and_saveexec_b64 s[12:13], vcc
.Lw0t5:
	s_cbranch_execz .Lw0c5
.Lw0b5:
	s_cbranch_execz .LBB0_25
	v_mov_b32_e32 v5, 0
	s_waitcnt lgkmcnt(0)
	v_lshl_add_u64 v[4:5], v[4:5], 2, s[10:11]
	global_load_dword v4, v[4:5], off offset:56
	s_waitcnt vmcnt(0)
	v_cvt_f16_f32_e32 v10, v4

.LBB0_26:
	s_or_b64 exec, exec, s[8:9]
.Lw0t6:
	s_cbranch_execz .Lw0c6
.Lw0b6:
	s_mov_b64 s[8:9], 0
.LBB0_27:
	s_andn2_b64 vcc, exec, s[8:9]
	s_cbranch_vccnz .LBB0_29
	s_load_dwordx2 s[8:9], s[0:1], 0x30
	v_lshlrev_b32_e32 v1, 3, v0
	v_lshrrev_b32_e32 v3, 4, v0
	v_add_u32_e32 v8, 0xffffe000, v2
	v_and_b32_e32 v1, 0x60, v1
	v_and_b32_e32 v3, 28, v3
	v_and_b32_e32 v4, 3, v0
	v_or3_b32 v1, v3, v4, v1
	v_lshlrev_b32_e32 v3, 1, v0
	v_lshrrev_b32_e32 v4, 6, v8
	v_and_b32_e32 v3, 0x60, v3
	v_and_b32_e32 v4, 0x3fffff8, v4
	v_add_u32_e32 v4, v4, v3
	v_lshlrev_b32_e32 v6, 2, v1
	v_mov_b32_e32 v7, 0
	s_waitcnt lgkmcnt(0)
	v_lshl_add_u64 v[10:11], s[8:9], 0, v[6:7]
	v_or_b32_e32 v6, 1, v4
	v_lshlrev_b64 v[14:15], 9, v[6:7]
	v_or_b32_e32 v6, 2, v4

.Lw0b7:
	v_lshlrev_b64 v[16:17], 9, v[6:7]
	v_or_b32_e32 v6, 3, v4
	v_lshlrev_b64 v[18:19], 9, v[6:7]
	v_or_b32_e32 v6, 4, v4
	v_lshlrev_b64 v[20:21], 9, v[6:7]
	v_or_b32_e32 v6, 5, v4
	v_mov_b32_e32 v5, v7
	v_lshlrev_b64 v[22:23], 9, v[6:7]
	v_or_b32_e32 v6, 6, v4
	v_lshlrev_b64 v[12:13], 9, v[4:5]
	v_lshlrev_b64 v[24:25], 9, v[6:7]
	v_or_b32_e32 v6, 7, v4
	v_lshl_add_u64 v[12:13], v[10:11], 0, v[12:13]
	v_lshlrev_b64 v[4:5], 9, v[6:7]
	v_lshl_add_u64 v[14:15], v[10:11], 0, v[14:15]
	v_lshl_add_u64 v[16:17], v[10:11], 0, v[16:17]
	v_lshl_add_u64 v[18:19], v[10:11], 0, v[18:19]
	v_lshl_add_u64 v[20:21], v[10:11], 0, v[20:21]
	v_lshl_add_u64 v[22:23], v[10:11], 0, v[22:23]

.Lw0b8:
	v_lshl_add_u64 v[24:25], v[10:11], 0, v[24:25]
	v_lshl_add_u64 v[4:5], v[10:11], 0, v[4:5]
	global_load_dword v1, v[12:13], off
	global_load_dword v3, v[14:15], off
	global_load_dword v6, v[16:17], off
	global_load_dword v10, v[18:19], off
	global_load_dword v11, v[20:21], off
	global_load_dword v26, v[22:23], off
	global_load_dword v27, v[24:25], off
	global_load_dword v28, v[4:5], off
	v_mov_b32_e32 v9, v7
	v_lshl_add_u64 v[8:9], v[8:9], 4, s[6:7]
	s_waitcnt vmcnt(6)
	v_cvt_pk_f16_f32 v4, v1, v3
	s_waitcnt vmcnt(4)
	v_cvt_pk_f16_f32 v5, v6, v10
	s_waitcnt vmcnt(2)

.Lw0b9:
	v_cvt_pk_f16_f32 v6, v11, v26
	s_waitcnt vmcnt(0)
	v_cvt_pk_f16_f32 v7, v27, v28
	global_store_dwordx4 v[8:9], v[4:7], off

.LBB0_30:
	s_andn2_b64 vcc, exec, s[6:7]
	s_cbranch_vccnz .LBB0_32
	s_load_dwordx2 s[6:7], s[0:1], 0x28
	v_lshlrev_b32_e32 v1, 3, v0
	v_lshrrev_b32_e32 v3, 4, v2
	v_and_b32_e32 v1, 0x60, v1
	v_and_b32_e32 v4, 28, v3
	v_and_b32_e32 v5, 3, v0
	v_lshrrev_b32_e32 v6, 1, v0
	v_and_b32_e32 v6, 24, v6
	s_movk_i32 s8, 0x1e0
	v_or3_b32 v1, v1, v5, v4
	v_and_or_b32 v3, v3, s8, v6
	v_lshlrev_b32_e32 v1, 2, v1
	v_lshl_or_b32 v1, v3, 9, v1
	s_waitcnt lgkmcnt(0)
	global_load_dword v4, v1, s[6:7] offset:1024

.Lw0b10:
	global_load_dword v5, v1, s[6:7] offset:1536
	global_load_dword v6, v1, s[6:7] offset:2048
	global_load_dword v7, v1, s[6:7] offset:3072
	global_load_dword v8, v1, s[6:7] offset:3584
	global_load_dword v9, v1, s[6:7] offset:2560
	global_load_dword v10, v1, s[6:7]
	global_load_dword v11, v1, s[6:7] offset:512
	s_load_dwordx2 s[6:7], s[0:1], 0x40
	v_mov_b32_e32 v3, 0
	s_waitcnt lgkmcnt(0)
	v_lshl_add_u64 v[2:3], v[2:3], 4, s[6:7]
	s_waitcnt vmcnt(6)
	v_cvt_pk_f16_f32 v5, v4, v5
	s_waitcnt vmcnt(3)
	v_cvt_pk_f16_f32 v7, v7, v8
	s_waitcnt vmcnt(2)
	v_cvt_pk_f16_f32 v6, v6, v9
	s_waitcnt vmcnt(0)

.Lw0b11:
	v_cvt_pk_f16_f32 v4, v10, v11
	global_store_dwordx4 v[2:3], v[4:7], off

.LBB0_35:
	s_andn2_saveexec_b64 s[8:9], s[8:9]
.Lw0t12:
	s_cbranch_execz .Lw0c12
.Lw0b12:
	s_cbranch_execz .LBB0_37
	v_mov_b32_e32 v3, 0
	s_waitcnt lgkmcnt(0)
	v_lshl_add_u64 v[4:5], s[4:5], 0, v[2:3]
	v_add_co_u32_e32 v6, vcc, 0x186a000, v4
	v_mov_b32_e32 v2, v3
	s_nop 0
	v_addc_co_u32_e32 v7, vcc, 0, v5, vcc
	v_mov_b32_e32 v4, v3
	v_mov_b32_e32 v5, v3
	global_store_dwordx4 v[6:7], v[2:5], off

.LBB0_39:
	s_andn2_b64 vcc, exec, s[4:5]
	s_cbranch_vccnz .LBB0_121
	s_mul_hi_i32 s3, s2, 0x5397829d
	s_load_dwordx4 s[4:7], s[0:1], 0x0
	s_lshr_b32 s8, s3, 31
	s_ashr_i32 s21, s3, 5
	s_add_i32 s21, s21, s8
	s_mul_i32 s3, s21, 0x62
	s_sub_i32 s25, s2, s3
	s_addk_i32 s2, 0x61
	s_cmpk_lt_u32 s2, 0xc3
	s_waitcnt lgkmcnt(0)
	s_cselect_b32 s16, s4, s6
	s_cselect_b32 s17, s5, s7

.Lw0b13:
	s_add_u32 s18, s16, 0x30d400
	s_addc_u32 s19, s17, 0
	s_lshl_b32 s20, s25, 13
	s_min_i32 s24, s20, 0xc1500
	s_addk_i32 s24, 0x2000
	v_or_b32_e32 v2, s20, v0
	v_cmp_gt_i32_e32 vcc, s24, v2
	v_mov_b32_e32 v1, -1
	v_ashrrev_i32_e32 v3, 31, v2
	v_mov_b32_e32 v21, -1
	s_and_saveexec_b64 s[2:3], vcc
	s_cbranch_execz .LBB0_42
	v_lshl_add_u64 v[4:5], v[2:3], 2, s[18:19]
	global_load_dword v21, v[4:5], off nt
.LBB0_42:
	s_or_b64 exec, exec, s[2:3]
	v_or_b32_e32 v4, 0x400, v2
	v_cmp_gt_i32_e64 s[2:3], s24, v4
	v_ashrrev_i32_e32 v5, 31, v4
	s_and_saveexec_b64 s[4:5], s[2:3]
	s_cbranch_execz .LBB0_44
	v_lshl_add_u64 v[6:7], v[4:5], 2, s[18:19]
.Lw0t14:
	s_cbranch_execz .Lw0c14
.Lw0b14:
	global_load_dword v1, v[6:7], off nt

.LBB0_48:
	s_or_b64 exec, exec, s[8:9]
	v_or_b32_e32 v10, 0x1000, v2
.Lw0t15:
	s_cbranch_execz .Lw0c15
.Lw0b15:
	v_cmp_gt_i32_e64 s[8:9], s24, v10
	v_mov_b32_e32 v19, -1
	v_ashrrev_i32_e32 v11, 31, v10
	v_mov_b32_e32 v23, -1
	s_and_saveexec_b64 s[10:11], s[8:9]
	s_cbranch_execz .LBB0_50
	v_lshl_add_u64 v[12:13], v[10:11], 2, s[18:19]
	global_load_dword v23, v[12:13], off nt

.LBB0_58:
	s_or_b64 exec, exec, s[18:19]
	s_and_saveexec_b64 s[18:19], s[2:3]
	s_cbranch_execz .LBB0_60
	v_lshl_add_u64 v[2:3], v[4:5], 2, s[16:17]

.Lw0b17:
	global_load_dword v25, v[2:3], off nt

.LBB0_66:
	s_or_b64 exec, exec, s[2:3]
	s_and_saveexec_b64 s[2:3], s[10:11]
	s_cbranch_execz .LBB0_68

.Lw0b18:
	v_lshl_add_u64 v[2:3], v[12:13], 2, s[16:17]
	global_load_dword v4, v[2:3], off nt

.LBB0_72:
	s_or_b64 exec, exec, s[2:3]
	s_movk_i32 s2, 0xc4
	v_cmp_gt_u32_e64 s[16:17], s2, v0
	v_lshlrev_b32_e32 v2, 2, v0
	s_and_saveexec_b64 s[2:3], s[16:17]
	v_mov_b32_e32 v8, 0
	ds_write_b32 v2, v8 offset:33552
	s_or_b64 exec, exec, s[2:3]
	s_waitcnt lgkmcnt(0)

.Lw0b19:
	s_waitcnt vmcnt(0)
	v_cmp_lt_i32_e32 vcc, -1, v21
	v_mov_b32_e32 v8, 0
	v_lshrrev_b32_e32 v14, 7, v21
	v_mov_b32_e32 v12, 0
	s_barrier
	s_and_saveexec_b64 s[2:3], vcc
	v_and_b32_e32 v9, 0x1fffffc, v14
	v_mov_b32_e32 v10, 1
	ds_add_rtn_u32 v12, v9, v10 offset:33552
	s_or_b64 exec, exec, s[2:3]
	v_cmp_lt_i32_e64 s[2:3], -1, v1
	v_lshrrev_b32_e32 v13, 7, v1
	s_and_saveexec_b64 s[4:5], s[2:3]
	v_and_b32_e32 v8, 0x1fffffc, v13
	v_mov_b32_e32 v9, 1
	ds_add_rtn_u32 v8, v8, v9 offset:33552
	s_or_b64 exec, exec, s[4:5]
	v_cmp_lt_i32_e64 s[4:5], -1, v22
	v_mov_b32_e32 v9, 0
	v_lshrrev_b32_e32 v17, 7, v22
	v_mov_b32_e32 v15, 0
	s_and_saveexec_b64 s[6:7], s[4:5]
	v_and_b32_e32 v10, 0x1fffffc, v17

.Lw0b20:
	v_mov_b32_e32 v11, 1
	ds_add_rtn_u32 v15, v10, v11 offset:33552
	s_or_b64 exec, exec, s[6:7]
	v_cmp_lt_i32_e64 s[6:7], -1, v18
	v_lshrrev_b32_e32 v16, 7, v18
	s_and_saveexec_b64 s[8:9], s[6:7]
	v_and_b32_e32 v9, 0x1fffffc, v16
	v_mov_b32_e32 v10, 1
	ds_add_rtn_u32 v9, v9, v10 offset:33552
	s_or_b64 exec, exec, s[8:9]
	v_cmp_lt_i32_e64 s[8:9], -1, v23
	v_mov_b32_e32 v10, 0
	v_lshrrev_b32_e32 v33, 7, v23
	v_mov_b32_e32 v28, 0
	s_and_saveexec_b64 s[10:11], s[8:9]
	v_and_b32_e32 v11, 0x1fffffc, v33
	v_mov_b32_e32 v28, 1
	ds_add_rtn_u32 v28, v11, v28 offset:33552
	s_or_b64 exec, exec, s[10:11]
	v_cmp_lt_i32_e64 s[12:13], -1, v19
	v_lshrrev_b32_e32 v32, 7, v19
	s_and_saveexec_b64 s[10:11], s[12:13]
	v_and_b32_e32 v10, 0x1fffffc, v32

.Lw0b21:
	v_mov_b32_e32 v11, 1
	ds_add_rtn_u32 v10, v10, v11 offset:33552
	s_or_b64 exec, exec, s[10:11]
	v_cmp_lt_i32_e64 s[10:11], -1, v24
	v_mov_b32_e32 v11, 0
	v_lshrrev_b32_e32 v31, 7, v24
	v_mov_b32_e32 v29, 0
	s_and_saveexec_b64 s[14:15], s[10:11]
	v_and_b32_e32 v29, 0x1fffffc, v31
	v_mov_b32_e32 v30, 1
	ds_add_rtn_u32 v29, v29, v30 offset:33552
	s_or_b64 exec, exec, s[14:15]
	v_cmp_lt_i32_e64 s[14:15], -1, v20
	v_lshrrev_b32_e32 v30, 7, v20
	s_and_saveexec_b64 s[18:19], s[14:15]
	v_and_b32_e32 v11, 0x1fffffc, v30
	v_mov_b32_e32 v34, 1
	ds_add_rtn_u32 v11, v11, v34 offset:33552
	s_or_b64 exec, exec, s[18:19]
	v_mov_b32_e32 v34, 0
	s_waitcnt lgkmcnt(0)
	s_barrier
	s_and_saveexec_b64 s[18:19], s[16:17]

.Lw0b22:
	ds_read_b32 v34, v2 offset:33552
	s_or_b64 exec, exec, s[18:19]
	s_waitcnt lgkmcnt(0)
	v_add_u32_dpp v35, v34, v34 row_shr:1 row_mask:0xf bank_mask:0xf bound_ctrl:1
	v_and_b32_e32 v36, 63, v0
	v_cmp_eq_u32_e64 s[18:19], 63, v36
	v_add_u32_dpp v35, v35, v35 row_shr:2 row_mask:0xf bank_mask:0xf bound_ctrl:1
	s_nop 1
	v_add_u32_dpp v35, v35, v35 row_shr:4 row_mask:0xf bank_mask:0xf bound_ctrl:1
	s_nop 1
	v_add_u32_dpp v35, v35, v35 row_shr:8 row_mask:0xf bank_mask:0xf bound_ctrl:1
	s_nop 1
	v_add_u32_dpp v35, v35, v35 row_bcast:15 row_mask:0xa bank_mask:0xf
	s_nop 1
	v_add_u32_dpp v35, v35, v35 row_bcast:31 row_mask:0xc bank_mask:0xf
	s_and_saveexec_b64 s[22:23], s[18:19]
	v_lshrrev_b32_e32 v36, 4, v0
	v_and_b32_e32 v36, 60, v36
	ds_write_b32 v36, v35 offset:34336
	s_or_b64 exec, exec, s[22:23]
	s_waitcnt lgkmcnt(0)
	s_barrier

.Lw0b23:
	s_and_saveexec_b64 s[18:19], s[16:17]
	s_cbranch_execz .LBB0_96
	v_mov_b32_e32 v36, 0
	ds_read_b96 v[36:38], v36 offset:34336
	s_movk_i32 s16, 0xbf
	s_movk_i32 s22, 0x7f
	v_cmp_lt_u32_e64 s[16:17], s16, v0
	v_sub_u32_e32 v35, v35, v34
	s_load_dwordx4 s[28:31], s[0:1], 0x10
	s_waitcnt lgkmcnt(0)
	v_cndmask_b32_e64 v38, 0, v38, s[16:17]
	v_cmp_lt_u32_e64 s[16:17], s22, v0
	s_nop 1
	v_cndmask_b32_e64 v37, 0, v37, s[16:17]
	v_cmp_lt_u32_e64 s[16:17], 63, v0
	s_nop 1
	v_cndmask_b32_e64 v36, 0, v36, s[16:17]
	v_add_u32_e32 v36, v37, v36
	s_mul_i32 s16, s21, 0xc4
	v_add3_u32 v40, v38, v36, v35
	v_add_u32_e32 v35, s16, v0

.Lw0b24:
	s_movk_i32 s16, 0x62
	v_mul_lo_u32 v35, v35, s16
	v_add_u32_e32 v36, s25, v35
	v_ashrrev_i32_e32 v37, 31, v36
	v_lshlrev_b64 v[36:37], 2, v[36:37]
	v_lshl_add_u64 v[38:39], s[28:29], 0, v[36:37]
	global_store_dword v[38:39], v34, off
	v_lshl_add_u64 v[34:35], s[30:31], 0, v[36:37]
	ds_write_b32 v2, v40 offset:32768
	global_store_dword v[34:35], v40, off

.LBB0_105:
	s_or_b64 exec, exec, s[2:3]
	s_mul_hi_i32 s2, s21, 0x30d400
.Lw0t26:
	s_cbranch_execz .Lw0c26
.Lw0b26:
	s_mul_i32 s21, s21, 0x30d400
	s_waitcnt lgkmcnt(0)
	s_add_u32 s3, s0, s21
	s_addc_u32 s2, s1, s2
	s_ashr_i32 s21, s20, 31
	s_lshl_b64 s[0:1], s[20:21], 2
	s_add_u32 s0, s3, s0
	s_addc_u32 s1, s2, s1
	s_sub_i32 s4, s24, s20
	v_cmp_gt_i32_e32 vcc, s4, v0
	s_barrier
	s_and_saveexec_b64 s[2:3], vcc
	s_cbranch_execz .LBB0_107
	ds_read_b32 v1, v2
	s_waitcnt lgkmcnt(0)
	global_store_dword v2, v1, s[0:1]
.LBB0_107:
	s_or_b64 exec, exec, s[2:3]
	v_or_b32_e32 v1, 0x400, v0
	v_cmp_gt_i32_e32 vcc, s4, v1
	s_and_saveexec_b64 s[2:3], vcc
	s_cbranch_execz .LBB0_109
	ds_read_b32 v3, v2 offset:4096
	v_lshlrev_b32_e32 v1, 2, v1
	s_waitcnt lgkmcnt(0)
	global_store_dword v1, v3, s[0:1]
.LBB0_109:
.Lw0t27:
	s_cbranch_execz .Lw0c27

.LBB0_113:
	s_or_b64 exec, exec, s[2:3]
	v_or_b32_e32 v1, 0x1000, v0
	v_cmp_gt_i32_e32 vcc, s4, v1
	s_and_saveexec_b64 s[2:3], vcc
	s_cbranch_execz .LBB0_115
.Lw0t28:
	s_cbranch_execz .Lw0c28
.Lw0b28:
	ds_read_b32 v3, v2 offset:16384
	v_lshlrev_b32_e32 v1, 2, v1
	s_waitcnt lgkmcnt(0)
	global_store_dword v1, v3, s[0:1]

.Lw0b29:
	v_or_b32_e32 v0, 0x1c00, v0
	v_cmp_gt_i32_e32 vcc, s4, v0
	s_and_saveexec_b64 s[2:3], vcc
	s_cbranch_execz .LBB0_121
	ds_read_b32 v1, v2 offset:28672
	v_lshlrev_b32_e32 v0, 2, v0
	s_waitcnt lgkmcnt(0)
	global_store_dword v0, v1, s[0:1]

.Lw0b30:
	ds_read_b32 v12, v12 offset:32768
	v_lshlrev_b32_e32 v1, 17, v1
	s_mov_b32 s2, 0x3fe0000
	v_lshlrev_b32_e32 v8, 2, v8
	v_and_or_b32 v1, v1, s2, v25
	s_waitcnt lgkmcnt(0)
	v_lshl_add_u32 v8, v12, 2, v8
	ds_write_b32 v8, v1
	s_or_b64 exec, exec, s[16:17]
	s_and_saveexec_b64 s[2:3], s[4:5]
	s_cbranch_execz .LBB0_99

.LBB0_128:
	v_and_b32_e32 v1, 0x1fffffc, v31
.Lw0t33:
	s_cbranch_execz .Lw0c33
.Lw0b33:
	ds_read_b32 v1, v1 offset:32768
	v_lshlrev_b32_e32 v4, 17, v24
	s_mov_b32 s4, 0x3fe0000
	v_lshlrev_b32_e32 v5, 2, v29
	v_and_or_b32 v4, v4, s4, v6
	s_waitcnt lgkmcnt(0)
	v_lshl_add_u32 v1, v1, 2, v5
	ds_write_b32 v1, v4
	s_or_b64 exec, exec, s[2:3]
	s_and_saveexec_b64 s[2:3], s[14:15]
	s_cbranch_execnz .LBB0_104
	s_branch .LBB0_105
.Lmy_cvt0:
	s_waitcnt lgkmcnt(0)
	s_load_dwordx4 s[20:23], s[0:1], 0x50
	s_sub_i32 s3, s2, 207
	v_and_b32_e32 v1, 0x3c0, v0
	v_and_b32_e32 v2, 63, v0
	v_lshlrev_b32_e32 v3, 5, v1
	v_lshl_or_b32 v3, v2, 4, v3
	v_and_b32_e32 v4, 1, v0
	v_lshrrev_b32_e32 v5, 1, v2
	v_lshl_or_b32 v5, v4, 5, v5

.Lw0b34:
	v_add_u32_e32 v5, v5, v1
	v_lshlrev_b32_e32 v5, 4, v5
	v_cmp_eq_u32_e32 vcc, 0, v4
	s_waitcnt lgkmcnt(0)
	s_add_i32 s8, s3, 0
	s_lshl_b32 s9, s8, 10
	s_sub_i32 s9, 0x1869c0, s9
	v_cmp_ge_i32_e64 s[24:25], s9, v1
	s_add_i32 s8, s3, 0
	s_lshl_b32 s9, s8, 15
	s_add_u32 s10, s20, s9
	s_addc_u32 s11, s21, 0
	s_mov_b64 exec, s[24:25]
	global_load_dwordx4 v[8:11], v3, s[10:11] nt
	global_load_dwordx4 v[12:15], v3, s[10:11] offset:1024 nt
	s_waitcnt vmcnt(0)
	s_add_i32 s8, s3, 0
	s_lshl_b32 s9, s8, 14
	s_add_u32 s10, s22, s9
	s_addc_u32 s11, s23, 0
	s_mov_b64 exec, s[24:25]
	v_cvt_pk_f16_f32 v8, v8, v9
	v_cvt_pk_f16_f32 v9, v10, v11
	v_cvt_pk_f16_f32 v10, v12, v13

.Lw0b35:
	v_cvt_pk_f16_f32 v11, v14, v15
	v_cndmask_b32_e32 v12, v8, v10, vcc
	v_cndmask_b32_e32 v13, v9, v11, vcc
	s_nop 1
	v_mov_b32_dpp v12, v12 quad_perm:[1,0,3,2] row_mask:0xf bank_mask:0xf bound_ctrl:1
	v_mov_b32_dpp v13, v13 quad_perm:[1,0,3,2] row_mask:0xf bank_mask:0xf bound_ctrl:1
	v_cndmask_b32_e32 v8, v12, v8, vcc
	v_cndmask_b32_e32 v9, v13, v9, vcc
	v_cndmask_b32_e32 v10, v10, v12, vcc
	v_cndmask_b32_e32 v11, v11, v13, vcc
	global_store_dwordx4 v5, v[8:11], s[10:11] sc1

.Lw1b1:
	v_sub_co_u32_e32 v1, vcc, s2, v1
	s_and_b64 s[4:5], vcc, exec
	v_readfirstlane_b32 s3, v1
	s_cselect_b32 s33, s2, s3
	s_cmpk_gt_u32 s2, 0xc3
	s_cselect_b64 s[30:31], -1, 0
	s_and_b64 s[4:5], s[30:31], exec
	s_cselect_b32 s3, 0xc4, 0
	s_add_i32 s3, s3, s33
	s_movk_i32 s6, 0x62
	s_mul_hi_u32 s5, s3, 0x62
	s_mul_i32 s4, s3, 0x62
	v_cmp_gt_u32_e32 vcc, s6, v0
	v_mov_b32_e32 v1, 0
	v_mov_b32_e32 v2, 0
	s_and_saveexec_b64 s[6:7], vcc
	s_cbranch_execz .LBB1_3
	s_load_dwordx2 s[8:9], s[0:1], 0x0
	s_lshl_b64 s[10:11], s[4:5], 2
	v_lshlrev_b32_e32 v2, 2, v0
	s_waitcnt lgkmcnt(0)
	s_add_u32 s8, s8, s10
	s_addc_u32 s9, s9, s11
	global_load_dword v2, v2, s[8:9]

.Lw1b2:
	v_mov_b32_e32 v3, 0
	s_and_saveexec_b64 s[6:7], vcc
	s_cbranch_execz .LBB1_5
	s_load_dwordx2 s[8:9], s[0:1], 0x8
	s_lshl_b64 s[4:5], s[4:5], 2
	v_lshlrev_b32_e32 v4, 2, v0
	s_waitcnt lgkmcnt(0)
	s_add_u32 s4, s8, s4
	s_addc_u32 s5, s9, s5
	global_load_dword v3, v4, s[4:5]
	v_add_u32_e32 v4, 0x11990, v4
	s_waitcnt vmcnt(0)
	ds_write_b32 v4, v3
.LBB1_5:
	s_or_b64 exec, exec, s[6:7]
	v_add_u32_dpp v3, v3, v3 row_shr:1 row_mask:0xf bank_mask:0xf bound_ctrl:1
	v_and_b32_e32 v5, 63, v0
	v_cmp_eq_u32_e64 s[4:5], 63, v5
	v_add_u32_dpp v3, v3, v3 row_shr:2 row_mask:0xf bank_mask:0xf bound_ctrl:1
	s_nop 1
	v_add_u32_dpp v3, v3, v3 row_shr:4 row_mask:0xf bank_mask:0xf bound_ctrl:1
	s_nop 1
	v_add_u32_dpp v4, v3, v3 row_shr:8 row_mask:0xf bank_mask:0xf bound_ctrl:1

.Lw1b3:
	s_waitcnt vmcnt(0)
	v_add_u32_dpp v3, v2, v2 row_shr:1 row_mask:0xf bank_mask:0xf bound_ctrl:1
	v_add_u32_dpp v4, v4, v4 row_bcast:15 row_mask:0xa bank_mask:0xf
	s_nop 0
	v_add_u32_dpp v3, v3, v3 row_shr:2 row_mask:0xf bank_mask:0xf bound_ctrl:1
	v_mov_b32_dpp v1, v4 row_bcast:31 row_mask:0xc bank_mask:0xf
	s_nop 0
	v_add_u32_dpp v3, v3, v3 row_shr:4 row_mask:0xf bank_mask:0xf bound_ctrl:1
	s_nop 1
	v_add_u32_dpp v3, v3, v3 row_shr:8 row_mask:0xf bank_mask:0xf bound_ctrl:1
	s_nop 1
	v_add_u32_dpp v3, v3, v3 row_bcast:15 row_mask:0xa bank_mask:0xf
	s_nop 1
	v_add_u32_dpp v3, v3, v3 row_bcast:31 row_mask:0xc bank_mask:0xf
	s_and_saveexec_b64 s[6:7], s[4:5]
	s_cbranch_execz .LBB1_7
	v_lshrrev_b32_e32 v5, 4, v0
	v_and_b32_e32 v5, 60, v5
	v_add_u32_e32 v6, 0x11b20, v5
	v_add_u32_e32 v5, 0x11b60, v5
	v_add_u32_e32 v1, v4, v1

.Lw1b4:
	ds_write_b32 v5, v3
	ds_write_b32 v6, v1

.LBB1_9:
	s_or_b64 exec, exec, s[6:7]
	v_mov_b32_e32 v1, 0x11b20
	s_waitcnt lgkmcnt(0)
	s_barrier
	ds_read_b128 v[4:7], v1
	v_mov_b32_e32 v1, 0x11b30
	ds_read_b128 v[8:11], v1

.Lw1b5:
	v_mov_b32_e32 v1, 0x11b40
	s_movk_i32 s3, 0x7f
	s_waitcnt lgkmcnt(1)
	v_readfirstlane_b32 s40, v4
	v_readfirstlane_b32 s41, v5
	v_readfirstlane_b32 s42, v6
	v_readfirstlane_b32 s43, v7
	ds_read_b128 v[4:7], v1
	v_mov_b32_e32 v1, 0x11b50
	s_waitcnt lgkmcnt(1)
	v_readfirstlane_b32 s44, v8
	v_readfirstlane_b32 s45, v9
	v_readfirstlane_b32 s46, v10
	v_readfirstlane_b32 s47, v11
	ds_read_b128 v[8:11], v1
	v_mov_b32_e32 v1, 0x11b60
	s_waitcnt lgkmcnt(1)
	v_readfirstlane_b32 s48, v4
	v_readfirstlane_b32 s49, v5
	v_readfirstlane_b32 s50, v6
	v_readfirstlane_b32 s51, v7
	s_waitcnt lgkmcnt(0)
	v_readfirstlane_b32 s52, v8
	ds_read_b128 v[4:7], v1
	v_mov_b32_e32 v8, 0x11b70

.Lw1b6:
	v_readfirstlane_b32 s53, v9
	v_readfirstlane_b32 s54, v10
	v_readfirstlane_b32 s55, v11
	ds_read_b128 v[8:11], v8
	v_cmp_lt_u32_e64 s[8:9], s3, v0
	s_movk_i32 s3, 0xbf
	v_cmp_lt_u32_e64 s[10:11], s3, v0
	s_movk_i32 s3, 0xff
	v_cmp_lt_u32_e64 s[12:13], s3, v0
	s_movk_i32 s3, 0x13f
	v_cmp_gt_u32_e64 s[6:7], 64, v0
	v_cmp_lt_u32_e64 s[14:15], s3, v0
	s_movk_i32 s3, 0x17f
	s_waitcnt lgkmcnt(1)
	v_cndmask_b32_e64 v4, v4, 0, s[6:7]
	v_cndmask_b32_e64 v5, 0, v5, s[8:9]
	v_cndmask_b32_e64 v6, 0, v6, s[10:11]
	v_cmp_lt_u32_e64 s[16:17], s3, v0
	s_movk_i32 s3, 0x1bf
	v_add3_u32 v4, v5, v4, v6

.Lw1b7:
	v_cndmask_b32_e64 v5, 0, v7, s[12:13]
	s_waitcnt lgkmcnt(0)
	v_cndmask_b32_e64 v6, 0, v8, s[14:15]
	v_cmp_lt_u32_e64 s[18:19], s3, v0
	v_add3_u32 v4, v5, v4, v6
	v_cndmask_b32_e64 v5, 0, v9, s[16:17]
	v_cndmask_b32_e64 v6, 0, v10, s[18:19]
	v_add3_u32 v12, v5, v4, v6
	v_mov_b32_e32 v4, 0x11b80
	ds_read_b128 v[4:7], v4
	s_movk_i32 s3, 0x1ff
	v_cmp_lt_u32_e64 s[20:21], s3, v0
	s_movk_i32 s3, 0x23f
	v_mov_b32_e32 v8, 0x11b90
	v_cndmask_b32_e64 v11, 0, v11, s[20:21]
	ds_read_b96 v[8:10], v8
	v_cmp_lt_u32_e64 s[20:21], s3, v0

.Lw1b8:
	s_movk_i32 s3, 0x27f
	s_load_dwordx2 s[24:25], s[0:1], 0x10
	s_waitcnt lgkmcnt(0)
	v_cndmask_b32_e64 v4, 0, v4, s[20:21]
	v_cmp_lt_u32_e64 s[20:21], s3, v0
	s_movk_i32 s3, 0x2bf
	v_add3_u32 v4, v11, v12, v4
	v_cndmask_b32_e64 v5, 0, v5, s[20:21]
	v_cmp_lt_u32_e64 s[20:21], s3, v0
	s_movk_i32 s3, 0x2ff
	v_lshrrev_b32_e32 v1, 6, v0
	v_cndmask_b32_e64 v6, 0, v6, s[20:21]
	v_cmp_lt_u32_e64 s[20:21], s3, v0
	s_movk_i32 s3, 0x33f
	v_add3_u32 v4, v5, v4, v6
	v_cndmask_b32_e64 v5, 0, v7, s[20:21]
	v_cmp_lt_u32_e64 s[20:21], s3, v0
	s_movk_i32 s3, 0x37f
	s_nop 0

.Lw1b9:
	v_cndmask_b32_e64 v6, 0, v8, s[20:21]
	v_cmp_lt_u32_e64 s[20:21], s3, v0
	v_add3_u32 v4, v5, v4, v6
	s_nop 0
	v_cndmask_b32_e64 v5, 0, v9, s[20:21]
	v_cmp_eq_u32_e64 s[20:21], 15, v1
	s_nop 1
	v_cndmask_b32_e64 v6, 0, v10, s[20:21]
	v_add3_u32 v4, v5, v4, v6
	s_and_saveexec_b64 s[26:27], vcc
	v_mov_b32_e32 v5, 0x11800
	v_sub_u32_e32 v2, v3, v2
	v_lshl_add_u32 v5, v0, 2, v5
	v_add_u32_e32 v2, v2, v4
	ds_write_b32 v5, v2
	s_or_b64 exec, exec, s[26:27]
	s_movk_i32 s3, 0x61
	v_cmp_eq_u32_e32 vcc, s3, v0
	s_and_saveexec_b64 s[26:27], vcc
	v_add_u32_e32 v2, v4, v3
	v_mov_b32_e32 v3, 0x11988

.Lw1b10:
	ds_write_b32 v3, v2
	s_or_b64 exec, exec, s[26:27]
	v_mov_b32_e32 v2, 0x11988
	s_waitcnt lgkmcnt(0)
	s_barrier
	ds_read_b32 v2, v2
	v_mov_b32_e32 v3, 0x11900
	s_and_b64 s[26:27], s[30:31], exec
	ds_read_b32 v5, v3
	s_cselect_b32 s26, 0xc3500, 0
	s_lshl_b32 s56, s26, 2
	s_add_u32 s28, s24, s56
	s_movk_i32 s24, 0x2001
	s_waitcnt lgkmcnt(1)
	v_cmp_gt_i32_e32 vcc, s24, v2
	v_readfirstlane_b32 s3, v2
	s_addc_u32 s29, s25, 0
	s_mov_b64 s[34:35], -1
	s_cbranch_vccnz .LBB1_37
	s_mov_b64 s[24:25], 0
	v_mov_b32_e32 v3, 0x11880
	s_movk_i32 s36, 0x51
	s_movk_i32 s37, 0x52

.Lw1b11:
	s_movk_i32 s38, 0x59
	s_movk_i32 s39, 0x5a
	s_movk_i32 s57, 0x5d
	s_movk_i32 s58, 0x5e
	s_movk_i32 s59, 0x5f
	s_movk_i32 s60, 0x60
	s_movk_i32 s61, 0x61
	v_mov_b32_e32 v4, 0x11990
	v_mov_b32_e32 v6, 1
	v_mov_b32_e32 v7, 0x11840
	v_mov_b32_e32 v8, 0x11820
	v_mov_b32_e32 v9, 0x11810
	v_mov_b32_e32 v10, 0x11808
	v_mov_b32_e32 v11, 0x11804
	v_mov_b32_e32 v12, 0x11800
	v_mov_b32_e32 v13, v0
	s_branch .LBB1_16
.LBB1_15:
	s_or_b64 exec, exec, s[34:35]
	v_lshl_add_u32 v14, v16, 2, v4
	ds_read_b32 v14, v14
	s_waitcnt lgkmcnt(0)
	v_lshl_add_u32 v14, v16, 13, v14
.Lw1t12:
	s_cbranch_execz .Lw1c12
.Lw1b12:
	v_sub_u32_e32 v14, v14, v15
	v_add_u32_e32 v14, v13, v14
	v_ashrrev_i32_e32 v15, 31, v14
	v_lshl_add_u64 v[14:15], v[14:15], 2, s[28:29]
	global_load_dword v14, v[14:15], off
	v_add_u32_e32 v13, 0x400, v13
	v_cmp_le_i32_e32 vcc, s3, v13
	s_or_b64 s[24:25], vcc, s[24:25]
	s_waitcnt vmcnt(0)
	v_lshrrev_b32_e32 v14, 15, v14
	v_and_b32_e32 v14, 0x1fffc, v14
	v_add_u32_e32 v14, 0x10000, v14
	ds_add_u32 v14, v6
	s_andn2_b64 exec, exec, s[24:25]
	s_cbranch_execz .LBB1_36
.LBB1_16:
	s_waitcnt lgkmcnt(0)
	v_cmp_gt_i32_e32 vcc, v5, v13
	s_nop 1
	v_cndmask_b32_e64 v14, 64, 0, vcc
	v_lshl_or_b32 v15, v14, 2, v3
	ds_read_b32 v15, v15
.Lw1t13:
	s_cbranch_execz .Lw1c13
.Lw1b13:
	v_or_b32_e32 v16, 32, v14
	s_waitcnt lgkmcnt(0)
	v_cmp_gt_i32_e32 vcc, v15, v13
	s_nop 1
	v_cndmask_b32_e32 v15, v16, v14, vcc
	v_cmp_lt_u32_e64 s[26:27], s36, v15
	v_cmp_gt_u32_e32 vcc, s37, v15
	s_and_saveexec_b64 s[34:35], vcc
	s_cbranch_execz .LBB1_18
	v_lshl_add_u32 v14, v15, 2, v7
	ds_read_b32 v16, v14
	s_andn2_b64 s[26:27], s[26:27], exec
	v_or_b32_e32 v14, 16, v15
	s_waitcnt lgkmcnt(0)
	v_cmp_gt_i32_e32 vcc, v16, v13
	s_and_b64 s[62:63], vcc, exec
	s_or_b64 s[26:27], s[26:27], s[62:63]
.LBB1_18:
	s_or_b64 exec, exec, s[34:35]
	s_and_saveexec_b64 s[34:35], s[26:27]
	v_mov_b32_e32 v14, v15
	s_or_b64 exec, exec, s[34:35]
	v_cmp_lt_u32_e64 s[26:27], s38, v14
	v_cmp_gt_u32_e32 vcc, s39, v14
	s_and_saveexec_b64 s[34:35], vcc
	s_cbranch_execz .LBB1_22
	v_lshl_add_u32 v15, v14, 2, v8
.Lw1t14:
	s_cbranch_execz .Lw1c14
.Lw1b14:
	ds_read_b32 v16, v15
	s_andn2_b64 s[26:27], s[26:27], exec
	v_add_u32_e32 v15, 8, v14
	s_waitcnt lgkmcnt(0)
	v_cmp_gt_i32_e32 vcc, v16, v13
	s_and_b64 s[62:63], vcc, exec
	s_or_b64 s[26:27], s[26:27], s[62:63]

.LBB1_26:
	s_or_b64 exec, exec, s[34:35]
	s_and_saveexec_b64 s[34:35], s[26:27]
	v_mov_b32_e32 v16, v15
	s_or_b64 exec, exec, s[34:35]
.Lw1t15:
	s_cbranch_execz .Lw1c15
.Lw1b15:
	v_cmp_lt_u32_e64 s[26:27], s59, v16
	v_cmp_gt_u32_e32 vcc, s60, v16
	s_and_saveexec_b64 s[34:35], vcc
	s_cbranch_execz .LBB1_30
	v_lshl_add_u32 v14, v16, 2, v10
	ds_read_b32 v15, v14
	s_andn2_b64 s[26:27], s[26:27], exec
	v_add_u32_e32 v14, 2, v16
	s_waitcnt lgkmcnt(0)
	v_cmp_gt_i32_e32 vcc, v15, v13
	s_and_b64 s[62:63], vcc, exec
	s_or_b64 s[26:27], s[26:27], s[62:63]
.LBB1_30:
	s_or_b64 exec, exec, s[34:35]
	s_and_saveexec_b64 s[34:35], s[26:27]
	v_mov_b32_e32 v14, v16
	s_or_b64 exec, exec, s[34:35]
	v_cmp_lt_u32_e64 s[26:27], s60, v14
	v_cmp_gt_u32_e32 vcc, s61, v14
	s_and_saveexec_b64 s[34:35], vcc
	s_cbranch_execz .LBB1_34
	v_lshl_add_u32 v15, v14, 2, v11
	ds_read_b32 v15, v15
	s_andn2_b64 s[26:27], s[26:27], exec
	v_add_u32_e32 v16, 1, v14
	s_waitcnt lgkmcnt(0)

.LBB1_37:
	s_load_dwordx4 s[24:27], s[0:1], 0x18
	s_movk_i32 s57, 0x2000
	s_and_b64 vcc, exec, s[34:35]
	s_cbranch_vccz .LBB1_231
	s_waitcnt lgkmcnt(0)
	s_load_dwordx4 s[68:71], s[0:1], 0x28
	s_and_b64 s[36:37], s[30:31], exec
	s_cselect_b32 s72, 0xc4, 0
	s_add_i32 s72, s72, s33
	s_addk_i32 s72, 0x190
	v_and_b32_e32 v48, 0x3c0, v0
	v_and_b32_e32 v49, 63, v0
	v_lshlrev_b32_e32 v58, 5, v48

.Lw1b17:
	v_lshl_or_b32 v58, v49, 4, v58
	v_and_b32_e32 v59, 1, v0
	v_lshrrev_b32_e32 v49, 1, v49
	v_lshl_or_b32 v49, v59, 5, v49
	v_add_u32_e32 v49, v49, v48
	v_lshlrev_b32_e32 v49, 4, v49
	s_lshl_b32 s73, s72, 15
	s_waitcnt lgkmcnt(0)
	s_add_u32 s68, s68, s73
	s_addc_u32 s69, s69, 0
	s_mov_b32 s34, 0x11800
	s_movk_i32 s35, 0x62
	v_mov_b32_e32 v32, v0
	v_add_u32_e32 v33, 1024, v0
	v_add_u32_e32 v34, 2048, v0
	v_add_u32_e32 v35, 3072, v0
	v_add_u32_e32 v36, 4096, v0
	v_add_u32_e32 v37, 5120, v0
	v_add_u32_e32 v38, 6144, v0
	v_add_u32_e32 v39, 7168, v0
	v_cmp_le_i32_e64 s[36:37], v5, v32

.Lw1b18:
	v_cmp_le_i32_e64 s[38:39], v5, v33
	v_cmp_le_i32_e64 s[58:59], v5, v34
	v_cmp_le_i32_e64 s[60:61], v5, v35
	v_cndmask_b32_e64 v40, 0, 64, s[36:37]
	v_cndmask_b32_e64 v41, 0, 64, s[38:39]
	v_cndmask_b32_e64 v42, 0, 64, s[58:59]
	v_cndmask_b32_e64 v43, 0, 64, s[60:61]
	v_cmp_le_i32_e64 s[36:37], v5, v36
	v_cmp_le_i32_e64 s[38:39], v5, v37
	v_cmp_le_i32_e64 s[58:59], v5, v38
	v_cmp_le_i32_e64 s[60:61], v5, v39
	v_cndmask_b32_e64 v44, 0, 64, s[36:37]
	v_cndmask_b32_e64 v45, 0, 64, s[38:39]
	v_cndmask_b32_e64 v46, 0, 64, s[58:59]
	v_cndmask_b32_e64 v47, 0, 64, s[60:61]

.Lw1b19:
	v_add_u32_e32 v3, 32, v40
	v_lshl_add_u32 v11, v3, 2, s34
	ds_read_b32 v11, v11
	v_add_u32_e32 v4, 32, v41
	v_lshl_add_u32 v12, v4, 2, s34
	ds_read_b32 v12, v12
	v_add_u32_e32 v6, 32, v42
	v_lshl_add_u32 v13, v6, 2, s34
	ds_read_b32 v13, v13
	v_add_u32_e32 v7, 32, v43
	v_lshl_add_u32 v14, v7, 2, s34
	ds_read_b32 v14, v14
	v_add_u32_e32 v8, 32, v44
	v_lshl_add_u32 v15, v8, 2, s34
	ds_read_b32 v15, v15
	v_add_u32_e32 v9, 32, v45
	v_lshl_add_u32 v16, v9, 2, s34
	ds_read_b32 v16, v16
	v_add_u32_e32 v10, 32, v46

.Lw1b20:
	v_lshl_add_u32 v17, v10, 2, s34
	ds_read_b32 v17, v17
	v_add_u32_e32 v19, 32, v47
	v_lshl_add_u32 v18, v19, 2, s34
	ds_read_b32 v18, v18
	s_waitcnt lgkmcnt(7)
	v_cmp_le_i32_e64 s[36:37], v11, v32
	s_waitcnt lgkmcnt(6)
	v_cmp_le_i32_e64 s[38:39], v12, v33
	s_waitcnt lgkmcnt(5)
	v_cmp_le_i32_e64 s[58:59], v13, v34
	s_waitcnt lgkmcnt(4)
	v_cmp_le_i32_e64 s[60:61], v14, v35
	v_cndmask_b32_e64 v40, v40, v3, s[36:37]
	v_cndmask_b32_e64 v41, v41, v4, s[38:39]
	v_cndmask_b32_e64 v42, v42, v6, s[58:59]
	v_cndmask_b32_e64 v43, v43, v7, s[60:61]
	s_waitcnt lgkmcnt(3)
	v_cmp_le_i32_e64 s[36:37], v15, v36

.Lw1b21:
	s_waitcnt lgkmcnt(2)
	v_cmp_le_i32_e64 s[38:39], v16, v37
	s_waitcnt lgkmcnt(1)
	v_cmp_le_i32_e64 s[58:59], v17, v38
	s_waitcnt lgkmcnt(0)
	v_cmp_le_i32_e64 s[60:61], v18, v39
	v_cndmask_b32_e64 v44, v44, v8, s[36:37]
	v_cndmask_b32_e64 v45, v45, v9, s[38:39]
	v_cndmask_b32_e64 v46, v46, v10, s[58:59]
	v_cndmask_b32_e64 v47, v47, v19, s[60:61]
	v_add_u32_e32 v3, 16, v40
	v_min_u32_e32 v11, s35, v3
	v_lshl_add_u32 v11, v11, 2, s34
	ds_read_b32 v11, v11
	v_add_u32_e32 v4, 16, v41
	v_min_u32_e32 v12, s35, v4
	v_lshl_add_u32 v12, v12, 2, s34
	ds_read_b32 v12, v12
	v_add_u32_e32 v6, 16, v42

.Lw1b22:
	v_min_u32_e32 v13, s35, v6
	v_lshl_add_u32 v13, v13, 2, s34
	ds_read_b32 v13, v13
	v_add_u32_e32 v7, 16, v43
	v_min_u32_e32 v14, s35, v7
	v_lshl_add_u32 v14, v14, 2, s34
	ds_read_b32 v14, v14
	v_add_u32_e32 v8, 16, v44
	v_min_u32_e32 v15, s35, v8
	v_lshl_add_u32 v15, v15, 2, s34
	ds_read_b32 v15, v15
	v_add_u32_e32 v9, 16, v45
	v_min_u32_e32 v16, s35, v9
	v_lshl_add_u32 v16, v16, 2, s34
	ds_read_b32 v16, v16
	v_add_u32_e32 v10, 16, v46
	v_min_u32_e32 v17, s35, v10
	v_lshl_add_u32 v17, v17, 2, s34
	ds_read_b32 v17, v17
	v_add_u32_e32 v19, 16, v47
	v_min_u32_e32 v18, s35, v19

.Lw1b23:
	v_lshl_add_u32 v18, v18, 2, s34
	ds_read_b32 v18, v18
	s_waitcnt lgkmcnt(7)
	v_cmp_le_i32_e64 s[36:37], v11, v32
	s_waitcnt lgkmcnt(6)
	v_cmp_le_i32_e64 s[38:39], v12, v33
	s_waitcnt lgkmcnt(5)
	v_cmp_le_i32_e64 s[58:59], v13, v34
	s_waitcnt lgkmcnt(4)
	v_cmp_le_i32_e64 s[60:61], v14, v35
	v_cndmask_b32_e64 v40, v40, v3, s[36:37]
	v_cndmask_b32_e64 v41, v41, v4, s[38:39]
	v_cndmask_b32_e64 v42, v42, v6, s[58:59]
	v_cndmask_b32_e64 v43, v43, v7, s[60:61]
	s_waitcnt lgkmcnt(3)
	v_cmp_le_i32_e64 s[36:37], v15, v36
	s_waitcnt lgkmcnt(2)
	v_cmp_le_i32_e64 s[38:39], v16, v37
	s_waitcnt lgkmcnt(1)

.Lw1b24:
	v_cmp_le_i32_e64 s[58:59], v17, v38
	s_waitcnt lgkmcnt(0)
	v_cmp_le_i32_e64 s[60:61], v18, v39
	v_cndmask_b32_e64 v44, v44, v8, s[36:37]
	v_cndmask_b32_e64 v45, v45, v9, s[38:39]
	v_cndmask_b32_e64 v46, v46, v10, s[58:59]
	v_cndmask_b32_e64 v47, v47, v19, s[60:61]
	v_add_u32_e32 v3, 8, v40
	v_min_u32_e32 v11, s35, v3
	v_lshl_add_u32 v11, v11, 2, s34
	ds_read_b32 v11, v11
	v_add_u32_e32 v4, 8, v41
	v_min_u32_e32 v12, s35, v4
	v_lshl_add_u32 v12, v12, 2, s34
	ds_read_b32 v12, v12
	v_add_u32_e32 v6, 8, v42
	v_min_u32_e32 v13, s35, v6
	v_lshl_add_u32 v13, v13, 2, s34
	ds_read_b32 v13, v13

.Lw1b25:
	v_add_u32_e32 v7, 8, v43
	v_min_u32_e32 v14, s35, v7
	v_lshl_add_u32 v14, v14, 2, s34
	ds_read_b32 v14, v14
	v_add_u32_e32 v8, 8, v44
	v_min_u32_e32 v15, s35, v8
	v_lshl_add_u32 v15, v15, 2, s34
	ds_read_b32 v15, v15
	v_add_u32_e32 v9, 8, v45
	v_min_u32_e32 v16, s35, v9
	v_lshl_add_u32 v16, v16, 2, s34
	ds_read_b32 v16, v16
	v_add_u32_e32 v10, 8, v46
	v_min_u32_e32 v17, s35, v10
	v_lshl_add_u32 v17, v17, 2, s34
	ds_read_b32 v17, v17
	v_add_u32_e32 v19, 8, v47
	v_min_u32_e32 v18, s35, v19
	v_lshl_add_u32 v18, v18, 2, s34
	ds_read_b32 v18, v18
	s_waitcnt lgkmcnt(7)

.Lw1b26:
	v_cmp_le_i32_e64 s[36:37], v11, v32
	s_waitcnt lgkmcnt(6)
	v_cmp_le_i32_e64 s[38:39], v12, v33
	s_waitcnt lgkmcnt(5)
	v_cmp_le_i32_e64 s[58:59], v13, v34
	s_waitcnt lgkmcnt(4)
	v_cmp_le_i32_e64 s[60:61], v14, v35
	v_cndmask_b32_e64 v40, v40, v3, s[36:37]
	v_cndmask_b32_e64 v41, v41, v4, s[38:39]
	v_cndmask_b32_e64 v42, v42, v6, s[58:59]
	v_cndmask_b32_e64 v43, v43, v7, s[60:61]
	s_waitcnt lgkmcnt(3)
	v_cmp_le_i32_e64 s[36:37], v15, v36
	s_waitcnt lgkmcnt(2)
	v_cmp_le_i32_e64 s[38:39], v16, v37
	s_waitcnt lgkmcnt(1)
	v_cmp_le_i32_e64 s[58:59], v17, v38
	s_waitcnt lgkmcnt(0)
	v_cmp_le_i32_e64 s[60:61], v18, v39

.Lw1b27:
	v_cndmask_b32_e64 v44, v44, v8, s[36:37]
	v_cndmask_b32_e64 v45, v45, v9, s[38:39]
	v_cndmask_b32_e64 v46, v46, v10, s[58:59]
	v_cndmask_b32_e64 v47, v47, v19, s[60:61]
	v_add_u32_e32 v3, 4, v40
	v_min_u32_e32 v11, s35, v3
	v_lshl_add_u32 v11, v11, 2, s34
	ds_read_b32 v11, v11
	v_add_u32_e32 v4, 4, v41
	v_min_u32_e32 v12, s35, v4
	v_lshl_add_u32 v12, v12, 2, s34
	ds_read_b32 v12, v12
	v_add_u32_e32 v6, 4, v42
	v_min_u32_e32 v13, s35, v6
	v_lshl_add_u32 v13, v13, 2, s34
	ds_read_b32 v13, v13
	v_add_u32_e32 v7, 4, v43
	v_min_u32_e32 v14, s35, v7
	v_lshl_add_u32 v14, v14, 2, s34
	ds_read_b32 v14, v14

.Lw1b28:
	v_add_u32_e32 v8, 4, v44
	v_min_u32_e32 v15, s35, v8
	v_lshl_add_u32 v15, v15, 2, s34
	ds_read_b32 v15, v15
	v_add_u32_e32 v9, 4, v45
	v_min_u32_e32 v16, s35, v9
	v_lshl_add_u32 v16, v16, 2, s34
	ds_read_b32 v16, v16
	v_add_u32_e32 v10, 4, v46
	v_min_u32_e32 v17, s35, v10
	v_lshl_add_u32 v17, v17, 2, s34
	ds_read_b32 v17, v17
	v_add_u32_e32 v19, 4, v47
	v_min_u32_e32 v18, s35, v19
	v_lshl_add_u32 v18, v18, 2, s34
	ds_read_b32 v18, v18
	s_waitcnt lgkmcnt(7)
	v_cmp_le_i32_e64 s[36:37], v11, v32
	s_waitcnt lgkmcnt(6)
	v_cmp_le_i32_e64 s[38:39], v12, v33

.Lw1b29:
	s_waitcnt lgkmcnt(5)
	v_cmp_le_i32_e64 s[58:59], v13, v34
	s_waitcnt lgkmcnt(4)
	v_cmp_le_i32_e64 s[60:61], v14, v35
	v_cndmask_b32_e64 v40, v40, v3, s[36:37]
	v_cndmask_b32_e64 v41, v41, v4, s[38:39]
	v_cndmask_b32_e64 v42, v42, v6, s[58:59]
	v_cndmask_b32_e64 v43, v43, v7, s[60:61]
	s_waitcnt lgkmcnt(3)
	v_cmp_le_i32_e64 s[36:37], v15, v36
	s_waitcnt lgkmcnt(2)
	v_cmp_le_i32_e64 s[38:39], v16, v37
	s_waitcnt lgkmcnt(1)
	v_cmp_le_i32_e64 s[58:59], v17, v38
	s_waitcnt lgkmcnt(0)
	v_cmp_le_i32_e64 s[60:61], v18, v39
	v_cndmask_b32_e64 v44, v44, v8, s[36:37]
	v_cndmask_b32_e64 v45, v45, v9, s[38:39]
	v_cndmask_b32_e64 v46, v46, v10, s[58:59]

.Lw1b30:
	v_cndmask_b32_e64 v47, v47, v19, s[60:61]
	v_add_u32_e32 v3, 2, v40
	v_min_u32_e32 v11, s35, v3
	v_lshl_add_u32 v11, v11, 2, s34
	ds_read_b32 v11, v11
	v_add_u32_e32 v4, 2, v41
	v_min_u32_e32 v12, s35, v4
	v_lshl_add_u32 v12, v12, 2, s34
	ds_read_b32 v12, v12
	v_add_u32_e32 v6, 2, v42
	v_min_u32_e32 v13, s35, v6
	v_lshl_add_u32 v13, v13, 2, s34
	ds_read_b32 v13, v13
	v_add_u32_e32 v7, 2, v43
	v_min_u32_e32 v14, s35, v7
	v_lshl_add_u32 v14, v14, 2, s34
	ds_read_b32 v14, v14
	v_add_u32_e32 v8, 2, v44
	v_min_u32_e32 v15, s35, v8
	v_lshl_add_u32 v15, v15, 2, s34

.Lw1b31:
	ds_read_b32 v15, v15
	v_add_u32_e32 v9, 2, v45
	v_min_u32_e32 v16, s35, v9
	v_lshl_add_u32 v16, v16, 2, s34
	ds_read_b32 v16, v16
	v_add_u32_e32 v10, 2, v46
	v_min_u32_e32 v17, s35, v10
	v_lshl_add_u32 v17, v17, 2, s34
	ds_read_b32 v17, v17
	v_add_u32_e32 v19, 2, v47
	v_min_u32_e32 v18, s35, v19
	v_lshl_add_u32 v18, v18, 2, s34
	ds_read_b32 v18, v18
	s_waitcnt lgkmcnt(7)
	v_cmp_le_i32_e64 s[36:37], v11, v32
	s_waitcnt lgkmcnt(6)
	v_cmp_le_i32_e64 s[38:39], v12, v33
	s_waitcnt lgkmcnt(5)
	v_cmp_le_i32_e64 s[58:59], v13, v34
	s_waitcnt lgkmcnt(4)
	v_cmp_le_i32_e64 s[60:61], v14, v35

.Lw1b32:
	v_cndmask_b32_e64 v40, v40, v3, s[36:37]
	v_cndmask_b32_e64 v41, v41, v4, s[38:39]
	v_cndmask_b32_e64 v42, v42, v6, s[58:59]
	v_cndmask_b32_e64 v43, v43, v7, s[60:61]
	s_waitcnt lgkmcnt(3)
	v_cmp_le_i32_e64 s[36:37], v15, v36
	s_waitcnt lgkmcnt(2)
	v_cmp_le_i32_e64 s[38:39], v16, v37
	s_waitcnt lgkmcnt(1)
	v_cmp_le_i32_e64 s[58:59], v17, v38
	s_waitcnt lgkmcnt(0)
	v_cmp_le_i32_e64 s[60:61], v18, v39
	v_cndmask_b32_e64 v44, v44, v8, s[36:37]
	v_cndmask_b32_e64 v45, v45, v9, s[38:39]
	v_cndmask_b32_e64 v46, v46, v10, s[58:59]
	v_cndmask_b32_e64 v47, v47, v19, s[60:61]
	v_add_u32_e32 v3, 1, v40
	v_min_u32_e32 v11, s35, v3

.Lw1b33:
	v_lshl_add_u32 v11, v11, 2, s34
	ds_read_b32 v11, v11
	v_add_u32_e32 v4, 1, v41
	v_min_u32_e32 v12, s35, v4
	v_lshl_add_u32 v12, v12, 2, s34
	ds_read_b32 v12, v12
	v_add_u32_e32 v6, 1, v42
	v_min_u32_e32 v13, s35, v6
	v_lshl_add_u32 v13, v13, 2, s34
	ds_read_b32 v13, v13
	v_add_u32_e32 v7, 1, v43
	v_min_u32_e32 v14, s35, v7
	v_lshl_add_u32 v14, v14, 2, s34
	ds_read_b32 v14, v14
	v_add_u32_e32 v8, 1, v44
	v_min_u32_e32 v15, s35, v8
	v_lshl_add_u32 v15, v15, 2, s34
	ds_read_b32 v15, v15
	v_add_u32_e32 v9, 1, v45
	v_min_u32_e32 v16, s35, v9
	v_lshl_add_u32 v16, v16, 2, s34

.Lw1b34:
	ds_read_b32 v16, v16
	v_add_u32_e32 v10, 1, v46
	v_min_u32_e32 v17, s35, v10
	v_lshl_add_u32 v17, v17, 2, s34
	ds_read_b32 v17, v17
	v_add_u32_e32 v19, 1, v47
	v_min_u32_e32 v18, s35, v19
	v_lshl_add_u32 v18, v18, 2, s34
	ds_read_b32 v18, v18
	s_waitcnt lgkmcnt(7)
	v_cmp_le_i32_e64 s[36:37], v11, v32
	s_waitcnt lgkmcnt(6)
	v_cmp_le_i32_e64 s[38:39], v12, v33
	s_waitcnt lgkmcnt(5)
	v_cmp_le_i32_e64 s[58:59], v13, v34
	s_waitcnt lgkmcnt(4)
	v_cmp_le_i32_e64 s[60:61], v14, v35
	v_cndmask_b32_e64 v40, v40, v3, s[36:37]
	v_cndmask_b32_e64 v41, v41, v4, s[38:39]

.Lw1b35:
	v_cndmask_b32_e64 v42, v42, v6, s[58:59]
	v_cndmask_b32_e64 v43, v43, v7, s[60:61]
	s_waitcnt lgkmcnt(3)
	v_cmp_le_i32_e64 s[36:37], v15, v36
	s_waitcnt lgkmcnt(2)
	v_cmp_le_i32_e64 s[38:39], v16, v37
	s_waitcnt lgkmcnt(1)
	v_cmp_le_i32_e64 s[58:59], v17, v38
	s_waitcnt lgkmcnt(0)
	v_cmp_le_i32_e64 s[60:61], v18, v39
	v_cndmask_b32_e64 v44, v44, v8, s[36:37]
	v_cndmask_b32_e64 v45, v45, v9, s[38:39]
	v_cndmask_b32_e64 v46, v46, v10, s[58:59]
	v_cndmask_b32_e64 v47, v47, v19, s[60:61]
	v_lshl_add_u32 v11, v40, 2, s34
	ds_read_b32 v3, v11
	ds_read_b32 v11, v11 offset:400
	v_lshl_add_u32 v12, v41, 2, s34

.Lw1b36:
	ds_read_b32 v4, v12
	ds_read_b32 v12, v12 offset:400
	v_lshl_add_u32 v13, v42, 2, s34
	ds_read_b32 v6, v13
	ds_read_b32 v13, v13 offset:400
	v_lshl_add_u32 v14, v43, 2, s34
	ds_read_b32 v7, v14
	ds_read_b32 v14, v14 offset:400
	v_lshl_add_u32 v15, v44, 2, s34
	ds_read_b32 v8, v15
	ds_read_b32 v15, v15 offset:400
	v_lshl_add_u32 v16, v45, 2, s34
	ds_read_b32 v9, v16
	ds_read_b32 v16, v16 offset:400
	v_lshl_add_u32 v17, v46, 2, s34

.Lw1b37:
	ds_read_b32 v10, v17
	ds_read_b32 v17, v17 offset:400
	v_lshl_add_u32 v18, v47, 2, s34
	ds_read_b32 v19, v18
	ds_read_b32 v18, v18 offset:400
	s_waitcnt lgkmcnt(14)
	v_sub_u32_e32 v3, v32, v3
	v_lshl_add_u32 v40, v40, 13, v3
	v_add_lshl_u32 v40, v40, v11, 2
	s_waitcnt lgkmcnt(12)
	v_sub_u32_e32 v4, v33, v4
	v_lshl_add_u32 v41, v41, 13, v4
	v_add_lshl_u32 v41, v41, v12, 2
	s_waitcnt lgkmcnt(10)
	v_sub_u32_e32 v6, v34, v6
	v_lshl_add_u32 v42, v42, 13, v6
	v_add_lshl_u32 v42, v42, v13, 2
	s_waitcnt lgkmcnt(8)
	v_sub_u32_e32 v7, v35, v7
	v_lshl_add_u32 v43, v43, 13, v7

.Lw1b38:
	v_add_lshl_u32 v43, v43, v14, 2
	s_waitcnt lgkmcnt(6)
	v_sub_u32_e32 v8, v36, v8
	v_lshl_add_u32 v44, v44, 13, v8
	v_add_lshl_u32 v44, v44, v15, 2
	s_waitcnt lgkmcnt(4)
	v_sub_u32_e32 v9, v37, v9
	v_lshl_add_u32 v45, v45, 13, v9
	v_add_lshl_u32 v45, v45, v16, 2
	s_waitcnt lgkmcnt(2)
	v_sub_u32_e32 v10, v38, v10
	v_lshl_add_u32 v46, v46, 13, v10
	v_add_lshl_u32 v46, v46, v17, 2
	s_waitcnt lgkmcnt(0)
	v_sub_u32_e32 v19, v39, v19
	v_lshl_add_u32 v47, v47, 13, v19
	v_add_lshl_u32 v47, v47, v18, 2
	v_cmp_gt_i32_e64 s[36:37], s3, v32
	v_mov_b32_e32 v3, -1
	s_mov_b64 exec, s[36:37]

.Lw1b39:
	global_load_dword v3, v40, s[28:29]
	s_mov_b64 exec, -1
	v_cmp_gt_i32_e64 s[38:39], s3, v33
	v_mov_b32_e32 v4, -1
	s_mov_b64 exec, s[38:39]
	global_load_dword v4, v41, s[28:29]
	s_mov_b64 exec, -1
	v_cmp_gt_i32_e64 s[58:59], s3, v34
	v_mov_b32_e32 v6, -1
	s_mov_b64 exec, s[58:59]
	global_load_dword v6, v42, s[28:29]
	s_mov_b64 exec, -1
	v_cmp_gt_i32_e64 s[60:61], s3, v35
	v_mov_b32_e32 v7, -1
	s_mov_b64 exec, s[60:61]
	global_load_dword v7, v43, s[28:29]
	s_mov_b64 exec, -1
	v_cmp_gt_i32_e64 s[36:37], s3, v36
	v_mov_b32_e32 v8, -1
	s_mov_b64 exec, s[36:37]
	global_load_dword v8, v44, s[28:29]
	s_mov_b64 exec, -1

.Lw1b40:
	v_cmp_gt_i32_e64 s[38:39], s3, v37
	v_mov_b32_e32 v9, -1
	s_mov_b64 exec, s[38:39]
	global_load_dword v9, v45, s[28:29]
	s_mov_b64 exec, -1
	v_cmp_gt_i32_e64 s[58:59], s3, v38
	v_mov_b32_e32 v10, -1
	s_mov_b64 exec, s[58:59]
	global_load_dword v10, v46, s[28:29]
	s_mov_b64 exec, -1
	v_cmp_gt_i32_e64 s[60:61], s3, v39
	v_mov_b32_e32 v13, -1
	s_mov_b64 exec, s[60:61]
	global_load_dword v13, v47, s[28:29]
	s_mov_b64 exec, -1
	global_load_dwordx4 v[50:53], v58, s[68:69] nt
	global_load_dwordx4 v[54:57], v58, s[68:69] offset:1024 nt
	v_mov_b32_e32 v19, 1
	s_waitcnt vmcnt(9)
	v_cmp_ne_u32_e64 s[36:37], -1, v3
	v_lshrrev_b32_e32 v32, 15, v3
	v_and_b32_e32 v32, 0x1fffc, v32

.Lw1b41:
	v_add_u32_e32 v32, 0x10000, v32
	v_mov_b32_e32 v15, 0
	s_mov_b64 exec, s[36:37]
	ds_add_rtn_u32 v15, v32, v19
	s_mov_b64 exec, -1
	s_waitcnt vmcnt(8)
	v_cmp_ne_u32_e64 s[38:39], -1, v4
	v_lshrrev_b32_e32 v33, 15, v4
	v_and_b32_e32 v33, 0x1fffc, v33
	v_add_u32_e32 v33, 0x10000, v33
	v_mov_b32_e32 v5, 0
	s_mov_b64 exec, s[38:39]
	ds_add_rtn_u32 v5, v33, v19
	s_mov_b64 exec, -1
	s_waitcnt vmcnt(7)
	v_cmp_ne_u32_e64 s[58:59], -1, v6
	v_lshrrev_b32_e32 v34, 15, v6
	v_and_b32_e32 v34, 0x1fffc, v34
	v_add_u32_e32 v34, 0x10000, v34
	v_mov_b32_e32 v16, 0
	s_mov_b64 exec, s[58:59]

.Lw1b42:
	ds_add_rtn_u32 v16, v34, v19
	s_mov_b64 exec, -1
	s_waitcnt vmcnt(6)
	v_cmp_ne_u32_e64 s[60:61], -1, v7
	v_lshrrev_b32_e32 v35, 15, v7
	v_and_b32_e32 v35, 0x1fffc, v35
	v_add_u32_e32 v35, 0x10000, v35
	v_mov_b32_e32 v11, 0
	s_mov_b64 exec, s[60:61]
	ds_add_rtn_u32 v11, v35, v19
	s_mov_b64 exec, -1
	s_waitcnt vmcnt(5)
	v_cmp_ne_u32_e64 s[36:37], -1, v8
	v_lshrrev_b32_e32 v36, 15, v8
	v_and_b32_e32 v36, 0x1fffc, v36
	v_add_u32_e32 v36, 0x10000, v36
	v_mov_b32_e32 v17, 0
	s_mov_b64 exec, s[36:37]
	ds_add_rtn_u32 v17, v36, v19
	s_mov_b64 exec, -1
	s_waitcnt vmcnt(4)
	v_cmp_ne_u32_e64 s[38:39], -1, v9

.Lw1b43:
	v_lshrrev_b32_e32 v37, 15, v9
	v_and_b32_e32 v37, 0x1fffc, v37
	v_add_u32_e32 v37, 0x10000, v37
	v_mov_b32_e32 v12, 0
	s_mov_b64 exec, s[38:39]
	ds_add_rtn_u32 v12, v37, v19
	s_mov_b64 exec, -1
	s_waitcnt vmcnt(3)
	v_cmp_ne_u32_e64 s[58:59], -1, v10
	v_lshrrev_b32_e32 v38, 15, v10
	v_and_b32_e32 v38, 0x1fffc, v38
	v_add_u32_e32 v38, 0x10000, v38
	v_mov_b32_e32 v18, 0
	s_mov_b64 exec, s[58:59]
	ds_add_rtn_u32 v18, v38, v19
	s_mov_b64 exec, -1
	s_waitcnt vmcnt(2)
	v_cmp_ne_u32_e64 s[60:61], -1, v13
	v_lshrrev_b32_e32 v39, 15, v13
	v_and_b32_e32 v39, 0x1fffc, v39
	v_add_u32_e32 v39, 0x10000, v39

.Lw1b44:
	v_mov_b32_e32 v14, 0
	s_mov_b64 exec, s[60:61]
	ds_add_rtn_u32 v14, v39, v19
	s_mov_b64 exec, -1
	s_waitcnt vmcnt(0)
	s_lshl_b32 s73, s72, 14
	s_add_u32 s70, s70, s73
	s_addc_u32 s71, s71, 0
	v_cmp_eq_u32_e64 s[36:37], 0, v59
	v_cvt_pk_f16_f32 v50, v50, v51
	v_cvt_pk_f16_f32 v51, v52, v53
	v_cvt_pk_f16_f32 v52, v54, v55
	v_cvt_pk_f16_f32 v53, v56, v57
	v_cndmask_b32_e64 v54, v50, v52, s[36:37]
	v_cndmask_b32_e64 v55, v51, v53, s[36:37]
	s_nop 1
	v_mov_b32_dpp v54, v54 quad_perm:[1,0,3,2] row_mask:0xf bank_mask:0xf bound_ctrl:1
	v_mov_b32_dpp v55, v55 quad_perm:[1,0,3,2] row_mask:0xf bank_mask:0xf bound_ctrl:1
	v_cndmask_b32_e64 v50, v54, v50, s[36:37]

.Lw1b45:
	v_cndmask_b32_e64 v51, v55, v51, s[36:37]
	v_cndmask_b32_e64 v52, v52, v54, s[36:37]
	v_cndmask_b32_e64 v53, v53, v55, s[36:37]
	global_store_dwordx4 v49, v[50:53], s[70:71] sc1
	s_branch .LBB1_232

.Lw1b46:
	s_nop 1
	v_add_u32_dpp v19, v19, v19 row_shr:2 row_mask:0xf bank_mask:0xf bound_ctrl:1
	s_nop 1
	v_add_u32_dpp v19, v19, v19 row_shr:4 row_mask:0xf bank_mask:0xf bound_ctrl:1
	s_nop 1
	v_add_u32_dpp v19, v19, v19 row_shr:8 row_mask:0xf bank_mask:0xf bound_ctrl:1
	s_nop 1
	v_add_u32_dpp v19, v19, v19 row_bcast:15 row_mask:0xa bank_mask:0xf
	s_nop 1
	v_add_u32_dpp v19, v19, v19 row_bcast:31 row_mask:0xc bank_mask:0xf
	s_and_saveexec_b64 s[34:35], s[4:5]
	v_mov_b32_e32 v20, 0x11b60
	v_lshl_add_u32 v1, v1, 2, v20
	ds_write_b32 v1, v19
	s_or_b64 exec, exec, s[34:35]
	s_add_i32 s41, s41, s40
	s_add_i32 s42, s42, s41
	s_add_i32 s43, s43, s42
	s_add_i32 s44, s44, s43
	s_add_i32 s45, s45, s44
	s_add_i32 s46, s46, s45
	s_add_i32 s47, s47, s46

.Lw1b47:
	s_add_i32 s48, s48, s47
	s_add_i32 s49, s49, s48
	s_add_i32 s50, s50, s49
	s_add_i32 s51, s51, s50
	s_add_i32 s52, s52, s51
	s_add_i32 s53, s53, s52
	s_add_i32 s54, s54, s53
	s_add_i32 s34, s55, s54
	s_waitcnt lgkmcnt(0)
	s_barrier
	s_and_saveexec_b64 s[36:37], s[22:23]
	s_cbranch_execz .LBB1_239
	v_mov_b32_e32 v1, 0x11b98
	v_mov_b32_e32 v20, 0x11b70
	ds_read_b32 v1, v1
	ds_read_b96 v[24:26], v20
	v_mov_b32_e32 v20, 0x11b60
	ds_read_b128 v[20:23], v20
	v_sub_u32_e32 v2, v19, v2
	s_waitcnt lgkmcnt(2)
	v_cndmask_b32_e64 v1, 0, v1, s[20:21]
	s_waitcnt lgkmcnt(1)
	v_cndmask_b32_e64 v24, 0, v24, s[14:15]

.Lw1b48:
	v_cndmask_b32_e64 v26, 0, v26, s[18:19]
	s_waitcnt lgkmcnt(0)
	v_cndmask_b32_e64 v22, 0, v22, s[10:11]
	v_cndmask_b32_e64 v21, 0, v21, s[8:9]
	v_cndmask_b32_e64 v20, v20, 0, s[6:7]
	v_cndmask_b32_e64 v23, 0, v23, s[12:13]
	v_add3_u32 v20, v21, v20, v22
	v_cndmask_b32_e64 v25, 0, v25, s[16:17]
	v_add3_u32 v20, v23, v20, v24
	v_add3_u32 v20, v25, v20, v26
	v_add3_u32 v1, v1, v20, v2
	v_mov_b32_e32 v2, 0x11000
	v_lshl_or_b32 v2, v0, 2, v2
	ds_write_b32 v2, v1
	v_lshl_or_b32 v2, s33, 9, v0
	s_mov_b32 s4, 0x186a0

.Lw1b49:
	v_cmp_gt_u32_e64 s[4:5], s4, v2
	s_and_b64 exec, exec, s[4:5]
	s_cbranch_execz .LBB1_239
	s_and_b64 s[4:5], s[30:31], exec
	s_cselect_b32 s4, 0x186a1, 0
	v_add_u32_e32 v20, s4, v2
	v_mov_b32_e32 v21, 0
	v_lshl_add_u64 v[20:21], v[20:21], 2, s[24:25]
	v_add_u32_e32 v1, s34, v1
	global_store_dword v[20:21], v1, off
.LBB1_239:
	s_or_b64 exec, exec, s[36:37]
	s_cmpk_eq_i32 s33, 0xc3
	s_cselect_b64 s[6:7], -1, 0
	v_cmp_eq_u32_e64 s[4:5], 0, v0
	s_and_b64 s[6:7], s[4:5], s[6:7]
	s_and_saveexec_b64 s[4:5], s[6:7]
	s_cbranch_execz .LBB1_241
	s_and_b64 s[6:7], s[30:31], exec
	s_cselect_b32 s6, 0x61a84, 0
	s_add_u32 s6, s24, s6
	s_addc_u32 s7, s25, 0
	v_mov_b32_e32 v1, 0x61000
	v_mov_b32_e32 v2, 0xc3500

.LBB1_241:
	s_or_b64 exec, exec, s[4:5]
	s_add_u32 s6, s26, s56
	s_addc_u32 s7, s27, 0
	s_ashr_i32 s35, s34, 31
	s_lshl_b64 s[4:5], s[34:35], 2
	s_add_u32 s8, s6, s4
	s_addc_u32 s9, s7, s5
	s_mov_b64 s[4:5], -1
	s_and_b64 vcc, exec, vcc
	s_waitcnt lgkmcnt(0)
	s_barrier
	s_cbranch_vccz .LBB1_265
	v_mov_b32_e32 v1, 0x11900
	ds_read_b32 v1, v1
	s_mov_b64 s[4:5], 0
	v_mov_b32_e32 v2, 0x11880
	s_movk_i32 s12, 0x51
	s_movk_i32 s13, 0x52
	s_movk_i32 s14, 0x59
	s_movk_i32 s15, 0x5a
	s_movk_i32 s16, 0x5d
	s_movk_i32 s17, 0x5e
	s_movk_i32 s18, 0x5f
	s_movk_i32 s19, 0x60
	s_movk_i32 s20, 0x61
	v_mov_b32_e32 v19, 0x11990

.Lw1b51:
	v_mov_b32_e32 v20, 1
	v_mov_b32_e32 v21, 0x11840
	v_mov_b32_e32 v22, 0x11820
	v_mov_b32_e32 v23, 0x11810
	v_mov_b32_e32 v24, 0x11808
	v_mov_b32_e32 v25, 0x11804
	v_mov_b32_e32 v26, 0x11800
	v_mov_b32_e32 v27, v0
	s_branch .LBB1_244
.LBB1_243:
	s_or_b64 exec, exec, s[10:11]
	v_lshl_add_u32 v28, v30, 2, v19
	ds_read_b32 v28, v28
	s_waitcnt lgkmcnt(0)
	v_lshl_add_u32 v28, v30, 13, v28
	v_sub_u32_e32 v28, v28, v29
	v_add_u32_e32 v28, v27, v28
	v_ashrrev_i32_e32 v29, 31, v28
	v_lshl_add_u64 v[28:29], v[28:29], 2, s[28:29]
	global_load_dword v28, v[28:29], off

.Lw1b52:
	v_add_u32_e32 v27, 0x400, v27
	v_cmp_le_i32_e32 vcc, s3, v27
	s_or_b64 s[4:5], vcc, s[4:5]
	s_waitcnt vmcnt(0)
	v_lshrrev_b32_e32 v29, 15, v28
	v_and_b32_e32 v29, 0x1fffc, v29
	v_add_u32_e32 v30, 0x11000, v29
	v_add_u32_e32 v29, 0x10800, v29
	ds_read_b32 v30, v30
	ds_add_rtn_u32 v29, v29, v20
	v_and_b32_e32 v31, 0x1fffff, v28
	s_waitcnt lgkmcnt(0)
	v_add_u32_e32 v28, v29, v30
	v_ashrrev_i32_e32 v29, 31, v28
	v_lshl_add_u64 v[28:29], v[28:29], 2, s[8:9]
	global_store_dword v[28:29], v31, off
	s_andn2_b64 exec, exec, s[4:5]
	s_cbranch_execz .LBB1_264
.LBB1_244:
	s_waitcnt lgkmcnt(0)
	v_cmp_gt_i32_e32 vcc, v1, v27
	s_nop 1
	v_cndmask_b32_e64 v28, 64, 0, vcc
.Lw1t53:
	s_cbranch_execz .Lw1c53
.Lw1b53:
	v_lshl_or_b32 v29, v28, 2, v2
	ds_read_b32 v29, v29
	v_or_b32_e32 v30, 32, v28
	s_waitcnt lgkmcnt(0)
	v_cmp_gt_i32_e32 vcc, v29, v27
	s_nop 1
	v_cndmask_b32_e32 v29, v30, v28, vcc
	v_cmp_lt_u32_e64 s[6:7], s12, v29
	v_cmp_gt_u32_e32 vcc, s13, v29
	s_and_saveexec_b64 s[10:11], vcc
	s_cbranch_execz .LBB1_246
	v_lshl_add_u32 v28, v29, 2, v21
	ds_read_b32 v30, v28
	s_andn2_b64 s[6:7], s[6:7], exec
	v_or_b32_e32 v28, 16, v29
	s_waitcnt lgkmcnt(0)
	v_cmp_gt_i32_e32 vcc, v30, v27
	s_and_b64 s[22:23], vcc, exec
	s_or_b64 s[6:7], s[6:7], s[22:23]
.LBB1_246:
	s_or_b64 exec, exec, s[10:11]
	s_and_saveexec_b64 s[10:11], s[6:7]
	v_mov_b32_e32 v28, v29
	s_or_b64 exec, exec, s[10:11]
	v_cmp_lt_u32_e64 s[6:7], s14, v28
.Lw1t54:
	s_cbranch_execz .Lw1c54
.Lw1b54:
	v_cmp_gt_u32_e32 vcc, s15, v28
	s_and_saveexec_b64 s[10:11], vcc
	s_cbranch_execz .LBB1_250
	v_lshl_add_u32 v29, v28, 2, v22
	ds_read_b32 v30, v29
	s_andn2_b64 s[6:7], s[6:7], exec
	v_add_u32_e32 v29, 8, v28
	s_waitcnt lgkmcnt(0)
	v_cmp_gt_i32_e32 vcc, v30, v27
	s_and_b64 s[22:23], vcc, exec
	s_or_b64 s[6:7], s[6:7], s[22:23]
.LBB1_250:
	s_or_b64 exec, exec, s[10:11]
	s_and_saveexec_b64 s[10:11], s[6:7]
	v_mov_b32_e32 v29, v28
	s_or_b64 exec, exec, s[10:11]
	v_cmp_lt_u32_e64 s[6:7], s16, v29
	v_cmp_gt_u32_e32 vcc, s17, v29
	s_and_saveexec_b64 s[10:11], vcc
	s_cbranch_execz .LBB1_254
	v_lshl_add_u32 v28, v29, 2, v23
	ds_read_b32 v28, v28
	s_andn2_b64 s[6:7], s[6:7], exec
	v_add_u32_e32 v30, 4, v29
	s_waitcnt lgkmcnt(0)
	v_cmp_gt_i32_e32 vcc, v28, v27
	s_and_b64 s[22:23], vcc, exec

.Lw1b55:
	s_or_b64 s[6:7], s[6:7], s[22:23]

.LBB1_273:
	v_lshrrev_b32_e32 v1, 15, v10
	v_and_b32_e32 v1, 0x1fffc, v1
	v_add_u32_e32 v1, 0x11000, v1
	ds_read_b32 v1, v1
.Lw1t59:
	s_cbranch_execz .Lw1c59
.Lw1b59:
	v_lshlrev_b32_e32 v2, 2, v18
	s_waitcnt lgkmcnt(0)
	v_lshl_add_u32 v1, v1, 2, v2
	ds_write_b32 v1, v10
	s_or_b64 exec, exec, s[4:5]
	v_cmp_ne_u32_e32 vcc, -1, v13
	s_and_saveexec_b64 s[4:5], vcc
	s_cbranch_execnz .LBB1_281
	s_branch .LBB1_282

.LBB1_275:
	v_lshrrev_b32_e32 v1, 15, v4
	v_and_b32_e32 v1, 0x1fffc, v1
	v_add_u32_e32 v1, 0x11000, v1
	ds_read_b32 v1, v1
	v_lshlrev_b32_e32 v2, 2, v5
	s_waitcnt lgkmcnt(0)
	v_lshl_add_u32 v1, v1, 2, v2
	ds_write_b32 v1, v4
	s_or_b64 exec, exec, s[4:5]
	v_cmp_ne_u32_e32 vcc, -1, v6

.LBB1_281:
	v_lshrrev_b32_e32 v1, 15, v13
	v_and_b32_e32 v1, 0x1fffc, v1
	v_add_u32_e32 v1, 0x11000, v1
	ds_read_b32 v1, v1
	v_lshlrev_b32_e32 v2, 2, v14
	s_waitcnt lgkmcnt(0)
	v_lshl_add_u32 v1, v1, 2, v2
	ds_write_b32 v1, v13
.LBB1_282:
	s_or_b64 exec, exec, s[4:5]

.Lw1b62:
	v_mov_b32_e32 v1, 0x11ba0
	v_mov_b32_e32 v2, -1
	ds_write_b32 v1, v2
	s_cmp_lt_i32 s3, 1
	s_waitcnt lgkmcnt(0)
	s_barrier
	s_cbranch_scc1 .LBB1_332
	v_lshlrev_b32_e32 v1, 2, v0
	s_lshl_b32 s18, s3, 2
	s_mov_b32 s19, 0x1fffc
	s_mov_b32 s20, 0x10000
	v_mov_b32_e32 v7, 0x11ba0
	v_mov_b32_e32 v2, v0
	v_cmp_gt_i32_e64 s[10:11], s3, v2
	ds_read_b32 v17, v1
	v_mov_b32_e32 v16, v1
	v_add_u32_e32 v2, 1024, v0
	v_cmp_gt_i32_e64 s[12:13], s3, v2
	ds_read_b32 v19, v1 offset:4096
	v_add_u32_e32 v18, 4096, v1

.Lw1b63:
	v_add_u32_e32 v2, 2048, v0
	v_cmp_gt_i32_e64 s[14:15], s3, v2
	ds_read_b32 v21, v1 offset:8192
	v_add_u32_e32 v20, 8192, v1
	v_add_u32_e32 v2, 3072, v0
	v_cmp_gt_i32_e64 s[16:17], s3, v2
	ds_read_b32 v23, v1 offset:12288
	v_add_u32_e32 v22, 12288, v1
	s_waitcnt lgkmcnt(0)
	v_lshrrev_b32_e32 v2, 15, v17
	v_and_b32_e32 v2, s19, v2
	v_lshrrev_b32_e32 v3, 15, v19
	v_and_b32_e32 v3, s19, v3
	v_lshrrev_b32_e32 v4, 15, v21
	v_and_b32_e32 v4, s19, v4
	v_lshrrev_b32_e32 v5, 15, v23
	v_and_b32_e32 v5, s19, v5
	v_cndmask_b32_e64 v2, 0, v2, s[10:11]
	v_add_u32_e32 v2, s20, v2
	v_cndmask_b32_e64 v3, 0, v3, s[12:13]
	v_add_u32_e32 v3, s20, v3

.Lw1b64:
	v_cndmask_b32_e64 v4, 0, v4, s[14:15]
	v_add_u32_e32 v4, s20, v4
	v_cndmask_b32_e64 v5, 0, v5, s[16:17]
	v_add_u32_e32 v5, s20, v5
	ds_read_b32 v24, v2
	ds_read_b32 v28, v2 offset:4096
	ds_read_b32 v25, v3
	ds_read_b32 v29, v3 offset:4096
	ds_read_b32 v26, v4
	ds_read_b32 v30, v4 offset:4096
	ds_read_b32 v27, v5
	ds_read_b32 v31, v5 offset:4096
	s_waitcnt lgkmcnt(0)
	v_cndmask_b32_e64 v2, 0, v24, s[10:11]
	v_lshlrev_b32_e32 v28, 2, v28
	v_mov_b32_e32 v8, v28
	v_mov_b32_e32 v24, 0
	v_cndmask_b32_e64 v3, 0, v25, s[12:13]
	v_lshlrev_b32_e32 v29, 2, v29

.Lw1b65:
	v_mov_b32_e32 v10, v29
	v_mov_b32_e32 v25, 0
	v_cndmask_b32_e64 v4, 0, v26, s[14:15]
	v_lshlrev_b32_e32 v30, 2, v30
	v_mov_b32_e32 v12, v30
	v_mov_b32_e32 v26, 0
	v_cndmask_b32_e64 v5, 0, v27, s[16:17]
	v_lshlrev_b32_e32 v31, 2, v31
	v_mov_b32_e32 v14, v31
	v_mov_b32_e32 v27, 0
	v_max_u32_e32 v6, v2, v3
	v_max3_u32 v6, v6, v4, v5
	s_mov_b32 s21, 0
.Lrs0_loop:
	v_cmp_lt_u32_e32 vcc, s21, v6
	s_cbranch_vccz .Lrs0_done
	v_cmp_gt_u32_e64 s[22:23], s18, v8
	v_cmp_gt_u32_e64 s[24:25], s18, v10
	v_cmp_gt_u32_e64 s[26:27], s18, v12
	v_cmp_gt_u32_e64 s[28:29], s18, v14
	v_cndmask_b32_e64 v2, v7, v8, s[22:23]
	v_cndmask_b32_e64 v3, v7, v10, s[24:25]
	v_cndmask_b32_e64 v4, v7, v12, s[26:27]

.Lw1b66:
	v_cndmask_b32_e64 v5, v7, v14, s[28:29]
	ds_read_b32 v9, v2
	ds_read_b32 v11, v3
	ds_read_b32 v13, v4
	ds_read_b32 v15, v5
	s_waitcnt lgkmcnt(3)
	v_cmp_lt_u64_e64 s[22:23], v[8:9], v[16:17]
	s_waitcnt lgkmcnt(2)
	v_cmp_lt_u64_e64 s[24:25], v[10:11], v[18:19]
	s_waitcnt lgkmcnt(1)
	v_cmp_lt_u64_e64 s[26:27], v[12:13], v[20:21]
	s_waitcnt lgkmcnt(0)
	v_cmp_lt_u64_e64 s[28:29], v[14:15], v[22:23]
	v_addc_co_u32_e64 v24, s[4:5], 0, v24, s[22:23]
	v_addc_co_u32_e64 v25, s[4:5], 0, v25, s[24:25]
	v_addc_co_u32_e64 v26, s[4:5], 0, v26, s[26:27]
	v_addc_co_u32_e64 v27, s[4:5], 0, v27, s[28:29]

.Lw1b67:
	v_add_u32_e32 v8, 4, v8
	v_add_u32_e32 v10, 4, v10
	v_add_u32_e32 v12, 4, v12
	v_add_u32_e32 v14, 4, v14
	s_add_i32 s21, s21, 1
	s_branch .Lrs0_loop
.Lrs0_done:
	v_and_b32_e32 v2, 0x1fffff, v17
	v_lshl_add_u32 v28, v24, 2, v28
	v_and_b32_e32 v3, 0x1fffff, v19
	v_lshl_add_u32 v29, v25, 2, v29
	v_and_b32_e32 v4, 0x1fffff, v21
	v_lshl_add_u32 v30, v26, 2, v30
	v_and_b32_e32 v5, 0x1fffff, v23
	v_lshl_add_u32 v31, v27, 2, v31
	s_mov_b64 exec, s[10:11]
	ds_write_b32 v28, v2 offset:32768
	s_mov_b64 exec, s[12:13]
	ds_write_b32 v29, v3 offset:32768
	s_mov_b64 exec, s[14:15]
	ds_write_b32 v30, v4 offset:32768

.LBB1_332:
	s_cmpk_lt_i32 s3, 0x1001
	s_cbranch_scc1 .LBB1_382
	v_add_u32_e32 v2, 4096, v0
	v_cmp_gt_i32_e64 s[10:11], s3, v2
	ds_read_b32 v17, v1 offset:16384
	v_add_u32_e32 v16, 16384, v1
	v_add_u32_e32 v2, 5120, v0
	v_cmp_gt_i32_e64 s[12:13], s3, v2
	ds_read_b32 v19, v1 offset:20480
	v_add_u32_e32 v18, 20480, v1
	v_add_u32_e32 v2, 6144, v0
	v_cmp_gt_i32_e64 s[14:15], s3, v2
	ds_read_b32 v21, v1 offset:24576
	v_add_u32_e32 v20, 24576, v1
	v_add_u32_e32 v2, 7168, v0

.Lw1b69:
	v_cmp_gt_i32_e64 s[16:17], s3, v2
	ds_read_b32 v23, v1 offset:28672
	v_add_u32_e32 v22, 28672, v1
	s_waitcnt lgkmcnt(0)
	v_lshrrev_b32_e32 v2, 15, v17
	v_and_b32_e32 v2, s19, v2
	v_lshrrev_b32_e32 v3, 15, v19
	v_and_b32_e32 v3, s19, v3
	v_lshrrev_b32_e32 v4, 15, v21
	v_and_b32_e32 v4, s19, v4
	v_lshrrev_b32_e32 v5, 15, v23
	v_and_b32_e32 v5, s19, v5
	v_cndmask_b32_e64 v2, 0, v2, s[10:11]
	v_add_u32_e32 v2, s20, v2
	v_cndmask_b32_e64 v3, 0, v3, s[12:13]
	v_add_u32_e32 v3, s20, v3
	v_cndmask_b32_e64 v4, 0, v4, s[14:15]
	v_add_u32_e32 v4, s20, v4
	v_cndmask_b32_e64 v5, 0, v5, s[16:17]
	v_add_u32_e32 v5, s20, v5
	ds_read_b32 v24, v2
	ds_read_b32 v28, v2 offset:4096

.Lw1b70:
	ds_read_b32 v25, v3
	ds_read_b32 v29, v3 offset:4096
	ds_read_b32 v26, v4
	ds_read_b32 v30, v4 offset:4096
	ds_read_b32 v27, v5
	ds_read_b32 v31, v5 offset:4096
	s_waitcnt lgkmcnt(0)
	v_cndmask_b32_e64 v2, 0, v24, s[10:11]
	v_lshlrev_b32_e32 v28, 2, v28
	v_mov_b32_e32 v8, v28
	v_mov_b32_e32 v24, 0
	v_cndmask_b32_e64 v3, 0, v25, s[12:13]
	v_lshlrev_b32_e32 v29, 2, v29
	v_mov_b32_e32 v10, v29
	v_mov_b32_e32 v25, 0
	v_cndmask_b32_e64 v4, 0, v26, s[14:15]
	v_lshlrev_b32_e32 v30, 2, v30
	v_mov_b32_e32 v12, v30
	v_mov_b32_e32 v26, 0
	v_cndmask_b32_e64 v5, 0, v27, s[16:17]

.Lw1b71:
	v_lshlrev_b32_e32 v31, 2, v31
	v_mov_b32_e32 v14, v31
	v_mov_b32_e32 v27, 0
	v_max_u32_e32 v6, v2, v3
	v_max3_u32 v6, v6, v4, v5
	s_mov_b32 s21, 0
.Lrs4_loop:
	v_cmp_lt_u32_e32 vcc, s21, v6
	s_cbranch_vccz .Lrs4_done
	v_cmp_gt_u32_e64 s[22:23], s18, v8
	v_cmp_gt_u32_e64 s[24:25], s18, v10
	v_cmp_gt_u32_e64 s[26:27], s18, v12
	v_cmp_gt_u32_e64 s[28:29], s18, v14
	v_cndmask_b32_e64 v2, v7, v8, s[22:23]
	v_cndmask_b32_e64 v3, v7, v10, s[24:25]
	v_cndmask_b32_e64 v4, v7, v12, s[26:27]
	v_cndmask_b32_e64 v5, v7, v14, s[28:29]
	ds_read_b32 v9, v2
	ds_read_b32 v11, v3
	ds_read_b32 v13, v4

.Lw1b72:
	ds_read_b32 v15, v5
	s_waitcnt lgkmcnt(3)
	v_cmp_lt_u64_e64 s[22:23], v[8:9], v[16:17]
	s_waitcnt lgkmcnt(2)
	v_cmp_lt_u64_e64 s[24:25], v[10:11], v[18:19]
	s_waitcnt lgkmcnt(1)
	v_cmp_lt_u64_e64 s[26:27], v[12:13], v[20:21]
	s_waitcnt lgkmcnt(0)
	v_cmp_lt_u64_e64 s[28:29], v[14:15], v[22:23]
	v_addc_co_u32_e64 v24, s[4:5], 0, v24, s[22:23]
	v_addc_co_u32_e64 v25, s[4:5], 0, v25, s[24:25]
	v_addc_co_u32_e64 v26, s[4:5], 0, v26, s[26:27]
	v_addc_co_u32_e64 v27, s[4:5], 0, v27, s[28:29]
	v_add_u32_e32 v8, 4, v8
	v_add_u32_e32 v10, 4, v10
	v_add_u32_e32 v12, 4, v12
	v_add_u32_e32 v14, 4, v14
	s_add_i32 s21, s21, 1
	s_branch .Lrs4_loop

.Lw1b73:
	v_and_b32_e32 v3, 0x1fffff, v19
	v_lshl_add_u32 v29, v25, 2, v29
	v_and_b32_e32 v4, 0x1fffff, v21
	v_lshl_add_u32 v30, v26, 2, v30
	v_and_b32_e32 v5, 0x1fffff, v23
	v_lshl_add_u32 v31, v27, 2, v31
	s_mov_b64 exec, s[10:11]
	ds_write_b32 v28, v2 offset:32768
	s_mov_b64 exec, s[12:13]
	ds_write_b32 v29, v3 offset:32768
	s_mov_b64 exec, s[14:15]
	ds_write_b32 v30, v4 offset:32768
	s_mov_b64 exec, s[16:17]
	ds_write_b32 v31, v5 offset:32768
	s_mov_b64 exec, -1
.LBB1_382:
	s_sub_i32 s4, 0, s34
	s_and_b32 s4, s4, 3
	s_min_i32 s4, s4, s3
	v_cmp_gt_i32_e32 vcc, s4, v0
	s_waitcnt lgkmcnt(0)
.Lw1t74:
	s_cbranch_execz .Lw1c74
.Lw1b74:
	s_barrier
	s_and_saveexec_b64 s[6:7], vcc
	s_cbranch_execz .LBB1_384
	v_lshlrev_b32_e32 v1, 2, v0
	ds_read_b32 v2, v1 offset:32768
	s_waitcnt lgkmcnt(0)
	global_store_dword v1, v2, s[8:9]

.Lmy_cvt1:
	s_waitcnt lgkmcnt(0)
	s_load_dwordx4 s[20:23], s[0:1], 0x28
	s_sub_i32 s3, s2, 392
	s_cmp_ge_u32 s3, 193
	s_cbranch_scc1 .Lmy_cvt1_end
	v_and_b32_e32 v1, 0x3c0, v0
	v_and_b32_e32 v2, 63, v0
	v_lshlrev_b32_e32 v3, 5, v1
	v_lshl_or_b32 v3, v2, 4, v3
	v_and_b32_e32 v4, 1, v0
	v_lshrrev_b32_e32 v5, 1, v2
	v_lshl_or_b32 v5, v4, 5, v5
	v_add_u32_e32 v5, v5, v1
	v_lshlrev_b32_e32 v5, 4, v5
	v_cmp_eq_u32_e32 vcc, 0, v4
	s_waitcnt lgkmcnt(0)
	s_add_i32 s8, s3, 792
	s_lshl_b32 s9, s8, 10
	s_sub_i32 s9, 0x1869c0, s9

.Lw1b77:
	v_cmp_ge_i32_e64 s[24:25], s9, v1
	s_add_i32 s8, s3, 985
	s_lshl_b32 s9, s8, 10
	s_sub_i32 s9, 0x1869c0, s9
	v_cmp_ge_i32_e64 s[26:27], s9, v1
	s_add_i32 s8, s3, 1178
	s_lshl_b32 s9, s8, 10
	s_sub_i32 s9, 0x1869c0, s9
	v_cmp_ge_i32_e64 s[28:29], s9, v1
	s_add_i32 s8, s3, 1371
	s_lshl_b32 s9, s8, 10
	s_sub_i32 s9, 0x1869c0, s9
	v_cmp_ge_i32_e64 s[30:31], s9, v1
	s_add_i32 s8, s3, 792
	s_lshl_b32 s9, s8, 15
	s_add_u32 s10, s20, s9
	s_addc_u32 s11, s21, 0
	s_mov_b64 exec, s[24:25]
	global_load_dwordx4 v[8:11], v3, s[10:11] nt

.Lw1b78:
	global_load_dwordx4 v[12:15], v3, s[10:11] offset:1024 nt
	s_add_i32 s8, s3, 985
	s_lshl_b32 s9, s8, 15
	s_add_u32 s10, s20, s9
	s_addc_u32 s11, s21, 0
	s_mov_b64 exec, s[26:27]
	global_load_dwordx4 v[16:19], v3, s[10:11] nt
	global_load_dwordx4 v[20:23], v3, s[10:11] offset:1024 nt
	s_add_i32 s8, s3, 1178
	s_lshl_b32 s9, s8, 15
	s_add_u32 s10, s20, s9
	s_addc_u32 s11, s21, 0
	s_mov_b64 exec, s[28:29]
	global_load_dwordx4 v[24:27], v3, s[10:11] nt
	global_load_dwordx4 v[28:31], v3, s[10:11] offset:1024 nt
	s_add_i32 s8, s3, 1371
	s_lshl_b32 s9, s8, 15
	s_add_u32 s10, s20, s9
	s_addc_u32 s11, s21, 0
	s_mov_b64 exec, s[30:31]
	global_load_dwordx4 v[32:35], v3, s[10:11] nt

.Lw1b79:
	global_load_dwordx4 v[36:39], v3, s[10:11] offset:1024 nt
	s_waitcnt vmcnt(6)
	s_add_i32 s8, s3, 792
	s_lshl_b32 s9, s8, 14
	s_add_u32 s10, s22, s9
	s_addc_u32 s11, s23, 0
	s_mov_b64 exec, s[24:25]
	v_cvt_pk_f16_f32 v8, v8, v9
	v_cvt_pk_f16_f32 v9, v10, v11
	v_cvt_pk_f16_f32 v10, v12, v13
	v_cvt_pk_f16_f32 v11, v14, v15
	v_cndmask_b32_e32 v12, v8, v10, vcc
	v_cndmask_b32_e32 v13, v9, v11, vcc
	s_nop 1
	v_mov_b32_dpp v12, v12 quad_perm:[1,0,3,2] row_mask:0xf bank_mask:0xf bound_ctrl:1
	v_mov_b32_dpp v13, v13 quad_perm:[1,0,3,2] row_mask:0xf bank_mask:0xf bound_ctrl:1
	v_cndmask_b32_e32 v8, v12, v8, vcc
	v_cndmask_b32_e32 v9, v13, v9, vcc
	v_cndmask_b32_e32 v10, v10, v12, vcc
	v_cndmask_b32_e32 v11, v11, v13, vcc
	global_store_dwordx4 v5, v[8:11], s[10:11] sc1
	s_waitcnt vmcnt(5)

.Lw1b80:
	s_add_i32 s8, s3, 985
	s_lshl_b32 s9, s8, 14
	s_add_u32 s10, s22, s9
	s_addc_u32 s11, s23, 0
	s_mov_b64 exec, s[26:27]
	v_cvt_pk_f16_f32 v16, v16, v17
	v_cvt_pk_f16_f32 v17, v18, v19
	v_cvt_pk_f16_f32 v18, v20, v21
	v_cvt_pk_f16_f32 v19, v22, v23
	v_cndmask_b32_e32 v20, v16, v18, vcc
	v_cndmask_b32_e32 v21, v17, v19, vcc
	s_nop 1
	v_mov_b32_dpp v20, v20 quad_perm:[1,0,3,2] row_mask:0xf bank_mask:0xf bound_ctrl:1
	v_mov_b32_dpp v21, v21 quad_perm:[1,0,3,2] row_mask:0xf bank_mask:0xf bound_ctrl:1
	v_cndmask_b32_e32 v16, v20, v16, vcc
	v_cndmask_b32_e32 v17, v21, v17, vcc
	v_cndmask_b32_e32 v18, v18, v20, vcc
	v_cndmask_b32_e32 v19, v19, v21, vcc
	global_store_dwordx4 v5, v[16:19], s[10:11] sc1
	s_waitcnt vmcnt(4)
	s_add_i32 s8, s3, 1178
	s_lshl_b32 s9, s8, 14

.Lw1b81:
	s_add_u32 s10, s22, s9
	s_addc_u32 s11, s23, 0
	s_mov_b64 exec, s[28:29]
	v_cvt_pk_f16_f32 v24, v24, v25
	v_cvt_pk_f16_f32 v25, v26, v27
	v_cvt_pk_f16_f32 v26, v28, v29
	v_cvt_pk_f16_f32 v27, v30, v31
	v_cndmask_b32_e32 v28, v24, v26, vcc
	v_cndmask_b32_e32 v29, v25, v27, vcc
	s_nop 1
	v_mov_b32_dpp v28, v28 quad_perm:[1,0,3,2] row_mask:0xf bank_mask:0xf bound_ctrl:1
	v_mov_b32_dpp v29, v29 quad_perm:[1,0,3,2] row_mask:0xf bank_mask:0xf bound_ctrl:1
	v_cndmask_b32_e32 v24, v28, v24, vcc
	v_cndmask_b32_e32 v25, v29, v25, vcc
	v_cndmask_b32_e32 v26, v26, v28, vcc
	v_cndmask_b32_e32 v27, v27, v29, vcc
	global_store_dwordx4 v5, v[24:27], s[10:11] sc1
	s_waitcnt vmcnt(3)
	s_add_i32 s8, s3, 1371
	s_lshl_b32 s9, s8, 14
	s_add_u32 s10, s22, s9
	s_addc_u32 s11, s23, 0
	s_mov_b64 exec, s[30:31]

.Lw1b82:
	v_cvt_pk_f16_f32 v32, v32, v33
	v_cvt_pk_f16_f32 v33, v34, v35
	v_cvt_pk_f16_f32 v34, v36, v37
	v_cvt_pk_f16_f32 v35, v38, v39
	v_cndmask_b32_e32 v36, v32, v34, vcc
	v_cndmask_b32_e32 v37, v33, v35, vcc
	s_nop 1
	v_mov_b32_dpp v36, v36 quad_perm:[1,0,3,2] row_mask:0xf bank_mask:0xf bound_ctrl:1
	v_mov_b32_dpp v37, v37 quad_perm:[1,0,3,2] row_mask:0xf bank_mask:0xf bound_ctrl:1
	v_cndmask_b32_e32 v32, v36, v32, vcc
	v_cndmask_b32_e32 v33, v37, v33, vcc
	v_cndmask_b32_e32 v34, v34, v36, vcc
	v_cndmask_b32_e32 v35, v35, v37, vcc
	global_store_dwordx4 v5, v[32:35], s[10:11] sc1

.Lw2b0:
	s_load_dwordx4 s[4:7], s[0:1], 0x28
	s_load_dwordx2 s[10:11], s[0:1], 0x38
	v_lshlrev_b32_e32 v2, 4, v0
	v_min_u32_e32 v1, 0x7f, v0
	v_lshlrev_b32_e32 v24, 2, v1
	v_readfirstlane_b32 s3, v0
	v_add_u32_e32 v28, 0x3400, v2
	v_add_u32_e32 v29, 0x6800, v2
	v_add_u32_e32 v30, 0x9c00, v2
	v_add_u32_e32 v31, 0xd00, v0
	v_min_u32_e32 v31, 0xfff, v31
	v_lshlrev_b32_e32 v31, 4, v31
	s_waitcnt lgkmcnt(0)
	global_load_dwordx4 v[14:17], v2, s[8:9]
	global_load_dwordx4 v[6:9], v28, s[8:9]
	global_load_dwordx4 v[10:13], v29, s[8:9]
	global_load_dwordx4 v[18:21], v30, s[8:9]

.Lw2b2:
	s_waitcnt vmcnt(8)
	ds_write_b128 v2, v[14:17]
	s_waitcnt vmcnt(7)

.Lw2b3:
	ds_write_b128 v2, v[6:9] offset:13312
	s_waitcnt vmcnt(6)
	ds_write_b128 v2, v[10:13] offset:26624
	s_waitcnt vmcnt(5)
	ds_write_b128 v2, v[18:21] offset:39936
	s_movk_i32 s4, 0x300
	v_cmp_gt_u32_e32 vcc, s4, v0
	s_waitcnt vmcnt(4)
	s_and_saveexec_b64 s[4:5], vcc
	ds_write_b128 v2, v[32:35] offset:53248
	s_or_b64 exec, exec, s[4:5]
	s_movk_i32 s4, 0x80
	v_cmp_gt_u32_e32 vcc, s4, v0
	s_and_saveexec_b64 s[4:5], vcc
	s_cbranch_execz .LBB2_4
	s_waitcnt vmcnt(2)
	v_add_f32_e32 v2, v4, v5
	v_mov_b32_e32 v4, 0x1dd00
	v_lshl_add_u32 v4, v0, 2, v4
	s_waitcnt vmcnt(1)
	ds_write2st64_b32 v4, v2, v1 offset1:2
	s_waitcnt vmcnt(0)
	ds_write_b32 v4, v3 offset:1024

.LBB2_6:
	s_or_b64 exec, exec, s[4:5]
	s_waitcnt vmcnt(1)
	v_bfe_u32 v1, v0, 4, 2
	v_bfe_u32 v2, v0, 2, 2
	v_cmp_eq_u32_e32 vcc, v1, v2
	v_and_b32_e32 v2, 3, v0
	v_cmp_eq_u32_e64 s[4:5], 0, v2
	s_waitcnt vmcnt(0)
	v_mov_b32_e32 v3, 0x3c00
	s_and_b64 s[4:5], vcc, s[4:5]

.Lw2b5:
	v_cndmask_b32_e64 v4, 0, v3, s[4:5]
	v_cmp_eq_u32_e64 s[4:5], 1, v2
	s_and_b64 s[4:5], vcc, s[4:5]
	s_lshr_b32 s12, s3, 6
	v_cndmask_b32_e64 v5, 0, v3, s[4:5]
	v_cmp_eq_u32_e64 s[4:5], 2, v2
	s_and_b64 s[4:5], vcc, s[4:5]
	v_and_b32_e32 v77, 63, v0
	v_cndmask_b32_e64 v6, 0, v3, s[4:5]
	v_cmp_eq_u32_e64 s[4:5], 3, v2
	s_and_b64 vcc, vcc, s[4:5]
	v_cndmask_b32_e32 v2, 0, v3, vcc
	v_pack_b32_f16 v73, v6, v2
	v_lshlrev_b32_e32 v2, 2, v0
	s_waitcnt lgkmcnt(0)
	s_barrier
	v_and_b32_e32 v82, 15, v0
	v_pack_b32_f16 v72, v4, v5
	s_load_dword s3, s[0:1], 0x68
	v_and_b32_e32 v84, 0xc0, v2
	s_mul_i32 s0, s12, 0x1100

.Lw2b6:
	v_and_b32_e32 v2, 48, v0
	v_bfe_u32 v5, v0, 2, 4
	v_lshlrev_b32_e32 v0, 6, v0
	s_add_i32 s4, s0, 0x10000
	v_mul_u32_u24_e32 v5, 0x110, v5
	v_and_b32_e32 v0, 0xc0, v0
	v_mov_b32_e32 v3, 0
	s_movk_i32 s20, 0x110
	v_add3_u32 v85, s4, v5, v0
	v_mov_b32_e32 v0, s4
	v_lshlrev_b32_e32 v4, 7, v1
	v_mad_u32_u24 v5, v82, s20, v0
	v_lshlrev_b32_e32 v86, 5, v1
	v_lshlrev_b32_e32 v0, 6, v1
	v_mov_b32_e32 v1, v3
	v_lshlrev_b32_e32 v83, 4, v82
	v_lshl_add_u64 v[78:79], s[14:15], 0, v[0:1]
	v_mbcnt_lo_u32_b32 v0, -1, 0
	v_cmp_eq_u32_e64 s[0:1], 0, v77
	v_lshl_add_u64 v[74:75], s[10:11], 0, v[2:3]

.Lw2b7:
	v_or_b32_e32 v76, s4, v83
	v_or_b32_e32 v87, 28, v84
	v_or_b32_e32 v88, 32, v84
	v_or_b32_e32 v89, 36, v84
	v_or_b32_e32 v90, 40, v84
	v_or_b32_e32 v91, 44, v84
	v_or_b32_e32 v92, 48, v84
	v_or_b32_e32 v93, 52, v84
	v_or_b32_e32 v94, 56, v84
	v_or_b32_e32 v95, 60, v84
	v_mov_b32_e32 v96, 0x1e900
	v_add_u32_e32 v97, 0x1dd00, v4
	s_mov_b32 s21, 0x1ffff00
	v_add_u32_e32 v98, v5, v2
	v_lshrrev_b32_e32 v125, 1, v86
	v_lshrrev_b32_e32 v126, 5, v86
	v_add3_u32 v125, v98, v86, v125
	v_mad_u32_u24 v126, v126, s20, v76
	v_mov_b32_e32 v99, 0x3727c5ac
	s_mov_b32 s22, 0x800000
	v_mov_b32_e32 v100, 0xc0135761
	v_mbcnt_hi_u32_b32 v101, -1, v0

.Lw2b8:
	v_mov_b32_e32 v102, 0x1dd00
	s_mov_b32 s47, s41

.LBB2_7:
	v_mov_b32_e32 v32, v28
	v_mov_b32_e32 v33, v24
	v_mov_b32_e32 v34, v29
	v_mov_b32_e32 v35, v25
	v_pk_add_f32 v[32:33], v[32:33], v[34:35]
	v_mov_b32_e32 v34, v30
	v_mov_b32_e32 v35, v26
	v_mov_b32_e32 v36, v31
	v_mov_b32_e32 v37, v27
	v_pk_add_f32 v[34:35], v[34:35], v[36:37]
	v_mov_b32_e32 v36, v20
	v_pk_add_f32 v[32:33], v[32:33], v[34:35]
	v_mov_b32_e32 v34, v21
	v_mov_b32_e32 v35, v22
	v_mov_b32_e32 v37, v23
	v_pk_add_f32 v[34:35], v[34:35], v[36:37]
	v_add_f32_e32 v32, 0, v32
	v_pk_add_f32 v[34:35], v[34:35], v[34:35] op_sel:[0,1] op_sel_hi:[1,0]

.Lw2b9:
	v_add_f32_e32 v32, v32, v33
	v_add_f32_e32 v36, v16, v17
	v_add_f32_e32 v38, v18, v19
	v_mov_b32_e32 v33, v12
	v_mov_b32_e32 v35, v13
	v_mov_b32_e32 v37, v14
	v_mov_b32_e32 v39, v15
	v_pk_add_f32 v[32:33], v[32:33], v[34:35]
	v_pk_add_f32 v[34:35], v[36:37], v[38:39]
	v_mov_b32_e32 v36, v8
	v_pk_add_f32 v[32:33], v[32:33], v[34:35]
	v_mov_b32_e32 v34, v9
	v_mov_b32_e32 v35, v10
	v_mov_b32_e32 v37, v11
	v_pk_add_f32 v[34:35], v[34:35], v[36:37]
	v_pk_add_f32 v[32:33], v[32:33], v[32:33] op_sel:[0,1] op_sel_hi:[1,0]
	v_pk_add_f32 v[34:35], v[34:35], v[34:35] op_sel:[0,1] op_sel_hi:[1,0]
	v_add_f32_e32 v36, v4, v5
	v_add_f32_e32 v38, v6, v7
	v_mov_b32_e32 v33, v0
	v_mov_b32_e32 v35, v1
	v_mov_b32_e32 v37, v2
	v_mov_b32_e32 v39, v3
	v_pk_add_f32 v[32:33], v[32:33], v[34:35]

.Lw2b10:
	v_pk_add_f32 v[34:35], v[36:37], v[38:39]
	s_nop 0
	v_pk_add_f32 v[32:33], v[32:33], v[34:35]
	v_and_b32_e32 v34, 64, v101
	v_add_f32_e32 v32, v32, v33
	v_xor_b32_e32 v33, 16, v101
	v_add_u32_e32 v34, 64, v34
	v_cmp_lt_i32_e32 vcc, v33, v34
	s_nop 1
	v_cndmask_b32_e32 v33, v101, v33, vcc
	v_lshlrev_b32_e32 v42, 2, v33
	ds_bpermute_b32 v33, v42, v32
	s_waitcnt lgkmcnt(0)
	v_add_f32_e32 v32, v32, v33
	v_xor_b32_e32 v33, 32, v101
	v_cmp_lt_i32_e32 vcc, v33, v34
	s_nop 1
	v_cndmask_b32_e32 v33, v101, v33, vcc
	v_lshlrev_b32_e32 v43, 2, v33
	ds_bpermute_b32 v33, v43, v32
	s_waitcnt lgkmcnt(0)
	v_add_f32_e32 v44, v32, v33
	v_fmamk_f32 v29, v44, 0xbc000000, v29
	v_fmamk_f32 v25, v44, 0xbc000000, v25

.Lw2b11:
	v_fmamk_f32 v41, v44, 0xbc000000, v31
	v_fmamk_f32 v40, v44, 0xbc000000, v30
	v_fmac_f32_e32 v28, 0xbc000000, v44
	v_fmamk_f32 v39, v44, 0xbc000000, v27
	v_fmac_f32_e32 v24, 0xbc000000, v44
	v_mov_b32_e32 v30, v29
	v_mov_b32_e32 v31, v25
	v_fmamk_f32 v38, v44, 0xbc000000, v26
	v_mov_b32_e32 v26, v28
	v_mov_b32_e32 v27, v24
	v_pk_mul_f32 v[30:31], v[30:31], v[30:31]
	v_mov_b32_e32 v32, v41
	v_mov_b32_e32 v33, v39
	v_pk_fma_f32 v[26:27], v[26:27], v[26:27], v[30:31]
	v_mov_b32_e32 v30, v40
	v_mov_b32_e32 v31, v38
	v_pk_mul_f32 v[32:33], v[32:33], v[32:33]
	v_fmamk_f32 v37, v44, 0xbc000000, v21
	v_pk_fma_f32 v[30:31], v[30:31], v[30:31], v[32:33]
	v_fmamk_f32 v36, v44, 0xbc000000, v20

.Lw2b12:
	v_fmamk_f32 v23, v44, 0xbc000000, v23
	v_fmac_f32_e32 v22, 0xbc000000, v44
	v_pk_add_f32 v[26:27], v[26:27], v[30:31]
	v_pk_mul_f32 v[20:21], v[22:23], v[22:23]
	v_pk_mul_f32 v[30:31], v[36:37], v[36:37]
	v_fmac_f32_e32 v12, 0xbc000000, v44
	v_pk_mov_b32 v[32:33], v[30:31], v[20:21] op_sel:[1,0]
	v_mov_b32_e32 v31, v21
	v_pk_add_f32 v[20:21], v[32:33], v[30:31]
	v_fmamk_f32 v34, v44, 0xbc000000, v18
	v_fmamk_f32 v31, v44, 0xbc000000, v15
	v_fmamk_f32 v30, v44, 0xbc000000, v14
	v_fmamk_f32 v13, v44, 0xbc000000, v13
	v_mul_f32_e32 v18, v12, v12
	v_pk_add_f32 v[14:15], v[26:27], v[26:27] op_sel:[0,1] op_sel_hi:[1,0]
	v_fmamk_f32 v35, v44, 0xbc000000, v19

.Lw2b13:
	v_mul_f32_e32 v32, v13, v13
	v_mov_b32_e32 v15, v18
	v_pk_add_f32 v[18:19], v[20:21], v[20:21] op_sel:[0,1] op_sel_hi:[1,0]
	v_fmamk_f32 v17, v44, 0xbc000000, v17
	v_mov_b32_e32 v19, v32
	v_fmac_f32_e32 v16, 0xbc000000, v44
	v_pk_add_f32 v[14:15], v[14:15], v[18:19]
	v_mul_f32_e32 v18, v17, v17
	v_mul_f32_e32 v20, v35, v35
	v_mul_f32_e32 v33, v30, v30
	v_mul_f32_e32 v45, v31, v31
	v_pk_fma_f32 v[18:19], v[16:17], v[16:17], v[18:19] op_sel_hi:[1,1,0]
	v_pk_fma_f32 v[20:21], v[34:35], v[34:35], v[20:21] op_sel_hi:[1,1,0]
	v_mov_b32_e32 v19, v33
	v_mov_b32_e32 v21, v45
	v_pk_add_f32 v[18:19], v[18:19], v[20:21]
	v_fmamk_f32 v33, v44, 0xbc000000, v9
	v_fmamk_f32 v32, v44, 0xbc000000, v8
	v_fmamk_f32 v11, v44, 0xbc000000, v11
	v_fmac_f32_e32 v10, 0xbc000000, v44

.Lw2b14:
	v_pk_add_f32 v[14:15], v[14:15], v[18:19]
	v_pk_mul_f32 v[8:9], v[10:11], v[10:11]
	v_pk_mul_f32 v[18:19], v[32:33], v[32:33]
	v_fmamk_f32 v1, v44, 0xbc000000, v1
	v_pk_mov_b32 v[20:21], v[18:19], v[8:9] op_sel:[1,0]
	v_mov_b32_e32 v19, v9
	v_pk_add_f32 v[8:9], v[20:21], v[18:19]
	v_fmac_f32_e32 v0, 0xbc000000, v44
	v_fmamk_f32 v19, v44, 0xbc000000, v7
	v_fmamk_f32 v18, v44, 0xbc000000, v6
	v_mul_f32_e32 v20, v0, v0
	v_mul_f32_e32 v21, v1, v1
	v_pk_add_f32 v[6:7], v[14:15], v[14:15] op_sel:[0,1] op_sel_hi:[1,0]
	v_pk_add_f32 v[8:9], v[8:9], v[8:9] op_sel:[0,1] op_sel_hi:[1,0]
	v_fmamk_f32 v5, v44, 0xbc000000, v5
	v_mov_b32_e32 v7, v20
	v_mov_b32_e32 v9, v21
	v_fmac_f32_e32 v4, 0xbc000000, v44

.Lw2b15:
	v_fmamk_f32 v3, v44, 0xbc000000, v3
	v_fmamk_f32 v2, v44, 0xbc000000, v2
	v_pk_add_f32 v[6:7], v[6:7], v[8:9]
	v_mul_f32_e32 v8, v5, v5
	v_mul_f32_e32 v14, v19, v19
	v_mul_f32_e32 v26, v2, v2
	v_mul_f32_e32 v27, v3, v3
	v_pk_fma_f32 v[8:9], v[4:5], v[4:5], v[8:9] op_sel_hi:[1,1,0]
	v_pk_fma_f32 v[14:15], v[18:19], v[18:19], v[14:15] op_sel_hi:[1,1,0]
	v_mov_b32_e32 v9, v26
	v_mov_b32_e32 v15, v27
	v_pk_add_f32 v[8:9], v[8:9], v[14:15]
	s_nop 0
	v_pk_add_f32 v[6:7], v[6:7], v[8:9]
	s_nop 0
	v_add_f32_e32 v6, v6, v7
	ds_bpermute_b32 v7, v42, v6
	s_waitcnt lgkmcnt(0)
	v_add_f32_e32 v6, v6, v7
	ds_bpermute_b32 v7, v43, v6
	s_waitcnt lgkmcnt(0)
	v_add_f32_e32 v6, v6, v7

.Lw2b16:
	v_fmamk_f32 v6, v6, 0x3c000000, v99
	v_mul_f32_e32 v7, 0x4b800000, v6
	v_cmp_gt_f32_e32 vcc, s22, v6
	s_nop 1
	v_cndmask_b32_e32 v6, v6, v7, vcc
	v_rsq_f32_e32 v14, v6
	ds_read_b128 v[6:9], v97 offset:512
	ds_read_b128 v[42:45], v97 offset:528
	ds_read_b128 v[46:49], v97 offset:1024
	ds_read_b128 v[50:53], v97 offset:1040
	v_mul_f32_e32 v15, 0x45800000, v14
	v_cndmask_b32_e32 v20, v14, v15, vcc
	v_pk_mul_f32 v[26:27], v[20:21], v[28:29] op_sel_hi:[0,1]
	s_waitcnt lgkmcnt(1)
	v_pk_fma_f32 v[6:7], v[6:7], v[26:27], v[46:47]
	v_or_b32_e32 v14, s4, v82
	v_pk_mul_f32 v[26:27], v[6:7], v[6:7]
	v_ashrrev_i32_e32 v15, 31, v14
	v_fmamk_f32 v21, v26, 0xbdd2d3e8, v100
	v_mul_f32_e32 v21, v6, v21

.Lw2b17:
	v_fmamk_f32 v26, v27, 0xbdd2d3e8, v100
	v_exp_f32_e32 v21, v21
	v_mul_f32_e32 v26, v7, v26
	v_exp_f32_e32 v26, v26
	v_lshlrev_b64 v[14:15], 8, v[14:15]
	v_add_f32_e32 v21, 1.0, v21
	v_rcp_f32_e32 v28, v21
	v_add_f32_e32 v21, 1.0, v26
	v_pk_mul_f32 v[26:27], v[20:21], v[40:41] op_sel_hi:[0,1]
	v_pk_fma_f32 v[8:9], v[8:9], v[26:27], v[48:49]
	v_rcp_f32_e32 v29, v21
	v_pk_mul_f32 v[40:41], v[8:9], v[8:9]
	v_mad_u32_u24 v104, v86, 6, v83
	s_cmp_ge_u32 s4, 0xd000
	s_cselect_b32 s47, 1, 0
	s_lshl_b32 s12, s4, 8
	v_mov_b32_e32 v105, 0
	v_add_u32_e32 v104, s12, v104
	s_nop 0
	v_lshl_add_u64 v[104:105], v[78:79], 0, v[104:105]
	v_fmamk_f32 v21, v40, 0xbdd2d3e8, v100
	v_mul_f32_e32 v21, v8, v21

.Lw2b18:
	v_exp_f32_e32 v21, v21
	v_fmamk_f32 v14, v41, 0xbdd2d3e8, v100
	v_pk_mul_f32 v[6:7], v[6:7], v[28:29]
	v_mul_f32_e32 v14, v9, v14
	v_cvt_pk_f16_f32 v6, v6, v7
	v_add_f32_e32 v7, 1.0, v21
	v_exp_f32_e32 v21, v14
	v_rcp_f32_e32 v28, v7
	v_pk_mul_f32 v[14:15], v[20:21], v[24:25] op_sel_hi:[0,1]
	s_waitcnt lgkmcnt(0)
	v_pk_fma_f32 v[14:15], v[42:43], v[14:15], v[50:51]
	v_add_f32_e32 v7, 1.0, v21
	v_pk_mul_f32 v[24:25], v[14:15], v[14:15]
	v_rcp_f32_e32 v29, v7
	v_fmamk_f32 v24, v24, 0xbdd2d3e8, v100
	v_mul_f32_e32 v24, v14, v24
	v_exp_f32_e32 v24, v24
	v_fmamk_f32 v21, v25, 0xbdd2d3e8, v100
	v_mul_f32_e32 v21, v15, v21
	v_pk_mul_f32 v[8:9], v[8:9], v[28:29]
	v_add_f32_e32 v7, 1.0, v24
	v_pk_mul_f32 v[24:25], v[20:21], v[38:39] op_sel_hi:[0,1]

.Lw2b19:
	v_pk_fma_f32 v[24:25], v[44:45], v[24:25], v[52:53]
	v_exp_f32_e32 v21, v21
	v_pk_mul_f32 v[38:39], v[24:25], v[24:25]
	v_rcp_f32_e32 v40, v7
	v_fmamk_f32 v38, v38, 0xbdd2d3e8, v100
	v_fmamk_f32 v39, v39, 0xbdd2d3e8, v100
	v_mul_f32_e32 v38, v24, v38
	v_mul_f32_e32 v39, v25, v39
	v_exp_f32_e32 v38, v38
	v_exp_f32_e32 v39, v39
	v_add_f32_e32 v7, 1.0, v21
	v_mov_b32_e32 v21, v86
	v_add_f32_e32 v38, 1.0, v38
	v_add_f32_e32 v39, 1.0, v39
	v_rcp_f32_e32 v38, v38
	v_rcp_f32_e32 v39, v39
	v_rcp_f32_e32 v41, v7
	v_pk_mul_f32 v[24:25], v[24:25], v[38:39]
	s_nop 0
	s_nop 0
	v_lshl_add_u32 v7, v21, 2, v102
	v_add_u32_e32 v54, 0x420, v7
	v_add_u32_e32 v48, 0x428, v7

.Lw2b20:
	v_add_u32_e32 v52, 0x430, v7
	ds_read2_b32 v[38:39], v7 offset0:138 offset1:139
	ds_read2_b32 v[42:43], v7 offset0:142 offset1:143
	ds_read2_b32 v[44:45], v7 offset0:140 offset1:141
	ds_read2_b32 v[46:47], v7 offset0:136 offset1:137
	v_add_u32_e32 v7, 0x438, v7
	ds_read2_b32 v[48:49], v48 offset1:1
	ds_read2_b32 v[50:51], v7 offset1:1
	ds_read2_b32 v[52:53], v52 offset1:1
	ds_read2_b32 v[54:55], v54 offset1:1
	v_cvt_pk_f16_f32 v7, v8, v9
	v_pk_mul_f32 v[8:9], v[14:15], v[40:41]
	s_nop 0
	v_cvt_pk_f16_f32 v8, v8, v9
	v_pk_mul_f32 v[14:15], v[20:21], v[36:37] op_sel_hi:[0,1]
	s_waitcnt lgkmcnt(0)

.Lw2b21:
	v_pk_fma_f32 v[14:15], v[46:47], v[14:15], v[54:55]
	v_pk_mul_f32 v[22:23], v[20:21], v[22:23] op_sel_hi:[0,1]
	v_pk_mul_f32 v[28:29], v[14:15], v[14:15]
	v_pk_fma_f32 v[22:23], v[38:39], v[22:23], v[48:49]
	v_fmamk_f32 v9, v28, 0xbdd2d3e8, v100
	v_mul_f32_e32 v9, v14, v9
	v_fmamk_f32 v28, v29, 0xbdd2d3e8, v100
	v_exp_f32_e32 v9, v9
	v_mul_f32_e32 v28, v15, v28
	v_exp_f32_e32 v29, v28
	v_pk_mul_f32 v[36:37], v[22:23], v[22:23]
	v_add_f32_e32 v9, 1.0, v9
	v_rcp_f32_e32 v28, v9
	v_add_f32_e32 v9, 1.0, v29
	v_rcp_f32_e32 v29, v9
	v_fmamk_f32 v9, v36, 0xbdd2d3e8, v100
	v_mul_f32_e32 v9, v22, v9
	v_exp_f32_e32 v36, v9
	v_cvt_pk_f16_f32 v9, v24, v25
	v_fmamk_f32 v24, v37, 0xbdd2d3e8, v100
	v_pk_mul_f32 v[16:17], v[20:21], v[16:17] op_sel_hi:[0,1]

.Lw2b22:
	v_mul_f32_e32 v24, v23, v24
	v_pk_fma_f32 v[16:17], v[44:45], v[16:17], v[52:53]
	v_pk_mul_f32 v[14:15], v[14:15], v[28:29]
	v_exp_f32_e32 v29, v24
	v_pk_mul_f32 v[24:25], v[16:17], v[16:17]
	v_cvt_pk_f16_f32 v14, v14, v15
	v_fmamk_f32 v24, v24, 0xbdd2d3e8, v100
	v_mul_f32_e32 v24, v16, v24
	v_exp_f32_e32 v24, v24
	v_add_f32_e32 v15, 1.0, v36
	v_rcp_f32_e32 v28, v15
	v_add_f32_e32 v15, 1.0, v29
	v_rcp_f32_e32 v29, v15
	v_add_f32_e32 v15, 1.0, v24
	v_fmamk_f32 v24, v25, 0xbdd2d3e8, v100
	v_mul_f32_e32 v36, v17, v24
	v_pk_mul_f32 v[24:25], v[20:21], v[34:35] op_sel_hi:[0,1]
	v_pk_fma_f32 v[24:25], v[42:43], v[24:25], v[50:51]
	v_exp_f32_e32 v37, v36
	v_pk_mul_f32 v[34:35], v[24:25], v[24:25]
	v_rcp_f32_e32 v36, v15

.Lw2b23:
	v_fmamk_f32 v34, v34, 0xbdd2d3e8, v100
	v_fmamk_f32 v35, v35, 0xbdd2d3e8, v100
	v_mul_f32_e32 v34, v24, v34
	v_mul_f32_e32 v35, v25, v35
	v_exp_f32_e32 v34, v34
	v_exp_f32_e32 v35, v35
	v_add_f32_e32 v15, 1.0, v37
	v_rcp_f32_e32 v37, v15
	v_add_f32_e32 v34, 1.0, v34
	v_add_f32_e32 v35, 1.0, v35
	v_rcp_f32_e32 v34, v34
	v_rcp_f32_e32 v35, v35
	v_pk_mul_f32 v[22:23], v[22:23], v[28:29]
	v_pk_mul_f32 v[16:17], v[16:17], v[36:37]
	v_pk_mul_f32 v[24:25], v[24:25], v[34:35]
	s_nop 0
	v_cvt_pk_f16_f32 v16, v16, v17
	v_lshl_add_u32 v15, v21, 2, v102
	v_add_u32_e32 v50, 0x440, v15
	v_add_u32_e32 v44, 0x448, v15
	v_add_u32_e32 v48, 0x450, v15

.Lw2b24:
	ds_read2_b32 v[34:35], v15 offset0:146 offset1:147
	ds_read2_b32 v[38:39], v15 offset0:150 offset1:151
	ds_read2_b32 v[40:41], v15 offset0:148 offset1:149
	ds_read2_b32 v[42:43], v15 offset0:144 offset1:145
	v_add_u32_e32 v15, 0x458, v15
	ds_read2_b32 v[44:45], v44 offset1:1
	ds_read2_b32 v[46:47], v15 offset1:1
	ds_read2_b32 v[48:49], v48 offset1:1
	ds_read2_b32 v[50:51], v50 offset1:1
	v_cvt_pk_f16_f32 v15, v22, v23
	v_pk_mul_f32 v[12:13], v[20:21], v[12:13] op_sel_hi:[0,1]
	s_waitcnt lgkmcnt(0)
	v_pk_fma_f32 v[12:13], v[42:43], v[12:13], v[50:51]
	v_pk_mul_f32 v[28:29], v[20:21], v[30:31] op_sel_hi:[0,1]
	v_pk_mul_f32 v[22:23], v[12:13], v[12:13]
	v_pk_fma_f32 v[28:29], v[34:35], v[28:29], v[44:45]

.Lw2b25:
	v_fmamk_f32 v17, v22, 0xbdd2d3e8, v100
	v_mul_f32_e32 v17, v12, v17
	v_fmamk_f32 v22, v23, 0xbdd2d3e8, v100
	v_exp_f32_e32 v17, v17
	v_mul_f32_e32 v22, v13, v22
	v_exp_f32_e32 v23, v22
	v_pk_mul_f32 v[30:31], v[28:29], v[28:29]
	v_add_f32_e32 v17, 1.0, v17
	v_rcp_f32_e32 v22, v17
	v_add_f32_e32 v17, 1.0, v23
	v_rcp_f32_e32 v23, v17
	v_fmamk_f32 v17, v30, 0xbdd2d3e8, v100
	v_mul_f32_e32 v17, v28, v17
	v_exp_f32_e32 v30, v17
	v_pk_mul_f32 v[12:13], v[12:13], v[22:23]
	v_cvt_pk_f16_f32 v17, v24, v25
	v_cvt_pk_f16_f32 v22, v12, v13
	v_fmamk_f32 v12, v31, 0xbdd2d3e8, v100
	v_mul_f32_e32 v12, v29, v12
	v_exp_f32_e32 v31, v12
	v_pk_mul_f32 v[12:13], v[20:21], v[32:33] op_sel_hi:[0,1]
	v_pk_fma_f32 v[12:13], v[40:41], v[12:13], v[48:49]

.Lw2b26:
	v_add_f32_e32 v23, 1.0, v30
	v_pk_mul_f32 v[24:25], v[12:13], v[12:13]
	v_rcp_f32_e32 v30, v23
	v_fmamk_f32 v24, v24, 0xbdd2d3e8, v100
	v_mul_f32_e32 v24, v12, v24
	v_exp_f32_e32 v24, v24
	v_add_f32_e32 v23, 1.0, v31
	v_pk_mul_f32 v[10:11], v[20:21], v[10:11] op_sel_hi:[0,1]
	v_rcp_f32_e32 v31, v23
	v_add_f32_e32 v23, 1.0, v24
	v_fmamk_f32 v24, v25, 0xbdd2d3e8, v100
	v_pk_fma_f32 v[10:11], v[38:39], v[10:11], v[46:47]
	v_mul_f32_e32 v32, v13, v24
	v_pk_mul_f32 v[24:25], v[10:11], v[10:11]
	v_exp_f32_e32 v33, v32
	v_fmamk_f32 v24, v24, 0xbdd2d3e8, v100
	v_fmamk_f32 v25, v25, 0xbdd2d3e8, v100
	v_mul_f32_e32 v24, v10, v24
	v_mul_f32_e32 v25, v11, v25
	v_exp_f32_e32 v24, v24
	v_exp_f32_e32 v25, v25
	v_rcp_f32_e32 v32, v23

.Lw2b27:
	v_add_f32_e32 v23, 1.0, v33
	v_add_f32_e32 v24, 1.0, v24
	v_add_f32_e32 v25, 1.0, v25
	v_rcp_f32_e32 v24, v24
	v_rcp_f32_e32 v25, v25
	v_rcp_f32_e32 v33, v23
	v_pk_mul_f32 v[10:11], v[10:11], v[24:25]
	s_nop 0
	v_pk_mul_f32 v[12:13], v[12:13], v[32:33]
	v_lshl_add_u32 v21, v21, 2, v102
	v_add_u32_e32 v24, 0x468, v21
	ds_read2_b32 v[34:35], v21 offset0:154 offset1:155
	ds_read2_b32 v[36:37], v21 offset0:158 offset1:159
	ds_read2_b32 v[38:39], v21 offset0:156 offset1:157
	ds_read2_b32 v[40:41], v21 offset0:152 offset1:153
	v_add_u32_e32 v23, 0x460, v21
	v_add_u32_e32 v25, 0x470, v21
	v_add_u32_e32 v21, 0x478, v21
	ds_read2_b32 v[42:43], v24 offset1:1

.Lw2b28:
	ds_read2_b32 v[44:45], v21 offset1:1
	ds_read2_b32 v[46:47], v25 offset1:1
	ds_read2_b32 v[48:49], v23 offset1:1
	v_pk_mul_f32 v[24:25], v[28:29], v[30:31]
	s_nop 0
	v_cvt_pk_f16_f32 v23, v24, v25
	v_cvt_pk_f16_f32 v24, v12, v13
	v_pk_mul_f32 v[4:5], v[20:21], v[4:5] op_sel_hi:[0,1]
	s_waitcnt lgkmcnt(0)
	v_pk_fma_f32 v[4:5], v[40:41], v[4:5], v[48:49]
	ds_write_b128 v125, v[6:9]
	v_pk_mul_f32 v[12:13], v[4:5], v[4:5]
	v_pk_mul_f32 v[0:1], v[20:21], v[0:1] op_sel_hi:[0,1]
	v_fmamk_f32 v12, v12, 0xbdd2d3e8, v100
	v_fmamk_f32 v13, v13, 0xbdd2d3e8, v100
	v_mul_f32_e32 v12, v4, v12
	v_mul_f32_e32 v13, v5, v13
	v_exp_f32_e32 v12, v12

.Lw2b29:
	v_exp_f32_e32 v13, v13
	v_pk_fma_f32 v[0:1], v[38:39], v[0:1], v[46:47]
	v_cvt_pk_f16_f32 v25, v10, v11
	v_add_f32_e32 v6, 1.0, v12
	v_add_f32_e32 v7, 1.0, v13
	v_rcp_f32_e32 v6, v6
	v_rcp_f32_e32 v7, v7
	v_pk_mul_f32 v[10:11], v[0:1], v[0:1]
	v_pk_mul_f32 v[2:3], v[20:21], v[2:3] op_sel_hi:[0,1]
	v_pk_fma_f32 v[2:3], v[36:37], v[2:3], v[44:45]
	v_pk_mul_f32 v[4:5], v[4:5], v[6:7]
	v_pk_mul_f32 v[6:7], v[20:21], v[18:19] op_sel_hi:[0,1]
	v_pk_fma_f32 v[6:7], v[34:35], v[6:7], v[42:43]
	v_cvt_pk_f16_f32 v4, v4, v5
	v_pk_mul_f32 v[8:9], v[6:7], v[6:7]
	s_mov_b64 s[4:5], 0
	v_fmamk_f32 v8, v8, 0xbdd2d3e8, v100
	v_mul_f32_e32 v8, v6, v8
	v_fmamk_f32 v9, v9, 0xbdd2d3e8, v100

.Lw2b30:
	v_exp_f32_e32 v8, v8
	v_mul_f32_e32 v9, v7, v9
	v_exp_f32_e32 v9, v9
	ds_write_b128 v125, v[14:17] offset:16
	v_add_f32_e32 v5, 1.0, v8
	v_rcp_f32_e32 v8, v5
	v_add_f32_e32 v5, 1.0, v9
	v_rcp_f32_e32 v9, v5
	v_fmamk_f32 v5, v10, 0xbdd2d3e8, v100
	v_mul_f32_e32 v5, v0, v5
	v_fmamk_f32 v10, v11, 0xbdd2d3e8, v100
	v_exp_f32_e32 v5, v5
	v_mul_f32_e32 v10, v1, v10
	v_exp_f32_e32 v10, v10
	v_pk_mul_f32 v[6:7], v[6:7], v[8:9]
	v_add_f32_e32 v5, 1.0, v5
	v_rcp_f32_e32 v8, v5
	v_add_f32_e32 v5, 1.0, v10
	v_pk_mul_f32 v[10:11], v[2:3], v[2:3]
	ds_write_b128 v125, v[22:25] offset:32
	v_fmamk_f32 v9, v10, 0xbdd2d3e8, v100
	v_mul_f32_e32 v9, v2, v9
	v_exp_f32_e32 v10, v9
	v_fmamk_f32 v9, v11, 0xbdd2d3e8, v100

.Lw2b31:
	v_mul_f32_e32 v9, v3, v9
	v_exp_f32_e32 v11, v9
	v_rcp_f32_e32 v9, v5
	v_add_f32_e32 v5, 1.0, v10
	v_rcp_f32_e32 v10, v5
	v_add_f32_e32 v5, 1.0, v11
	v_rcp_f32_e32 v11, v5
	v_pk_mul_f32 v[0:1], v[0:1], v[8:9]
	v_cvt_pk_f16_f32 v5, v6, v7
	v_cvt_pk_f16_f32 v6, v0, v1
	v_pk_mul_f32 v[0:1], v[2:3], v[10:11]
	s_nop 0
	v_cvt_pk_f16_f32 v7, v0, v1
	ds_write_b128 v125, v[4:7] offset:48
	ds_read_b128 v[4:7], v126
	ds_read_b128 v[8:11], v126 offset:1088
	ds_read_b128 v[12:15], v126 offset:2176
	ds_read_b128 v[16:19], v126 offset:3264
	s_cmp_lg_u32 s47, 0
	s_waitcnt lgkmcnt(0)
	s_cbranch_scc1 .Lh1_wt

.LBB2_9:
	v_mov_b32_e32 v0, 0
	s_and_saveexec_b64 s[4:5], s[0:1]
	s_cbranch_execz .LBB2_13
	s_mov_b64 s[14:15], exec
	v_mbcnt_lo_u32_b32 v0, s14, 0
	v_mbcnt_hi_u32_b32 v0, s15, v0
	v_cmp_eq_u32_e32 vcc, 0, v0
	s_and_saveexec_b64 s[10:11], vcc
	s_bcnt1_i32_b64 s12, s[14:15]

.Lw2b33:
	v_mov_b32_e32 v1, s12
	ds_add_rtn_u32 v1, v96, v1
	s_or_b64 exec, exec, s[10:11]
	s_waitcnt lgkmcnt(0)
	v_readfirstlane_b32 s10, v1
	s_nop 1
	v_add_u32_e32 v0, s10, v0
.LBB2_13:
	s_or_b64 exec, exec, s[4:5]
	v_readfirstlane_b32 s4, v0
	s_waitcnt lgkmcnt(0)
	s_mul_i32 s10, s4, s3
	s_add_i32 s10, s10, s2
	s_cmpk_gt_i32 s10, 0x1869
	s_mov_b64 s[4:5], -1
	s_cbranch_scc1 .LBB2_8
	ds_read_b128 v[28:31], v97
	ds_read_b128 v[24:27], v97 offset:16
	ds_read_b128 v[20:23], v97 offset:32
	ds_read_b128 v[16:19], v97 offset:48
	ds_read_b128 v[12:15], v97 offset:64
	ds_read_b128 v[8:11], v97 offset:80
	ds_read_b128 v[4:7], v97 offset:96
	ds_read_b128 v[0:3], v97 offset:112

.LBB2_15:
	s_or_b64 exec, exec, s[14:15]
	v_mov_b32_e32 v48, v77
	ds_read_b128 v[32:35], v98
	ds_read_b128 v[36:39], v98 offset:64
	ds_read_b128 v[40:43], v98 offset:128
	ds_read_b128 v[44:47], v98 offset:192
	s_nop 0
	v_lshlrev_b32_e32 v48, 4, v48
	v_lshl_add_u32 v103, s5, 15, v48
	ds_read_b128 v[48:51], v103
	ds_read_b128 v[52:55], v103 offset:1024
	ds_read_b128 v[56:59], v103 offset:2048
	ds_read_b128 v[60:63], v103 offset:3072
	ds_read_b128 v[64:67], v103 offset:4096

.Lw2b35:
	ds_read_b128 v[68:71], v103 offset:5120
	ds_read_b128 v[104:107], v103 offset:6144
	ds_read_b128 v[108:111], v103 offset:7168
	s_waitcnt lgkmcnt(7)
	v_mfma_f32_16x16x32_f16 v[28:31], v[48:51], v[32:35], v[28:31]
	s_waitcnt lgkmcnt(6)
	v_mfma_f32_16x16x32_f16 v[24:27], v[52:55], v[32:35], v[24:27]
	s_waitcnt lgkmcnt(5)
	v_mfma_f32_16x16x32_f16 v[20:23], v[56:59], v[32:35], v[20:23]
	s_waitcnt lgkmcnt(4)
	v_mfma_f32_16x16x32_f16 v[16:19], v[60:63], v[32:35], v[16:19]
	ds_read_b128 v[48:51], v103 offset:8192
	ds_read_b128 v[52:55], v103 offset:9216
	ds_read_b128 v[56:59], v103 offset:10240
	ds_read_b128 v[60:63], v103 offset:11264
	s_waitcnt lgkmcnt(7)
	v_mfma_f32_16x16x32_f16 v[12:15], v[64:67], v[32:35], v[12:15]
	s_waitcnt lgkmcnt(6)

.Lw2b36:
	v_mfma_f32_16x16x32_f16 v[8:11], v[68:71], v[32:35], v[8:11]
	s_waitcnt lgkmcnt(5)
	v_mfma_f32_16x16x32_f16 v[4:7], v[104:107], v[32:35], v[4:7]
	s_waitcnt lgkmcnt(4)
	v_mfma_f32_16x16x32_f16 v[0:3], v[108:111], v[32:35], v[0:3]
	ds_read_b128 v[32:35], v103 offset:12288
	ds_read_b128 v[64:67], v103 offset:13312
	ds_read_b128 v[68:71], v103 offset:14336
	ds_read_b128 v[104:107], v103 offset:15360
	s_waitcnt lgkmcnt(7)
	v_mfma_f32_16x16x32_f16 v[28:31], v[48:51], v[36:39], v[28:31]
	s_waitcnt lgkmcnt(6)
	v_mfma_f32_16x16x32_f16 v[24:27], v[52:55], v[36:39], v[24:27]
	s_waitcnt lgkmcnt(5)
	v_mfma_f32_16x16x32_f16 v[20:23], v[56:59], v[36:39], v[20:23]
	s_waitcnt lgkmcnt(4)
	v_mfma_f32_16x16x32_f16 v[16:19], v[60:63], v[36:39], v[16:19]
	ds_read_b128 v[48:51], v103 offset:16384
	ds_read_b128 v[52:55], v103 offset:17408

.Lw2b37:
	ds_read_b128 v[56:59], v103 offset:18432
	ds_read_b128 v[60:63], v103 offset:19456
	s_waitcnt lgkmcnt(7)
	v_mfma_f32_16x16x32_f16 v[12:15], v[32:35], v[36:39], v[12:15]
	s_waitcnt lgkmcnt(6)
	v_mfma_f32_16x16x32_f16 v[8:11], v[64:67], v[36:39], v[8:11]
	s_waitcnt lgkmcnt(5)
	v_mfma_f32_16x16x32_f16 v[4:7], v[68:71], v[36:39], v[4:7]
	s_waitcnt lgkmcnt(4)
	v_mfma_f32_16x16x32_f16 v[0:3], v[104:107], v[36:39], v[0:3]
	ds_read_b128 v[32:35], v103 offset:20480
	ds_read_b128 v[36:39], v103 offset:21504
	ds_read_b128 v[64:67], v103 offset:22528
	ds_read_b128 v[68:71], v103 offset:23552
	s_waitcnt lgkmcnt(7)
	v_mfma_f32_16x16x32_f16 v[28:31], v[48:51], v[40:43], v[28:31]
	s_waitcnt lgkmcnt(6)
	v_mfma_f32_16x16x32_f16 v[24:27], v[52:55], v[40:43], v[24:27]

.Lw2b38:
	s_waitcnt lgkmcnt(5)
	v_mfma_f32_16x16x32_f16 v[20:23], v[56:59], v[40:43], v[20:23]
	s_waitcnt lgkmcnt(4)
	v_mfma_f32_16x16x32_f16 v[16:19], v[60:63], v[40:43], v[16:19]
	ds_read_b128 v[48:51], v103 offset:24576
	ds_read_b128 v[52:55], v103 offset:25600
	ds_read_b128 v[56:59], v103 offset:26624
	ds_read_b128 v[60:63], v103 offset:27648
	s_waitcnt lgkmcnt(7)
	v_mfma_f32_16x16x32_f16 v[12:15], v[32:35], v[40:43], v[12:15]
	s_waitcnt lgkmcnt(6)
	v_mfma_f32_16x16x32_f16 v[8:11], v[36:39], v[40:43], v[8:11]
	s_waitcnt lgkmcnt(5)
	v_mfma_f32_16x16x32_f16 v[4:7], v[64:67], v[40:43], v[4:7]
	s_waitcnt lgkmcnt(4)
	v_mfma_f32_16x16x32_f16 v[0:3], v[68:71], v[40:43], v[0:3]
	ds_read_b128 v[32:35], v103 offset:28672
	ds_read_b128 v[36:39], v103 offset:29696
	ds_read_b128 v[40:43], v103 offset:30720

.Lw2b39:
	ds_read_b128 v[64:67], v103 offset:31744
	s_waitcnt lgkmcnt(7)
	v_mfma_f32_16x16x32_f16 v[28:31], v[48:51], v[44:47], v[28:31]
	s_waitcnt lgkmcnt(6)
	v_mfma_f32_16x16x32_f16 v[24:27], v[52:55], v[44:47], v[24:27]
	s_waitcnt lgkmcnt(5)
	v_mfma_f32_16x16x32_f16 v[20:23], v[56:59], v[44:47], v[20:23]
	s_waitcnt lgkmcnt(4)
	v_mfma_f32_16x16x32_f16 v[16:19], v[60:63], v[44:47], v[16:19]
	s_waitcnt lgkmcnt(3)
	v_mfma_f32_16x16x32_f16 v[12:15], v[32:35], v[44:47], v[12:15]
	s_waitcnt lgkmcnt(2)
	v_mfma_f32_16x16x32_f16 v[8:11], v[36:39], v[44:47], v[8:11]
	s_waitcnt lgkmcnt(1)
	v_mfma_f32_16x16x32_f16 v[4:7], v[40:43], v[44:47], v[4:7]
	s_waitcnt lgkmcnt(0)
	v_mfma_f32_16x16x32_f16 v[0:3], v[64:67], v[44:47], v[0:3]
	s_mov_b32 s5, 1
	s_mov_b64 s[18:19], 0
	s_and_b64 vcc, exec, s[10:11]
	s_cbranch_vccnz .LBB2_7

.Lw2b40:
	s_mul_i32 s12, s5, 0x186a1
	v_lshl_add_u64 v[32:33], s[12:13], 2, v[80:81]
	global_load_dword v113, v[32:33], off
	global_load_dword v103, v[32:33], off offset:16
	s_mov_b32 s14, s13
	s_mov_b32 s15, s13
	s_mul_i32 s12, s5, 0xc3500
	s_lshl_b64 s[10:11], s[12:13], 2
	s_mov_b32 s12, s13
	v_mov_b64_e32 v[34:35], s[14:15]
	v_mov_b64_e32 v[32:33], s[12:13]
	s_add_u32 s16, s6, s10
	ds_write_b128 v85, v[32:35]
	ds_write_b128 v85, v[32:35] offset:16
	ds_write_b128 v85, v[32:35] offset:32
	ds_write_b128 v85, v[32:35] offset:48
	s_addc_u32 s17, s7, s11
	v_mov_b32_e32 v116, 0x3f86a0
	s_waitcnt vmcnt(1)
	v_add_u32_e32 v32, v113, v82
	s_waitcnt vmcnt(0)

.Lw2b41:
	v_cmp_lt_i32_e32 vcc, v32, v103
	s_and_saveexec_b64 s[10:11], vcc
	s_cbranch_execz .LBB2_18
	v_ashrrev_i32_e32 v33, 31, v32
	v_lshl_add_u64 v[32:33], v[32:33], 2, s[16:17]
	global_load_dword v116, v[32:33], off

.Lw2b42:
	v_mov_b32_e32 v112, v56
	v_mov_b32_e32 v107, v115
	v_cmp_lt_i32_e32 vcc, v113, v103
	s_cbranch_vccz .LBB2_19
	v_or_b32_e32 v32, 4, v84
	s_waitcnt vmcnt(0)
	ds_bpermute_b32 v66, v84, v116
	ds_bpermute_b32 v123, v32, v116
	v_or_b32_e32 v32, 8, v84
	v_or_b32_e32 v34, 12, v84
	ds_bpermute_b32 v122, v32, v116
	ds_bpermute_b32 v121, v34, v116
	v_or_b32_e32 v34, 16, v84
	ds_bpermute_b32 v120, v34, v116
	v_or_b32_e32 v34, 20, v84
	ds_bpermute_b32 v119, v34, v116
	s_waitcnt lgkmcnt(5)
	v_lshlrev_b32_e32 v32, 8, v66
	s_waitcnt lgkmcnt(4)
	v_lshlrev_b32_e32 v33, 8, v123
	v_or_b32_e32 v34, 24, v84
	v_and_or_b32 v32, v32, s21, v83
	v_and_or_b32 v33, v33, s21, v83

.Lw2b43:
	ds_bpermute_b32 v118, v34, v116
	ds_bpermute_b32 v117, v87, v116
	global_load_dwordx4 v[60:63], v32, s[8:9]
	global_load_dwordx4 v[56:59], v33, s[8:9]
	s_waitcnt lgkmcnt(5)
	v_lshlrev_b32_e32 v32, 8, v122
	s_waitcnt lgkmcnt(4)
	v_lshlrev_b32_e32 v33, 8, v121
	v_and_or_b32 v32, v32, s21, v83
	v_and_or_b32 v33, v33, s21, v83
	global_load_dwordx4 v[52:55], v32, s[8:9]
	global_load_dwordx4 v[48:51], v33, s[8:9]
	s_waitcnt lgkmcnt(3)
	v_lshlrev_b32_e32 v32, 8, v120
	s_waitcnt lgkmcnt(2)
	v_lshlrev_b32_e32 v33, 8, v119
	v_and_or_b32 v32, v32, s21, v83
	v_and_or_b32 v33, v33, s21, v83
	global_load_dwordx4 v[44:47], v32, s[8:9]
	global_load_dwordx4 v[40:43], v33, s[8:9]

.Lw2b44:
	s_waitcnt lgkmcnt(1)
	v_lshlrev_b32_e32 v32, 8, v118
	s_waitcnt lgkmcnt(0)
	v_lshlrev_b32_e32 v33, 8, v117
	v_and_or_b32 v32, v32, s21, v83
	v_and_or_b32 v33, v33, s21, v83
	global_load_dwordx4 v[36:39], v32, s[8:9]
	s_nop 0
	global_load_dwordx4 v[32:35], v33, s[8:9]
	v_or_b32_e32 v64, 16, v82
	v_add_u32_e32 v64, v64, v113
	v_cmp_lt_i32_e32 vcc, v64, v103
	v_mov_b32_e32 v114, 0x3f86a0
	s_and_saveexec_b64 s[14:15], vcc
	s_cbranch_execz .LBB2_23
	v_ashrrev_i32_e32 v65, 31, v64
	v_lshl_add_u64 v[64:65], v[64:65], 2, s[16:17]
	global_load_dword v114, v[64:65], off
.LBB2_23:
	s_or_b64 exec, exec, s[14:15]
	v_ashrrev_i32_e32 v124, 17, v66
	v_cmp_ne_u32_e32 vcc, v124, v107
	s_cmp_lg_u64 vcc, 0
	s_cselect_b64 s[14:15], -1, 0
.Lw2t45:
	s_cbranch_execz .Lw2c45
.Lw2b45:
	s_and_b64 s[18:19], s[14:15], vcc
	v_mov_b32_e32 v115, v107
	v_mov_b32_e32 v68, v112
	v_mov_b32_e32 v69, v110
	v_mov_b32_e32 v70, v111
	v_mov_b32_e32 v71, v109
	v_mov_b32_e32 v64, v108
	v_mov_b32_e32 v65, v105
	v_mov_b32_e32 v66, v106
	v_mov_b32_e32 v67, v104
	s_and_saveexec_b64 s[14:15], s[18:19]
	s_cbranch_execz .LBB2_27
	v_cmp_gt_i32_e32 vcc, 16, v107
	s_and_saveexec_b64 s[18:19], vcc
	s_cbranch_execz .LBB2_26
	v_cvt_pk_f16_f32 v67, v111, v109
	v_cvt_pk_f16_f32 v66, v112, v110
	v_cvt_pk_f16_f32 v65, v106, v104
	v_cvt_pk_f16_f32 v64, v108, v105
	v_mad_u64_u32 v[68:69], s[24:25], v107, s20, v[76:77]
	ds_write_b128 v68, v[64:67]
.LBB2_26:
	s_or_b64 exec, exec, s[18:19]
	v_mov_b32_e32 v68, 0
	v_mov_b32_e32 v115, v124
	v_mov_b32_e32 v69, v68
.Lw2t46:
	s_cbranch_execz .Lw2c46
.Lw2b46:
	v_mov_b32_e32 v70, v68
	v_mov_b32_e32 v71, v68
	v_mov_b32_e32 v64, v68
	v_mov_b32_e32 v65, v68
	v_mov_b32_e32 v66, v68
	v_mov_b32_e32 v67, v68
.LBB2_27:
	s_or_b64 exec, exec, s[14:15]
	v_ashrrev_i32_e32 v123, 17, v123
	s_waitcnt vmcnt(7)
	v_mfma_f32_16x16x16_f16 v[64:67], v[72:73], v[60:61], v[64:67]
	v_cmp_ne_u32_e32 vcc, v123, v115
	s_cmp_lg_u64 vcc, 0
	s_cselect_b64 s[14:15], -1, 0
	v_mfma_f32_16x16x16_f16 v[60:63], v[72:73], v[62:63], v[68:71]
	s_and_b64 s[18:19], s[14:15], vcc
	s_and_saveexec_b64 s[14:15], s[18:19]
	s_cbranch_execz .LBB2_31
	v_cmp_gt_i32_e32 vcc, 16, v115
	s_and_saveexec_b64 s[18:19], vcc
	s_cbranch_execz .LBB2_30
	s_nop 1
	v_cvt_pk_f16_f32 v63, v62, v63
	v_cvt_pk_f16_f32 v62, v60, v61
	v_cvt_pk_f16_f32 v61, v66, v67
	v_cvt_pk_f16_f32 v60, v64, v65

.LBB2_31:
	s_or_b64 exec, exec, s[14:15]
	v_ashrrev_i32_e32 v68, 17, v122
	s_waitcnt vmcnt(6)
	v_mfma_f32_16x16x16_f16 v[64:67], v[72:73], v[56:57], v[64:67]
	v_cmp_ne_u32_e32 vcc, v68, v115
	s_cmp_lg_u64 vcc, 0
	s_cselect_b64 s[14:15], -1, 0
	v_mfma_f32_16x16x16_f16 v[56:59], v[72:73], v[58:59], v[60:63]
	s_and_b64 s[18:19], s[14:15], vcc
	s_and_saveexec_b64 s[14:15], s[18:19]
	s_cbranch_execz .LBB2_35
	v_cmp_gt_i32_e32 vcc, 16, v115
	s_and_saveexec_b64 s[18:19], vcc
	s_cbranch_execz .LBB2_34

.Lw2b48:
	s_nop 1
	v_cvt_pk_f16_f32 v59, v58, v59
	v_cvt_pk_f16_f32 v58, v56, v57
	v_cvt_pk_f16_f32 v57, v66, v67
	v_cvt_pk_f16_f32 v56, v64, v65
	v_mad_u64_u32 v[60:61], s[24:25], v115, s20, v[76:77]
	ds_write_b128 v60, v[56:59]

.Lw2b49:
	v_mfma_f32_16x16x16_f16 v[52:55], v[72:73], v[54:55], v[56:59]
	s_and_b64 s[18:19], s[14:15], vcc
	s_and_saveexec_b64 s[14:15], s[18:19]
	s_cbranch_execz .LBB2_39
	v_cmp_gt_i32_e32 vcc, 16, v115
	s_and_saveexec_b64 s[18:19], vcc
	s_cbranch_execz .LBB2_38
	s_nop 1
	v_cvt_pk_f16_f32 v55, v54, v55
	v_cvt_pk_f16_f32 v54, v52, v53
	v_cvt_pk_f16_f32 v53, v62, v63
	v_cvt_pk_f16_f32 v52, v60, v61
	v_mad_u64_u32 v[56:57], s[24:25], v115, s20, v[76:77]
	ds_write_b128 v56, v[52:55]
.LBB2_38:
	s_or_b64 exec, exec, s[18:19]
	s_nop 0
	v_mov_b32_e32 v52, 0
	v_mov_b32_e32 v115, v68
	v_mov_b32_e32 v53, v52
	v_mov_b32_e32 v54, v52
	v_mov_b32_e32 v55, v52
	v_mov_b32_e32 v60, v52
	v_mov_b32_e32 v61, v52

.LBB2_43:
	s_or_b64 exec, exec, s[14:15]
	v_ashrrev_i32_e32 v60, 17, v119
	s_waitcnt vmcnt(3)
	v_mfma_f32_16x16x16_f16 v[52:55], v[72:73], v[44:45], v[56:59]
	v_cmp_ne_u32_e32 vcc, v60, v115
	s_cmp_lg_u64 vcc, 0
	s_cselect_b64 s[14:15], -1, 0
	v_mfma_f32_16x16x16_f16 v[44:47], v[72:73], v[46:47], v[48:51]
	s_and_b64 s[18:19], s[14:15], vcc
	s_and_saveexec_b64 s[14:15], s[18:19]
	s_cbranch_execz .LBB2_47
	v_cmp_gt_i32_e32 vcc, 16, v115
	s_and_saveexec_b64 s[18:19], vcc
	s_cbranch_execz .LBB2_46
	s_nop 1
	v_cvt_pk_f16_f32 v47, v46, v47
	v_cvt_pk_f16_f32 v46, v44, v45

.Lw2b53:
	s_and_saveexec_b64 s[14:15], s[18:19]
	s_cbranch_execz .LBB2_51
	v_cmp_gt_i32_e32 vcc, 16, v115
	s_and_saveexec_b64 s[18:19], vcc
	s_cbranch_execz .LBB2_50
	s_nop 1
	v_cvt_pk_f16_f32 v43, v42, v43
	v_cvt_pk_f16_f32 v42, v40, v41
	v_cvt_pk_f16_f32 v41, v50, v51
	v_cvt_pk_f16_f32 v40, v48, v49
	v_mad_u64_u32 v[44:45], s[24:25], v115, s20, v[76:77]
	ds_write_b128 v44, v[40:43]

.LBB2_51:
	s_or_b64 exec, exec, s[14:15]
	v_ashrrev_i32_e32 v52, 17, v117
.Lw2t54:
	s_cbranch_execz .Lw2c54
.Lw2b54:
	s_waitcnt vmcnt(1)
	v_mfma_f32_16x16x16_f16 v[44:47], v[72:73], v[36:37], v[48:51]
	v_cmp_ne_u32_e32 vcc, v52, v115
	s_cmp_lg_u64 vcc, 0
	s_cselect_b64 s[14:15], -1, 0
	v_mfma_f32_16x16x16_f16 v[36:39], v[72:73], v[38:39], v[40:43]
	s_and_b64 s[18:19], s[14:15], vcc
	s_and_saveexec_b64 s[14:15], s[18:19]
	s_cbranch_execz .LBB2_55
	v_cmp_gt_i32_e32 vcc, 16, v115
	s_and_saveexec_b64 s[18:19], vcc
	s_cbranch_execz .LBB2_54
	s_nop 1
	v_cvt_pk_f16_f32 v39, v38, v39
	v_cvt_pk_f16_f32 v38, v36, v37
	v_cvt_pk_f16_f32 v37, v46, v47
	v_cvt_pk_f16_f32 v36, v44, v45
	v_mad_u64_u32 v[40:41], s[24:25], v115, s20, v[76:77]
	ds_write_b128 v40, v[36:39]
.LBB2_54:
	s_or_b64 exec, exec, s[18:19]
	s_nop 0
	v_mov_b32_e32 v36, 0
	v_mov_b32_e32 v115, v52
.Lw2t55:
	s_cbranch_execz .Lw2c55

.LBB2_55:
	s_or_b64 exec, exec, s[14:15]
	s_waitcnt vmcnt(0)
	v_mfma_f32_16x16x16_f16 v[60:63], v[72:73], v[32:33], v[44:47]
	v_add_u32_e32 v32, 8, v113
	v_cmp_lt_i32_e32 vcc, v32, v103
	v_mfma_f32_16x16x16_f16 v[56:59], v[72:73], v[34:35], v[36:39]
	s_cbranch_vccz .LBB2_89
	ds_bpermute_b32 v123, v88, v116
	ds_bpermute_b32 v122, v89, v116
	ds_bpermute_b32 v121, v90, v116
	ds_bpermute_b32 v120, v91, v116
	ds_bpermute_b32 v119, v92, v116
	ds_bpermute_b32 v118, v93, v116
	s_waitcnt lgkmcnt(5)
	v_lshlrev_b32_e32 v32, 8, v123
	s_waitcnt lgkmcnt(4)

.Lw2b56:
	v_lshlrev_b32_e32 v33, 8, v122
	v_and_or_b32 v32, v32, s21, v83
	v_and_or_b32 v33, v33, s21, v83
	ds_bpermute_b32 v117, v94, v116
	ds_bpermute_b32 v116, v95, v116
	global_load_dwordx4 v[68:71], v32, s[8:9]
	global_load_dwordx4 v[64:67], v33, s[8:9]
	s_waitcnt lgkmcnt(5)
	v_lshlrev_b32_e32 v32, 8, v121
	s_waitcnt lgkmcnt(4)
	v_lshlrev_b32_e32 v33, 8, v120
	v_and_or_b32 v32, v32, s21, v83
	v_and_or_b32 v33, v33, s21, v83
	global_load_dwordx4 v[52:55], v32, s[8:9]
	global_load_dwordx4 v[48:51], v33, s[8:9]
	s_waitcnt lgkmcnt(3)
	v_lshlrev_b32_e32 v32, 8, v119
	s_waitcnt lgkmcnt(2)
	v_lshlrev_b32_e32 v33, 8, v118
	v_and_or_b32 v32, v32, s21, v83

.Lw2b57:
	v_and_or_b32 v33, v33, s21, v83
	global_load_dwordx4 v[44:47], v32, s[8:9]
	global_load_dwordx4 v[40:43], v33, s[8:9]
	s_waitcnt lgkmcnt(1)
	v_lshlrev_b32_e32 v32, 8, v117
	s_waitcnt lgkmcnt(0)
	v_lshlrev_b32_e32 v33, 8, v116
	v_and_or_b32 v32, v32, s21, v83
	v_and_or_b32 v33, v33, s21, v83
	global_load_dwordx4 v[36:39], v32, s[8:9]
	s_nop 0
	global_load_dwordx4 v[32:35], v33, s[8:9]
	v_ashrrev_i32_e32 v123, 17, v123
	v_cmp_ne_u32_e32 vcc, v123, v115
	s_cmp_lg_u64 vcc, 0
	s_cselect_b64 s[14:15], -1, 0
	s_and_b64 s[18:19], s[14:15], vcc
	s_and_saveexec_b64 s[14:15], s[18:19]
	s_cbranch_execz .LBB2_60
	v_cmp_gt_i32_e32 vcc, 16, v115
	s_and_saveexec_b64 s[18:19], vcc
	s_cbranch_execz .LBB2_59
	v_cvt_pk_f16_f32 v59, v58, v59

.LBB2_60:
	s_or_b64 exec, exec, s[14:15]
	v_ashrrev_i32_e32 v122, 17, v122
	s_waitcnt vmcnt(7)
	v_mfma_f32_16x16x16_f16 v[60:63], v[72:73], v[68:69], v[60:63]
	v_cmp_ne_u32_e32 vcc, v122, v115
	s_cmp_lg_u64 vcc, 0
	s_cselect_b64 s[14:15], -1, 0
	v_mfma_f32_16x16x16_f16 v[56:59], v[72:73], v[70:71], v[56:59]
	s_and_b64 s[18:19], s[14:15], vcc
.Lw2t59:
	s_cbranch_execz .Lw2c59
.Lw2b59:
	s_and_saveexec_b64 s[14:15], s[18:19]
	s_cbranch_execz .LBB2_64
	v_cmp_gt_i32_e32 vcc, 16, v115
	s_and_saveexec_b64 s[18:19], vcc
	s_cbranch_execz .LBB2_63
	s_nop 1
	v_cvt_pk_f16_f32 v59, v58, v59
	v_cvt_pk_f16_f32 v58, v56, v57
	v_cvt_pk_f16_f32 v57, v62, v63
	v_cvt_pk_f16_f32 v56, v60, v61
	v_mad_u64_u32 v[60:61], s[24:25], v115, s20, v[76:77]
	ds_write_b128 v60, v[56:59]

.LBB2_64:
	s_or_b64 exec, exec, s[14:15]
	v_ashrrev_i32_e32 v68, 17, v121
.Lw2t60:
	s_cbranch_execz .Lw2c60
.Lw2b60:
	s_waitcnt vmcnt(6)
	v_mfma_f32_16x16x16_f16 v[60:63], v[72:73], v[64:65], v[60:63]
	v_cmp_ne_u32_e32 vcc, v68, v115
	s_cmp_lg_u64 vcc, 0
	s_cselect_b64 s[14:15], -1, 0
	v_mfma_f32_16x16x16_f16 v[56:59], v[72:73], v[66:67], v[56:59]
	s_and_b64 s[18:19], s[14:15], vcc
	s_and_saveexec_b64 s[14:15], s[18:19]
	s_cbranch_execz .LBB2_68
	v_cmp_gt_i32_e32 vcc, 16, v115
	s_and_saveexec_b64 s[18:19], vcc
	s_cbranch_execz .LBB2_67
	s_nop 1
	v_cvt_pk_f16_f32 v59, v58, v59
	v_cvt_pk_f16_f32 v58, v56, v57
	v_cvt_pk_f16_f32 v57, v62, v63
	v_cvt_pk_f16_f32 v56, v60, v61
	v_mad_u64_u32 v[60:61], s[24:25], v115, s20, v[76:77]
	ds_write_b128 v60, v[56:59]
.LBB2_67:
	s_or_b64 exec, exec, s[18:19]
	s_nop 0
	v_mov_b32_e32 v56, 0
	v_mov_b32_e32 v115, v68
.Lw2t61:
	s_cbranch_execz .Lw2c61
.Lw2b61:
	v_mov_b32_e32 v57, v56
	v_mov_b32_e32 v58, v56
	v_mov_b32_e32 v59, v56
	v_mov_b32_e32 v60, v56
	v_mov_b32_e32 v61, v56
	v_mov_b32_e32 v62, v56
	v_mov_b32_e32 v63, v56
.LBB2_68:
	s_or_b64 exec, exec, s[14:15]
	v_ashrrev_i32_e32 v64, 17, v120
	s_waitcnt vmcnt(5)
	v_mfma_f32_16x16x16_f16 v[60:63], v[72:73], v[52:53], v[60:63]
	v_cmp_ne_u32_e32 vcc, v64, v115
	s_cmp_lg_u64 vcc, 0
	s_cselect_b64 s[14:15], -1, 0
	v_mfma_f32_16x16x16_f16 v[52:55], v[72:73], v[54:55], v[56:59]
	s_and_b64 s[18:19], s[14:15], vcc
	s_and_saveexec_b64 s[14:15], s[18:19]
	s_cbranch_execz .LBB2_72
	v_cmp_gt_i32_e32 vcc, 16, v115
	s_and_saveexec_b64 s[18:19], vcc
	s_cbranch_execz .LBB2_71
	s_nop 1
	v_cvt_pk_f16_f32 v55, v54, v55
	v_cvt_pk_f16_f32 v54, v52, v53
	v_cvt_pk_f16_f32 v53, v62, v63
	v_cvt_pk_f16_f32 v52, v60, v61

.LBB2_72:
	s_or_b64 exec, exec, s[14:15]
	v_ashrrev_i32_e32 v64, 17, v119
	s_waitcnt vmcnt(4)
	v_mfma_f32_16x16x16_f16 v[56:59], v[72:73], v[48:49], v[60:63]
	v_cmp_ne_u32_e32 vcc, v64, v115
	s_cmp_lg_u64 vcc, 0
	s_cselect_b64 s[14:15], -1, 0
	v_mfma_f32_16x16x16_f16 v[48:51], v[72:73], v[50:51], v[52:55]
	s_and_b64 s[18:19], s[14:15], vcc
	s_and_saveexec_b64 s[14:15], s[18:19]
	s_cbranch_execz .LBB2_76
	v_cmp_gt_i32_e32 vcc, 16, v115
	s_and_saveexec_b64 s[18:19], vcc

.Lw2b63:
	s_cbranch_execz .LBB2_75
	s_nop 1
	v_cvt_pk_f16_f32 v51, v50, v51
	v_cvt_pk_f16_f32 v50, v48, v49
	v_cvt_pk_f16_f32 v49, v58, v59
	v_cvt_pk_f16_f32 v48, v56, v57
	v_mad_u64_u32 v[52:53], s[24:25], v115, s20, v[76:77]
	ds_write_b128 v52, v[48:51]

.Lw2b64:
	s_cmp_lg_u64 vcc, 0
	s_cselect_b64 s[14:15], -1, 0
	v_mfma_f32_16x16x16_f16 v[44:47], v[72:73], v[46:47], v[48:51]
	s_and_b64 s[18:19], s[14:15], vcc
	s_and_saveexec_b64 s[14:15], s[18:19]
	s_cbranch_execz .LBB2_80
	v_cmp_gt_i32_e32 vcc, 16, v115
	s_and_saveexec_b64 s[18:19], vcc
	s_cbranch_execz .LBB2_79
	s_nop 1
	v_cvt_pk_f16_f32 v47, v46, v47
	v_cvt_pk_f16_f32 v46, v44, v45
	v_cvt_pk_f16_f32 v45, v54, v55
	v_cvt_pk_f16_f32 v44, v52, v53
	v_mad_u64_u32 v[48:49], s[24:25], v115, s20, v[76:77]
	ds_write_b128 v48, v[44:47]
.LBB2_79:
	s_or_b64 exec, exec, s[18:19]
	s_nop 0
	v_mov_b32_e32 v44, 0
	v_mov_b32_e32 v115, v60
	v_mov_b32_e32 v45, v44
	v_mov_b32_e32 v46, v44
	v_mov_b32_e32 v47, v44
	v_mov_b32_e32 v52, v44

.LBB2_84:
	s_or_b64 exec, exec, s[14:15]
	v_ashrrev_i32_e32 v52, 17, v116
	s_waitcnt vmcnt(1)
	v_mfma_f32_16x16x16_f16 v[44:47], v[72:73], v[36:37], v[48:51]
	v_cmp_ne_u32_e32 vcc, v52, v115
	s_cmp_lg_u64 vcc, 0
	s_cselect_b64 s[14:15], -1, 0
	v_mfma_f32_16x16x16_f16 v[36:39], v[72:73], v[38:39], v[40:43]
	s_and_b64 s[18:19], s[14:15], vcc
	s_and_saveexec_b64 s[14:15], s[18:19]
	s_cbranch_execz .LBB2_88
	v_cmp_gt_i32_e32 vcc, 16, v115
	s_and_saveexec_b64 s[18:19], vcc
	s_cbranch_execz .LBB2_87
	s_nop 1
	v_cvt_pk_f16_f32 v39, v38, v39

.Lw2b67:
	v_cvt_pk_f16_f32 v38, v36, v37
	v_cvt_pk_f16_f32 v37, v46, v47
	v_cvt_pk_f16_f32 v36, v44, v45
	v_mad_u64_u32 v[40:41], s[24:25], v115, s20, v[76:77]
	ds_write_b128 v40, v[36:39]

.Lw3b0:
	s_load_dwordx8 s[4:11], s[0:1], 0x18
	v_lshlrev_b32_e32 v2, 4, v0
	v_min_u32_e32 v1, 0x7f, v0
	v_lshlrev_b32_e32 v26, 2, v1
	v_readfirstlane_b32 s3, v0
	v_add_u32_e32 v28, 0x3400, v2
	v_add_u32_e32 v29, 0x6800, v2
	v_add_u32_e32 v30, 0x9c00, v2
	v_add_u32_e32 v31, 0xd00, v0
	v_min_u32_e32 v31, 0xfff, v31
	v_lshlrev_b32_e32 v31, 4, v31
	v_add_u32_e32 v27, 0x680, v0
	v_min_u32_e32 v27, 0x8ff, v27
	v_lshlrev_b32_e32 v27, 4, v27
	s_waitcnt lgkmcnt(0)
	global_load_dwordx4 v[16:19], v2, s[4:5]
	global_load_dwordx4 v[8:11], v28, s[4:5]
	global_load_dwordx4 v[12:15], v29, s[4:5]

.Lw3b1:
	global_load_dwordx4 v[20:23], v30, s[4:5]
	global_load_dwordx4 v[32:35], v31, s[4:5]
	global_load_dwordx4 v[36:39], v2, s[6:7]
	global_load_dwordx4 v[40:43], v28, s[6:7]
	global_load_dwordx4 v[44:47], v27, s[6:7]
	global_load_dword v5, v26, s[8:9]
	global_load_dword v7, v26, s[8:9] offset:512
	global_load_dword v1, v26, s[10:11]
	global_load_dword v4, v26, s[12:13]
	global_load_dword v6, v26, s[14:15]
	s_load_dword s42, s[0:1], 0x0
	s_load_dword s43, s[0:1], 0x40
	v_lshrrev_b32_e32 v48, 6, v0
	s_nop 0
	v_readfirstlane_b32 s41, v48
	s_movk_i32 s40, 0x5aa5
	s_mov_b64 exec, 0
	s_cmpk_lt_u32 s41, 6
	s_cbranch_scc1 .Lw3s0d0_13
	s_cmpk_lt_u32 s41, 9
	s_cbranch_scc1 .Lw3s0d6_13
	s_cmpk_lt_u32 s41, 11
	s_cbranch_scc1 .Lw3s0d9_13
	s_cmpk_lt_u32 s41, 12
	s_cbranch_scc1 .Lw3s0d11_13
	s_branch .Lw3t12

.Lw3b2:
	s_waitcnt vmcnt(12)
	ds_write_b128 v2, v[16:19]
	s_waitcnt vmcnt(11)
	ds_write_b128 v2, v[8:11] offset:13312
	s_waitcnt vmcnt(10)
	ds_write_b128 v2, v[12:15] offset:26624
	s_waitcnt vmcnt(9)
	ds_write_b128 v2, v[20:23] offset:39936
	s_movk_i32 s4, 0x300
	v_cmp_gt_u32_e32 vcc, s4, v0
	s_waitcnt vmcnt(8)
	s_and_saveexec_b64 s[4:5], vcc
	ds_write_b128 v2, v[32:35] offset:53248
	s_or_b64 exec, exec, s[4:5]
	v_mov_b32_e32 v3, 0x1dd00
	v_lshl_add_u32 v3, v0, 4, v3
	s_waitcnt vmcnt(7)
	ds_write_b128 v3, v[36:39]

.Lw3b3:
	s_waitcnt vmcnt(6)
	ds_write_b128 v3, v[40:43] offset:13312
	s_movk_i32 s4, 0x280
	v_cmp_gt_u32_e32 vcc, s4, v0
	s_waitcnt vmcnt(5)
	s_and_saveexec_b64 s[4:5], vcc
	ds_write_b128 v3, v[44:47] offset:26624
	s_or_b64 exec, exec, s[4:5]
	s_waitcnt vmcnt(0)
	s_movk_i32 s4, 0x80
	v_cmp_gt_u32_e32 vcc, s4, v0
	s_and_saveexec_b64 s[4:5], vcc
	s_cbranch_execz .LBB3_6
	v_mov_b32_e32 v3, 0x26d00
	v_add_f32_e32 v2, v5, v7
	v_lshl_add_u32 v3, v0, 2, v3
	ds_write2st64_b32 v3, v2, v1 offset1:2
	ds_write2st64_b32 v3, v4, v6 offset0:4 offset1:6

.Lw3b4:
	s_load_dwordx2 s[18:19], s[0:1], 0x10
	s_mov_b32 s13, 0
	v_cmp_eq_u32_e32 vcc, 0, v0
	s_and_saveexec_b64 s[4:5], vcc
	v_mov_b32_e32 v1, 0
	v_mov_b32_e32 v2, 0x27900
	ds_write_b32 v2, v1
	s_or_b64 exec, exec, s[4:5]
	v_bfe_u32 v1, v0, 4, 2
	v_bfe_u32 v2, v0, 2, 2
	v_cmp_eq_u32_e32 vcc, v1, v2
	v_and_b32_e32 v2, 3, v0
	v_cmp_eq_u32_e64 s[4:5], 0, v2
	v_mov_b32_e32 v3, 0x3c00
	s_and_b64 s[4:5], vcc, s[4:5]
	v_cndmask_b32_e64 v4, 0, v3, s[4:5]
	v_cmp_eq_u32_e64 s[4:5], 1, v2
	s_and_b64 s[4:5], vcc, s[4:5]
	s_lshr_b32 s12, s3, 6
	v_cndmask_b32_e64 v5, 0, v3, s[4:5]

.Lw3b5:
	v_cmp_eq_u32_e64 s[4:5], 2, v2
	s_and_b64 s[4:5], vcc, s[4:5]
	v_and_b32_e32 v77, 63, v0
	v_cndmask_b32_e64 v6, 0, v3, s[4:5]
	v_cmp_eq_u32_e64 s[4:5], 3, v2
	s_and_b64 vcc, vcc, s[4:5]
	v_cndmask_b32_e32 v2, 0, v3, vcc
	v_pack_b32_f16 v73, v6, v2
	v_lshlrev_b32_e32 v2, 2, v0
	v_and_b32_e32 v82, 0xc0, v2
	v_and_b32_e32 v2, 48, v0
	v_mov_b32_e32 v3, 0
	s_waitcnt lgkmcnt(0)
	s_barrier
	v_and_b32_e32 v80, 15, v0
	s_load_dword s3, s[0:1], 0x68
	s_mul_i32 s0, s12, 0x1100
	v_lshl_add_u64 v[74:75], s[10:11], 0, v[2:3]
	v_bfe_u32 v3, v0, 2, 4
	v_lshlrev_b32_e32 v0, 6, v0
	s_add_i32 s4, s0, 0x10000

.Lw3b6:
	v_mul_u32_u24_e32 v3, 0x110, v3
	v_and_b32_e32 v0, 0xc0, v0
	s_movk_i32 s26, 0x110
	v_add3_u32 v83, s4, v3, v0
	v_mov_b32_e32 v0, s4
	v_mad_u32_u24 v0, v80, s26, v0
	v_pack_b32_f16 v72, v4, v5
	v_lshlrev_b32_e32 v81, 4, v80
	v_lshlrev_b32_e32 v4, 7, v1
	v_add_u32_e32 v97, v0, v2
	v_mbcnt_lo_u32_b32 v0, -1, 0
	v_cmp_eq_u32_e64 s[0:1], 0, v77
	v_or_b32_e32 v76, s4, v81
	v_lshlrev_b32_e32 v84, 5, v1
	v_cmp_gt_u32_e64 s[4:5], 16, v77
	v_or_b32_e32 v85, 24, v82
	v_or_b32_e32 v86, 28, v82
	v_or_b32_e32 v87, 32, v82
	v_or_b32_e32 v88, 36, v82
	v_or_b32_e32 v89, 40, v82
	v_or_b32_e32 v90, 44, v82
	v_or_b32_e32 v91, 48, v82
	v_or_b32_e32 v92, 52, v82

.Lw3b7:
	v_or_b32_e32 v93, 56, v82
	v_or_b32_e32 v94, 60, v82
	v_mov_b32_e32 v95, 0x27900
	v_add_u32_e32 v96, 0x26d00, v4
	s_mov_b32 s27, 0x1ffff00
	v_mov_b32_e32 v98, 0x3727c5ac
	s_mov_b32 s28, 0x800000
	v_mov_b32_e32 v99, 0xc0135761
	v_mbcnt_hi_u32_b32 v100, -1, v0
	v_mov_b32_e32 v101, 0x26d00
	v_mov_b32_e32 v102, 0x1dd00
	s_mov_b32 s47, s41

.LBB3_15:
	s_or_b64 exec, exec, s[10:11]
	v_readfirstlane_b32 s10, v0
	s_waitcnt lgkmcnt(0)
	s_mul_i32 s12, s10, s3
	s_add_i32 s12, s12, s2
	s_cmpk_gt_i32 s12, 0x1869
	s_mov_b64 s[10:11], -1
	s_cbranch_scc1 .LBB3_10
	ds_read_b128 v[28:31], v96
	ds_read_b128 v[24:27], v96 offset:16

.Lw3b9:
	ds_read_b128 v[20:23], v96 offset:32
	ds_read_b128 v[16:19], v96 offset:48
	ds_read_b128 v[12:15], v96 offset:64
	ds_read_b128 v[8:11], v96 offset:80
	ds_read_b128 v[4:7], v96 offset:96
	ds_read_b128 v[0:3], v96 offset:112
	s_lshl_b32 s10, s12, 4
	s_ashr_i32 s11, s10, 31
	v_lshl_add_u64 v[78:79], s[10:11], 2, v[74:75]
	s_mov_b32 s11, 0
	s_mov_b64 s[22:23], -1
	s_branch .LBB3_18
.LBB3_17:
	s_or_b64 exec, exec, s[20:21]
	v_mov_b32_e32 v48, v77
	ds_read_b128 v[32:35], v97
	ds_read_b128 v[36:39], v97 offset:64
	ds_read_b128 v[40:43], v97 offset:128
	ds_read_b128 v[44:47], v97 offset:192
	s_nop 0

.Lw3b10:
	v_lshlrev_b32_e32 v48, 4, v48
	v_lshl_add_u32 v103, s11, 15, v48
	ds_read_b128 v[48:51], v103
	ds_read_b128 v[52:55], v103 offset:1024
	ds_read_b128 v[56:59], v103 offset:2048
	ds_read_b128 v[60:63], v103 offset:3072
	ds_read_b128 v[64:67], v103 offset:4096
	ds_read_b128 v[68:71], v103 offset:5120
	ds_read_b128 v[104:107], v103 offset:6144
	ds_read_b128 v[108:111], v103 offset:7168
	s_waitcnt lgkmcnt(7)
	v_mfma_f32_16x16x32_f16 v[28:31], v[48:51], v[32:35], v[28:31]
	s_waitcnt lgkmcnt(6)
	v_mfma_f32_16x16x32_f16 v[24:27], v[52:55], v[32:35], v[24:27]
	s_waitcnt lgkmcnt(5)
	v_mfma_f32_16x16x32_f16 v[20:23], v[56:59], v[32:35], v[20:23]
	s_waitcnt lgkmcnt(4)
	v_mfma_f32_16x16x32_f16 v[16:19], v[60:63], v[32:35], v[16:19]

.Lw3b11:
	ds_read_b128 v[48:51], v103 offset:8192
	ds_read_b128 v[52:55], v103 offset:9216
	ds_read_b128 v[56:59], v103 offset:10240
	ds_read_b128 v[60:63], v103 offset:11264
	s_waitcnt lgkmcnt(7)
	v_mfma_f32_16x16x32_f16 v[12:15], v[64:67], v[32:35], v[12:15]
	s_waitcnt lgkmcnt(6)
	v_mfma_f32_16x16x32_f16 v[8:11], v[68:71], v[32:35], v[8:11]
	s_waitcnt lgkmcnt(5)
	v_mfma_f32_16x16x32_f16 v[4:7], v[104:107], v[32:35], v[4:7]
	s_waitcnt lgkmcnt(4)
	v_mfma_f32_16x16x32_f16 v[0:3], v[108:111], v[32:35], v[0:3]
	ds_read_b128 v[32:35], v103 offset:12288
	ds_read_b128 v[64:67], v103 offset:13312
	ds_read_b128 v[68:71], v103 offset:14336
	ds_read_b128 v[104:107], v103 offset:15360
	s_waitcnt lgkmcnt(7)
	v_mfma_f32_16x16x32_f16 v[28:31], v[48:51], v[36:39], v[28:31]

.Lw3b12:
	s_waitcnt lgkmcnt(6)
	v_mfma_f32_16x16x32_f16 v[24:27], v[52:55], v[36:39], v[24:27]
	s_waitcnt lgkmcnt(5)
	v_mfma_f32_16x16x32_f16 v[20:23], v[56:59], v[36:39], v[20:23]
	s_waitcnt lgkmcnt(4)
	v_mfma_f32_16x16x32_f16 v[16:19], v[60:63], v[36:39], v[16:19]
	ds_read_b128 v[48:51], v103 offset:16384
	ds_read_b128 v[52:55], v103 offset:17408
	ds_read_b128 v[56:59], v103 offset:18432
	ds_read_b128 v[60:63], v103 offset:19456
	s_waitcnt lgkmcnt(7)
	v_mfma_f32_16x16x32_f16 v[12:15], v[32:35], v[36:39], v[12:15]
	s_waitcnt lgkmcnt(6)
	v_mfma_f32_16x16x32_f16 v[8:11], v[64:67], v[36:39], v[8:11]
	s_waitcnt lgkmcnt(5)
	v_mfma_f32_16x16x32_f16 v[4:7], v[68:71], v[36:39], v[4:7]
	s_waitcnt lgkmcnt(4)
	v_mfma_f32_16x16x32_f16 v[0:3], v[104:107], v[36:39], v[0:3]
	ds_read_b128 v[32:35], v103 offset:20480

.Lw3b13:
	ds_read_b128 v[36:39], v103 offset:21504
	ds_read_b128 v[64:67], v103 offset:22528
	ds_read_b128 v[68:71], v103 offset:23552
	s_waitcnt lgkmcnt(7)
	v_mfma_f32_16x16x32_f16 v[28:31], v[48:51], v[40:43], v[28:31]
	s_waitcnt lgkmcnt(6)
	v_mfma_f32_16x16x32_f16 v[24:27], v[52:55], v[40:43], v[24:27]
	s_waitcnt lgkmcnt(5)
	v_mfma_f32_16x16x32_f16 v[20:23], v[56:59], v[40:43], v[20:23]
	s_waitcnt lgkmcnt(4)
	v_mfma_f32_16x16x32_f16 v[16:19], v[60:63], v[40:43], v[16:19]
	ds_read_b128 v[48:51], v103 offset:24576
	ds_read_b128 v[52:55], v103 offset:25600
	ds_read_b128 v[56:59], v103 offset:26624
	ds_read_b128 v[60:63], v103 offset:27648
	s_waitcnt lgkmcnt(7)
	v_mfma_f32_16x16x32_f16 v[12:15], v[32:35], v[40:43], v[12:15]
	s_waitcnt lgkmcnt(6)
	v_mfma_f32_16x16x32_f16 v[8:11], v[36:39], v[40:43], v[8:11]

.Lw3b14:
	s_waitcnt lgkmcnt(5)
	v_mfma_f32_16x16x32_f16 v[4:7], v[64:67], v[40:43], v[4:7]
	s_waitcnt lgkmcnt(4)
	v_mfma_f32_16x16x32_f16 v[0:3], v[68:71], v[40:43], v[0:3]
	ds_read_b128 v[32:35], v103 offset:28672
	ds_read_b128 v[36:39], v103 offset:29696
	ds_read_b128 v[40:43], v103 offset:30720
	ds_read_b128 v[64:67], v103 offset:31744
	s_waitcnt lgkmcnt(7)
	v_mfma_f32_16x16x32_f16 v[28:31], v[48:51], v[44:47], v[28:31]
	s_waitcnt lgkmcnt(6)
	v_mfma_f32_16x16x32_f16 v[24:27], v[52:55], v[44:47], v[24:27]
	s_waitcnt lgkmcnt(5)
	v_mfma_f32_16x16x32_f16 v[20:23], v[56:59], v[44:47], v[20:23]
	s_waitcnt lgkmcnt(4)
	v_mfma_f32_16x16x32_f16 v[16:19], v[60:63], v[44:47], v[16:19]
	s_waitcnt lgkmcnt(3)
	v_mfma_f32_16x16x32_f16 v[12:15], v[32:35], v[44:47], v[12:15]
	s_waitcnt lgkmcnt(2)

.LBB3_18:
	s_mul_i32 s12, s11, 0x186a1
	v_lshl_add_u64 v[32:33], s[12:13], 2, v[78:79]
	global_load_dword v113, v[32:33], off
	global_load_dword v103, v[32:33], off offset:16
	s_mov_b32 s14, s13
	s_mov_b32 s15, s13
	s_mul_i32 s12, s11, 0xc3500
	s_lshl_b64 s[20:21], s[12:13], 2
	s_mov_b32 s12, s13
	v_mov_b64_e32 v[34:35], s[14:15]
	v_mov_b64_e32 v[32:33], s[12:13]
	s_add_u32 s20, s18, s20
	ds_write_b128 v83, v[32:35]
	ds_write_b128 v83, v[32:35] offset:16
	ds_write_b128 v83, v[32:35] offset:32
	ds_write_b128 v83, v[32:35] offset:48
	s_addc_u32 s21, s19, s21

.LBB3_20:
	s_or_b64 exec, exec, s[14:15]
	v_mov_b32_e32 v56, 0
	s_xor_b64 s[14:15], s[22:23], -1
	v_mov_b32_e32 v115, 31
	v_mov_b32_e32 v57, v56
	v_mov_b32_e32 v58, v56
	v_mov_b32_e32 v59, v56
	v_mov_b32_e32 v60, v56
	v_mov_b32_e32 v61, v56
	v_mov_b32_e32 v62, v56
	v_mov_b32_e32 v63, v56

.Lw3b17:
	s_branch .LBB3_22
.LBB3_21:
	s_waitcnt vmcnt(0)
	v_mov_b32_e32 v116, v114
	s_cbranch_execnz .LBB3_92
.LBB3_22:
	s_nop 2
	v_mov_b32_e32 v104, v63
	v_mov_b32_e32 v106, v62
	v_mov_b32_e32 v105, v61
	v_mov_b32_e32 v108, v60
	v_mov_b32_e32 v109, v59
	v_mov_b32_e32 v111, v58
	v_mov_b32_e32 v110, v57
	v_mov_b32_e32 v112, v56
	v_mov_b32_e32 v107, v115
	v_cmp_lt_i32_e32 vcc, v113, v103
	s_cbranch_vccz .LBB3_21
	v_or_b32_e32 v32, 4, v82
	s_waitcnt vmcnt(0)
	ds_bpermute_b32 v66, v82, v116
	ds_bpermute_b32 v123, v32, v116
	v_or_b32_e32 v32, 8, v82
	v_or_b32_e32 v34, 12, v82
	ds_bpermute_b32 v122, v32, v116
	ds_bpermute_b32 v121, v34, v116
	v_or_b32_e32 v34, 16, v82
	ds_bpermute_b32 v120, v34, v116

.Lw3b18:
	v_or_b32_e32 v34, 20, v82
	ds_bpermute_b32 v119, v34, v116
	s_waitcnt lgkmcnt(5)
	v_lshlrev_b32_e32 v32, 8, v66
	s_waitcnt lgkmcnt(4)
	v_lshlrev_b32_e32 v33, 8, v123
	v_and_or_b32 v32, v32, s27, v81
	v_and_or_b32 v33, v33, s27, v81
	ds_bpermute_b32 v118, v85, v116
	ds_bpermute_b32 v117, v86, v116
	global_load_dwordx4 v[60:63], v32, s[8:9]
	global_load_dwordx4 v[56:59], v33, s[8:9]
	s_waitcnt lgkmcnt(5)
	v_lshlrev_b32_e32 v32, 8, v122
	s_waitcnt lgkmcnt(4)
	v_lshlrev_b32_e32 v33, 8, v121
	v_and_or_b32 v32, v32, s27, v81
	v_and_or_b32 v33, v33, s27, v81
	global_load_dwordx4 v[52:55], v32, s[8:9]
	global_load_dwordx4 v[48:51], v33, s[8:9]

.Lw3b19:
	s_waitcnt lgkmcnt(3)
	v_lshlrev_b32_e32 v32, 8, v120
	s_waitcnt lgkmcnt(2)
	v_lshlrev_b32_e32 v33, 8, v119
	v_and_or_b32 v32, v32, s27, v81
	v_and_or_b32 v33, v33, s27, v81
	global_load_dwordx4 v[44:47], v32, s[8:9]
	global_load_dwordx4 v[40:43], v33, s[8:9]
	s_waitcnt lgkmcnt(1)
	v_lshlrev_b32_e32 v32, 8, v118
	s_waitcnt lgkmcnt(0)
	v_lshlrev_b32_e32 v33, 8, v117
	v_and_or_b32 v32, v32, s27, v81
	v_and_or_b32 v33, v33, s27, v81
	global_load_dwordx4 v[36:39], v32, s[8:9]
	s_nop 0
	global_load_dwordx4 v[32:35], v33, s[8:9]
	v_or_b32_e32 v64, 16, v80
	v_add_u32_e32 v64, v64, v113
	v_cmp_lt_i32_e32 vcc, v64, v103
	v_mov_b32_e32 v114, 0x3f86a0
	s_and_saveexec_b64 s[22:23], vcc

.Lw3b20:
	s_cbranch_execz .LBB3_25
	v_ashrrev_i32_e32 v65, 31, v64
	v_lshl_add_u64 v[64:65], v[64:65], 2, s[20:21]
	global_load_dword v114, v[64:65], off
.LBB3_25:
	s_or_b64 exec, exec, s[22:23]
	v_ashrrev_i32_e32 v124, 17, v66
	v_cmp_ne_u32_e32 vcc, v124, v107
	s_cmp_lg_u64 vcc, 0
	s_cselect_b64 s[22:23], -1, 0
	s_and_b64 s[24:25], s[22:23], vcc
	v_mov_b32_e32 v115, v107
	v_mov_b32_e32 v68, v112
	v_mov_b32_e32 v69, v110
	v_mov_b32_e32 v70, v111
	v_mov_b32_e32 v71, v109
	v_mov_b32_e32 v64, v108
	v_mov_b32_e32 v65, v105
	v_mov_b32_e32 v66, v106
	v_mov_b32_e32 v67, v104
	s_and_saveexec_b64 s[22:23], s[24:25]
	s_cbranch_execz .LBB3_29
	v_cmp_gt_i32_e32 vcc, 16, v107
	s_and_saveexec_b64 s[24:25], vcc
	s_cbranch_execz .LBB3_28
	v_cvt_pk_f16_f32 v67, v111, v109
	v_cvt_pk_f16_f32 v66, v112, v110
	v_cvt_pk_f16_f32 v65, v106, v104

.LBB3_29:
	s_or_b64 exec, exec, s[22:23]
	v_ashrrev_i32_e32 v123, 17, v123
	s_waitcnt vmcnt(7)
	v_mfma_f32_16x16x16_f16 v[64:67], v[72:73], v[60:61], v[64:67]
	v_cmp_ne_u32_e32 vcc, v123, v115
	s_cmp_lg_u64 vcc, 0
	s_cselect_b64 s[22:23], -1, 0
	v_mfma_f32_16x16x16_f16 v[60:63], v[72:73], v[62:63], v[68:71]
	s_and_b64 s[24:25], s[22:23], vcc
	s_and_saveexec_b64 s[22:23], s[24:25]
	s_cbranch_execz .LBB3_33
	v_cmp_gt_i32_e32 vcc, 16, v115

.Lw3b22:
	s_and_saveexec_b64 s[24:25], vcc
	s_cbranch_execz .LBB3_32
	s_nop 1
	v_cvt_pk_f16_f32 v63, v62, v63
	v_cvt_pk_f16_f32 v62, v60, v61
	v_cvt_pk_f16_f32 v61, v66, v67
	v_cvt_pk_f16_f32 v60, v64, v65
	v_mad_u64_u32 v[64:65], s[30:31], v115, s26, v[76:77]
	ds_write_b128 v64, v[60:63]

.Lw3b23:
	v_cmp_ne_u32_e32 vcc, v68, v115
	s_cmp_lg_u64 vcc, 0
	s_cselect_b64 s[22:23], -1, 0
	v_mfma_f32_16x16x16_f16 v[56:59], v[72:73], v[58:59], v[60:63]
	s_and_b64 s[24:25], s[22:23], vcc
	s_and_saveexec_b64 s[22:23], s[24:25]
	s_cbranch_execz .LBB3_37
	v_cmp_gt_i32_e32 vcc, 16, v115
	s_and_saveexec_b64 s[24:25], vcc
	s_cbranch_execz .LBB3_36
	s_nop 1
	v_cvt_pk_f16_f32 v59, v58, v59
	v_cvt_pk_f16_f32 v58, v56, v57
	v_cvt_pk_f16_f32 v57, v66, v67
	v_cvt_pk_f16_f32 v56, v64, v65
	v_mad_u64_u32 v[60:61], s[30:31], v115, s26, v[76:77]
	ds_write_b128 v60, v[56:59]
.LBB3_36:
	s_or_b64 exec, exec, s[24:25]
	s_nop 0
	v_mov_b32_e32 v56, 0
	v_mov_b32_e32 v115, v68
	v_mov_b32_e32 v57, v56
	v_mov_b32_e32 v58, v56
	v_mov_b32_e32 v59, v56
.Lw3t24:
	s_cbranch_execz .Lw3c24

.LBB3_37:
	s_or_b64 exec, exec, s[22:23]
	v_ashrrev_i32_e32 v68, 17, v121
	s_waitcnt vmcnt(5)
	v_mfma_f32_16x16x16_f16 v[60:63], v[72:73], v[52:53], v[64:67]
	v_cmp_ne_u32_e32 vcc, v68, v115
	s_cmp_lg_u64 vcc, 0
	s_cselect_b64 s[22:23], -1, 0
	v_mfma_f32_16x16x16_f16 v[52:55], v[72:73], v[54:55], v[56:59]
	s_and_b64 s[24:25], s[22:23], vcc
	s_and_saveexec_b64 s[22:23], s[24:25]
	s_cbranch_execz .LBB3_41
	v_cmp_gt_i32_e32 vcc, 16, v115
	s_and_saveexec_b64 s[24:25], vcc
	s_cbranch_execz .LBB3_40
	s_nop 1
	v_cvt_pk_f16_f32 v55, v54, v55
	v_cvt_pk_f16_f32 v54, v52, v53
	v_cvt_pk_f16_f32 v53, v62, v63
	v_cvt_pk_f16_f32 v52, v60, v61
	v_mad_u64_u32 v[56:57], s[30:31], v115, s26, v[76:77]

.LBB3_41:
	s_or_b64 exec, exec, s[22:23]
	v_ashrrev_i32_e32 v64, 17, v120
	s_waitcnt vmcnt(4)
	v_mfma_f32_16x16x16_f16 v[56:59], v[72:73], v[48:49], v[60:63]
	v_cmp_ne_u32_e32 vcc, v64, v115
	s_cmp_lg_u64 vcc, 0
	s_cselect_b64 s[22:23], -1, 0
	v_mfma_f32_16x16x16_f16 v[48:51], v[72:73], v[50:51], v[52:55]
	s_and_b64 s[24:25], s[22:23], vcc
	s_and_saveexec_b64 s[22:23], s[24:25]
	s_cbranch_execz .LBB3_45
	v_cmp_gt_i32_e32 vcc, 16, v115
	s_and_saveexec_b64 s[24:25], vcc
	s_cbranch_execz .LBB3_44
	s_nop 1
	v_cvt_pk_f16_f32 v51, v50, v51

.LBB3_44:
	s_or_b64 exec, exec, s[24:25]
	s_nop 0
	v_mov_b32_e32 v48, 0
	v_mov_b32_e32 v115, v64
	v_mov_b32_e32 v49, v48
	v_mov_b32_e32 v50, v48
	v_mov_b32_e32 v51, v48
	v_mov_b32_e32 v56, v48
	v_mov_b32_e32 v57, v48
	v_mov_b32_e32 v58, v48
	v_mov_b32_e32 v59, v48
.LBB3_45:
	s_or_b64 exec, exec, s[22:23]
	v_ashrrev_i32_e32 v60, 17, v119
	s_waitcnt vmcnt(3)
	v_mfma_f32_16x16x16_f16 v[52:55], v[72:73], v[44:45], v[56:59]
	v_cmp_ne_u32_e32 vcc, v60, v115
	s_cmp_lg_u64 vcc, 0
	s_cselect_b64 s[22:23], -1, 0
	v_mfma_f32_16x16x16_f16 v[44:47], v[72:73], v[46:47], v[48:51]
.Lw3t27:
	s_cbranch_execz .Lw3c27
.Lw3b27:
	s_and_b64 s[24:25], s[22:23], vcc
	s_and_saveexec_b64 s[22:23], s[24:25]
	s_cbranch_execz .LBB3_49
	v_cmp_gt_i32_e32 vcc, 16, v115
	s_and_saveexec_b64 s[24:25], vcc
	s_cbranch_execz .LBB3_48
	s_nop 1
	v_cvt_pk_f16_f32 v47, v46, v47
	v_cvt_pk_f16_f32 v46, v44, v45
	v_cvt_pk_f16_f32 v45, v54, v55
	v_cvt_pk_f16_f32 v44, v52, v53
	v_mad_u64_u32 v[48:49], s[30:31], v115, s26, v[76:77]
	ds_write_b128 v48, v[44:47]
.LBB3_48:
	s_or_b64 exec, exec, s[24:25]
	s_nop 0
	v_mov_b32_e32 v44, 0
	v_mov_b32_e32 v115, v60
	v_mov_b32_e32 v45, v44
	v_mov_b32_e32 v46, v44
	v_mov_b32_e32 v47, v44
	v_mov_b32_e32 v52, v44
	v_mov_b32_e32 v53, v44
	v_mov_b32_e32 v54, v44
	v_mov_b32_e32 v55, v44
.LBB3_49:
.Lw3t28:
	s_cbranch_execz .Lw3c28

.Lw3b29:
	v_mov_b32_e32 v40, 0
	v_mov_b32_e32 v115, v56
	v_mov_b32_e32 v41, v40
	v_mov_b32_e32 v42, v40
	v_mov_b32_e32 v43, v40
	v_mov_b32_e32 v48, v40
	v_mov_b32_e32 v49, v40
	v_mov_b32_e32 v50, v40
	v_mov_b32_e32 v51, v40
.LBB3_53:
	s_or_b64 exec, exec, s[22:23]
	v_ashrrev_i32_e32 v52, 17, v117
	s_waitcnt vmcnt(1)
	v_mfma_f32_16x16x16_f16 v[44:47], v[72:73], v[36:37], v[48:51]
	v_cmp_ne_u32_e32 vcc, v52, v115
	s_cmp_lg_u64 vcc, 0
	s_cselect_b64 s[22:23], -1, 0
	v_mfma_f32_16x16x16_f16 v[36:39], v[72:73], v[38:39], v[40:43]
	s_and_b64 s[24:25], s[22:23], vcc
	s_and_saveexec_b64 s[22:23], s[24:25]
	s_cbranch_execz .LBB3_57
	v_cmp_gt_i32_e32 vcc, 16, v115
	s_and_saveexec_b64 s[24:25], vcc
	s_cbranch_execz .LBB3_56
	s_nop 1
	v_cvt_pk_f16_f32 v39, v38, v39
	v_cvt_pk_f16_f32 v38, v36, v37
	v_cvt_pk_f16_f32 v37, v46, v47

.Lw3b30:
	v_cvt_pk_f16_f32 v36, v44, v45
	v_mad_u64_u32 v[40:41], s[30:31], v115, s26, v[76:77]
	ds_write_b128 v40, v[36:39]
.LBB3_56:
	s_or_b64 exec, exec, s[24:25]
	s_nop 0
	v_mov_b32_e32 v36, 0
	v_mov_b32_e32 v115, v52
	v_mov_b32_e32 v37, v36
	v_mov_b32_e32 v38, v36
	v_mov_b32_e32 v39, v36
	v_mov_b32_e32 v44, v36
	v_mov_b32_e32 v45, v36
	v_mov_b32_e32 v46, v36
	v_mov_b32_e32 v47, v36
.LBB3_57:
	s_or_b64 exec, exec, s[22:23]
	s_waitcnt vmcnt(0)
	v_mfma_f32_16x16x16_f16 v[60:63], v[72:73], v[32:33], v[44:47]
	v_add_u32_e32 v32, 8, v113
	v_cmp_lt_i32_e32 vcc, v32, v103
	v_mfma_f32_16x16x16_f16 v[56:59], v[72:73], v[34:35], v[36:39]
	s_cbranch_vccz .LBB3_91
	ds_bpermute_b32 v123, v87, v116
	ds_bpermute_b32 v122, v88, v116

.Lw3b31:
	ds_bpermute_b32 v121, v89, v116
	ds_bpermute_b32 v120, v90, v116
	ds_bpermute_b32 v119, v91, v116
	ds_bpermute_b32 v118, v92, v116
	s_waitcnt lgkmcnt(5)
	v_lshlrev_b32_e32 v32, 8, v123
	s_waitcnt lgkmcnt(4)
	v_lshlrev_b32_e32 v33, 8, v122
	v_and_or_b32 v32, v32, s27, v81
	v_and_or_b32 v33, v33, s27, v81
	ds_bpermute_b32 v117, v93, v116
	ds_bpermute_b32 v116, v94, v116
	global_load_dwordx4 v[68:71], v32, s[8:9]
	global_load_dwordx4 v[64:67], v33, s[8:9]
	s_waitcnt lgkmcnt(5)
	v_lshlrev_b32_e32 v32, 8, v121
	s_waitcnt lgkmcnt(4)
	v_lshlrev_b32_e32 v33, 8, v120
	v_and_or_b32 v32, v32, s27, v81
	v_and_or_b32 v33, v33, s27, v81

.Lw3b32:
	global_load_dwordx4 v[52:55], v32, s[8:9]
	global_load_dwordx4 v[48:51], v33, s[8:9]
	s_waitcnt lgkmcnt(3)
	v_lshlrev_b32_e32 v32, 8, v119
	s_waitcnt lgkmcnt(2)
	v_lshlrev_b32_e32 v33, 8, v118
	v_and_or_b32 v32, v32, s27, v81
	v_and_or_b32 v33, v33, s27, v81
	global_load_dwordx4 v[44:47], v32, s[8:9]
	global_load_dwordx4 v[40:43], v33, s[8:9]
	s_waitcnt lgkmcnt(1)
	v_lshlrev_b32_e32 v32, 8, v117
	s_waitcnt lgkmcnt(0)
	v_lshlrev_b32_e32 v33, 8, v116
	v_and_or_b32 v32, v32, s27, v81
	v_and_or_b32 v33, v33, s27, v81
	global_load_dwordx4 v[36:39], v32, s[8:9]
	s_nop 0
	global_load_dwordx4 v[32:35], v33, s[8:9]
	v_ashrrev_i32_e32 v123, 17, v123

.Lw3b33:
	v_cmp_ne_u32_e32 vcc, v123, v115
	s_cmp_lg_u64 vcc, 0
	s_cselect_b64 s[22:23], -1, 0
	s_and_b64 s[24:25], s[22:23], vcc
	s_and_saveexec_b64 s[22:23], s[24:25]
	s_cbranch_execz .LBB3_62
	v_cmp_gt_i32_e32 vcc, 16, v115
	s_and_saveexec_b64 s[24:25], vcc
	s_cbranch_execz .LBB3_61
	v_cvt_pk_f16_f32 v59, v58, v59
	v_cvt_pk_f16_f32 v58, v56, v57
	v_cvt_pk_f16_f32 v57, v62, v63
	v_cvt_pk_f16_f32 v56, v60, v61
	v_mad_u64_u32 v[60:61], s[30:31], v115, s26, v[76:77]
	ds_write_b128 v60, v[56:59]

.LBB3_66:
	s_or_b64 exec, exec, s[22:23]
	v_ashrrev_i32_e32 v68, 17, v121
	s_waitcnt vmcnt(6)
	v_mfma_f32_16x16x16_f16 v[60:63], v[72:73], v[64:65], v[60:63]
	v_cmp_ne_u32_e32 vcc, v68, v115
	s_cmp_lg_u64 vcc, 0
	s_cselect_b64 s[22:23], -1, 0
	v_mfma_f32_16x16x16_f16 v[56:59], v[72:73], v[66:67], v[56:59]
	s_and_b64 s[24:25], s[22:23], vcc
	s_and_saveexec_b64 s[22:23], s[24:25]
	s_cbranch_execz .LBB3_70
	v_cmp_gt_i32_e32 vcc, 16, v115
	s_and_saveexec_b64 s[24:25], vcc
	s_cbranch_execz .LBB3_69
	s_nop 1
	v_cvt_pk_f16_f32 v59, v58, v59
	v_cvt_pk_f16_f32 v58, v56, v57
	v_cvt_pk_f16_f32 v57, v62, v63

.LBB3_70:
	s_or_b64 exec, exec, s[22:23]
	v_ashrrev_i32_e32 v64, 17, v120
	s_waitcnt vmcnt(5)
	v_mfma_f32_16x16x16_f16 v[60:63], v[72:73], v[52:53], v[60:63]
	v_cmp_ne_u32_e32 vcc, v64, v115
	s_cmp_lg_u64 vcc, 0
	s_cselect_b64 s[22:23], -1, 0
	v_mfma_f32_16x16x16_f16 v[52:55], v[72:73], v[54:55], v[56:59]
	s_and_b64 s[24:25], s[22:23], vcc
	s_and_saveexec_b64 s[22:23], s[24:25]
	s_cbranch_execz .LBB3_74

.Lw3b38:
	v_cmp_ne_u32_e32 vcc, v64, v115
	s_cmp_lg_u64 vcc, 0
	s_cselect_b64 s[22:23], -1, 0
	v_mfma_f32_16x16x16_f16 v[48:51], v[72:73], v[50:51], v[52:55]
	s_and_b64 s[24:25], s[22:23], vcc
	s_and_saveexec_b64 s[22:23], s[24:25]
	s_cbranch_execz .LBB3_78
	v_cmp_gt_i32_e32 vcc, 16, v115
	s_and_saveexec_b64 s[24:25], vcc
	s_cbranch_execz .LBB3_77
	s_nop 1
	v_cvt_pk_f16_f32 v51, v50, v51
	v_cvt_pk_f16_f32 v50, v48, v49
	v_cvt_pk_f16_f32 v49, v58, v59
	v_cvt_pk_f16_f32 v48, v56, v57
	v_mad_u64_u32 v[52:53], s[30:31], v115, s26, v[76:77]
	ds_write_b128 v52, v[48:51]
.LBB3_77:
	s_or_b64 exec, exec, s[24:25]
	s_nop 0
	v_mov_b32_e32 v48, 0
	v_mov_b32_e32 v115, v64
	v_mov_b32_e32 v49, v48
	v_mov_b32_e32 v50, v48
.Lw3t39:
	s_cbranch_execz .Lw3c39

.LBB3_78:
	s_or_b64 exec, exec, s[22:23]
	v_ashrrev_i32_e32 v60, 17, v118
	s_waitcnt vmcnt(3)
	v_mfma_f32_16x16x16_f16 v[52:55], v[72:73], v[44:45], v[56:59]
	v_cmp_ne_u32_e32 vcc, v60, v115
	s_cmp_lg_u64 vcc, 0
	s_cselect_b64 s[22:23], -1, 0
	v_mfma_f32_16x16x16_f16 v[44:47], v[72:73], v[46:47], v[48:51]
	s_and_b64 s[24:25], s[22:23], vcc
	s_and_saveexec_b64 s[22:23], s[24:25]
	s_cbranch_execz .LBB3_82
	v_cmp_gt_i32_e32 vcc, 16, v115
	s_and_saveexec_b64 s[24:25], vcc
	s_cbranch_execz .LBB3_81
	s_nop 1
	v_cvt_pk_f16_f32 v47, v46, v47
	v_cvt_pk_f16_f32 v46, v44, v45
	v_cvt_pk_f16_f32 v45, v54, v55
	v_cvt_pk_f16_f32 v44, v52, v53
	v_mad_u64_u32 v[48:49], s[30:31], v115, s26, v[76:77]

.LBB3_82:
	s_or_b64 exec, exec, s[22:23]
	v_ashrrev_i32_e32 v56, 17, v117
	s_waitcnt vmcnt(2)
	v_mfma_f32_16x16x16_f16 v[48:51], v[72:73], v[40:41], v[52:55]
	v_cmp_ne_u32_e32 vcc, v56, v115
	s_cmp_lg_u64 vcc, 0
	s_cselect_b64 s[22:23], -1, 0
	v_mfma_f32_16x16x16_f16 v[40:43], v[72:73], v[42:43], v[44:47]
	s_and_b64 s[24:25], s[22:23], vcc
	s_and_saveexec_b64 s[22:23], s[24:25]
	s_cbranch_execz .LBB3_86
	v_cmp_gt_i32_e32 vcc, 16, v115
	s_and_saveexec_b64 s[24:25], vcc
	s_cbranch_execz .LBB3_85
	s_nop 1

.Lw3b42:
	v_mfma_f32_16x16x16_f16 v[36:39], v[72:73], v[38:39], v[40:43]
	s_and_b64 s[24:25], s[22:23], vcc
	s_and_saveexec_b64 s[22:23], s[24:25]
	s_cbranch_execz .LBB3_90
	v_cmp_gt_i32_e32 vcc, 16, v115
	s_and_saveexec_b64 s[24:25], vcc
	s_cbranch_execz .LBB3_89
	s_nop 1
	v_cvt_pk_f16_f32 v39, v38, v39
	v_cvt_pk_f16_f32 v38, v36, v37
	v_cvt_pk_f16_f32 v37, v46, v47
	v_cvt_pk_f16_f32 v36, v44, v45
	v_mad_u64_u32 v[40:41], s[30:31], v115, s26, v[76:77]
	ds_write_b128 v40, v[36:39]
.LBB3_89:
	s_or_b64 exec, exec, s[24:25]
	s_nop 0
	v_mov_b32_e32 v36, 0
	v_mov_b32_e32 v115, v52
	v_mov_b32_e32 v37, v36
	v_mov_b32_e32 v38, v36
	v_mov_b32_e32 v39, v36
	v_mov_b32_e32 v44, v36
	v_mov_b32_e32 v45, v36
	v_mov_b32_e32 v46, v36
.Lw3t43:
	s_cbranch_execz .Lw3c43

.LBB3_94:
	v_mov_b32_e32 v32, v28
	v_mov_b32_e32 v33, v24
	v_mov_b32_e32 v34, v29
	v_mov_b32_e32 v35, v25
.Lw3t44:
	s_cbranch_execz .Lw3c44
.Lw3b44:
	v_pk_add_f32 v[32:33], v[32:33], v[34:35]
	v_mov_b32_e32 v34, v30
	v_mov_b32_e32 v35, v26
	v_mov_b32_e32 v36, v31
	v_mov_b32_e32 v37, v27
	v_pk_add_f32 v[34:35], v[34:35], v[36:37]
	v_mov_b32_e32 v36, v20
	v_pk_add_f32 v[32:33], v[32:33], v[34:35]
	v_mov_b32_e32 v34, v21
	v_mov_b32_e32 v35, v22
	v_mov_b32_e32 v37, v23
	v_pk_add_f32 v[34:35], v[34:35], v[36:37]
	v_add_f32_e32 v32, 0, v32
	v_pk_add_f32 v[34:35], v[34:35], v[34:35] op_sel:[0,1] op_sel_hi:[1,0]
	v_add_f32_e32 v32, v32, v33
	v_add_f32_e32 v36, v16, v17
	v_add_f32_e32 v38, v18, v19
	v_mov_b32_e32 v33, v12
	v_mov_b32_e32 v35, v13
	v_mov_b32_e32 v37, v14
	v_mov_b32_e32 v39, v15
	v_pk_add_f32 v[32:33], v[32:33], v[34:35]
	v_pk_add_f32 v[34:35], v[36:37], v[38:39]
	v_mov_b32_e32 v36, v8

.Lw3b45:
	v_pk_add_f32 v[32:33], v[32:33], v[34:35]
	v_mov_b32_e32 v34, v9
	v_mov_b32_e32 v35, v10
	v_mov_b32_e32 v37, v11
	v_pk_add_f32 v[34:35], v[34:35], v[36:37]
	v_pk_add_f32 v[32:33], v[32:33], v[32:33] op_sel:[0,1] op_sel_hi:[1,0]
	v_pk_add_f32 v[34:35], v[34:35], v[34:35] op_sel:[0,1] op_sel_hi:[1,0]
	v_add_f32_e32 v36, v4, v5
	v_add_f32_e32 v38, v6, v7
	v_mov_b32_e32 v33, v0
	v_mov_b32_e32 v35, v1
	v_mov_b32_e32 v37, v2
	v_mov_b32_e32 v39, v3
	v_pk_add_f32 v[32:33], v[32:33], v[34:35]
	v_pk_add_f32 v[34:35], v[36:37], v[38:39]
	s_nop 0
	v_pk_add_f32 v[32:33], v[32:33], v[34:35]
	v_and_b32_e32 v34, 64, v100
	v_add_f32_e32 v32, v32, v33
	v_xor_b32_e32 v33, 16, v100
	v_add_u32_e32 v34, 64, v34
	v_cmp_lt_i32_e32 vcc, v33, v34
	s_nop 1
	v_cndmask_b32_e32 v33, v100, v33, vcc

.Lw3b46:
	v_lshlrev_b32_e32 v40, 2, v33
	ds_bpermute_b32 v33, v40, v32
	s_waitcnt lgkmcnt(0)
	v_add_f32_e32 v32, v32, v33
	v_xor_b32_e32 v33, 32, v100
	v_cmp_lt_i32_e32 vcc, v33, v34
	s_nop 1
	v_cndmask_b32_e32 v33, v100, v33, vcc
	v_lshlrev_b32_e32 v41, 2, v33
	ds_bpermute_b32 v33, v41, v32
	s_waitcnt lgkmcnt(0)
	v_add_f32_e32 v42, v32, v33
	v_fmamk_f32 v29, v42, 0xbc000000, v29
	v_fmamk_f32 v25, v42, 0xbc000000, v25
	v_fmamk_f32 v39, v42, 0xbc000000, v31
	v_fmamk_f32 v38, v42, 0xbc000000, v30
	v_fmac_f32_e32 v28, 0xbc000000, v42
	v_fmamk_f32 v37, v42, 0xbc000000, v27
	v_fmac_f32_e32 v24, 0xbc000000, v42
	v_mov_b32_e32 v30, v29
	v_mov_b32_e32 v31, v25
	v_fmamk_f32 v36, v42, 0xbc000000, v26

.Lw3b47:
	v_mov_b32_e32 v26, v28
	v_mov_b32_e32 v27, v24
	v_pk_mul_f32 v[30:31], v[30:31], v[30:31]
	v_mov_b32_e32 v32, v39
	v_mov_b32_e32 v33, v37
	v_pk_fma_f32 v[26:27], v[26:27], v[26:27], v[30:31]
	v_mov_b32_e32 v30, v38
	v_mov_b32_e32 v31, v36
	v_pk_mul_f32 v[32:33], v[32:33], v[32:33]
	v_fmamk_f32 v35, v42, 0xbc000000, v21
	v_pk_fma_f32 v[30:31], v[30:31], v[30:31], v[32:33]
	v_fmamk_f32 v34, v42, 0xbc000000, v20
	v_fmamk_f32 v23, v42, 0xbc000000, v23
	v_fmac_f32_e32 v22, 0xbc000000, v42
	v_pk_add_f32 v[26:27], v[26:27], v[30:31]
	v_pk_mul_f32 v[20:21], v[22:23], v[22:23]
	v_pk_mul_f32 v[30:31], v[34:35], v[34:35]
	v_fmamk_f32 v13, v42, 0xbc000000, v13

.Lw3b48:
	v_pk_mov_b32 v[32:33], v[30:31], v[20:21] op_sel:[1,0]
	v_mov_b32_e32 v31, v21
	v_pk_add_f32 v[20:21], v[32:33], v[30:31]
	v_fmac_f32_e32 v12, 0xbc000000, v42
	v_fmamk_f32 v33, v42, 0xbc000000, v19
	v_fmamk_f32 v32, v42, 0xbc000000, v18
	v_fmamk_f32 v19, v42, 0xbc000000, v15
	v_fmamk_f32 v18, v42, 0xbc000000, v14
	v_mul_f32_e32 v30, v12, v12
	v_mul_f32_e32 v31, v13, v13
	v_pk_add_f32 v[14:15], v[26:27], v[26:27] op_sel:[0,1] op_sel_hi:[1,0]
	v_pk_add_f32 v[20:21], v[20:21], v[20:21] op_sel:[0,1] op_sel_hi:[1,0]
	v_fmamk_f32 v17, v42, 0xbc000000, v17
	v_mov_b32_e32 v15, v30
	v_mov_b32_e32 v21, v31
	v_fmac_f32_e32 v16, 0xbc000000, v42
	v_pk_add_f32 v[14:15], v[14:15], v[20:21]
	v_mul_f32_e32 v20, v17, v17
	v_mul_f32_e32 v26, v33, v33

.Lw3b49:
	v_mul_f32_e32 v43, v18, v18
	v_mul_f32_e32 v44, v19, v19
	v_pk_fma_f32 v[20:21], v[16:17], v[16:17], v[20:21] op_sel_hi:[1,1,0]
	v_pk_fma_f32 v[26:27], v[32:33], v[32:33], v[26:27] op_sel_hi:[1,1,0]
	v_mov_b32_e32 v21, v43
	v_mov_b32_e32 v27, v44
	v_pk_add_f32 v[20:21], v[20:21], v[26:27]
	v_fmamk_f32 v11, v42, 0xbc000000, v11
	v_pk_add_f32 v[14:15], v[14:15], v[20:21]
	v_fmamk_f32 v21, v42, 0xbc000000, v9
	v_fmamk_f32 v20, v42, 0xbc000000, v8
	v_fmac_f32_e32 v10, 0xbc000000, v42
	v_pk_mul_f32 v[8:9], v[10:11], v[10:11]
	v_pk_mul_f32 v[26:27], v[20:21], v[20:21]
	v_fmamk_f32 v1, v42, 0xbc000000, v1
	v_pk_mov_b32 v[30:31], v[26:27], v[8:9] op_sel:[1,0]
	v_mov_b32_e32 v27, v9
	v_pk_add_f32 v[8:9], v[30:31], v[26:27]

.Lw3b50:
	v_fmac_f32_e32 v0, 0xbc000000, v42
	v_fmamk_f32 v27, v42, 0xbc000000, v7
	v_fmamk_f32 v26, v42, 0xbc000000, v6
	v_mul_f32_e32 v30, v0, v0
	v_mul_f32_e32 v31, v1, v1
	v_pk_add_f32 v[6:7], v[14:15], v[14:15] op_sel:[0,1] op_sel_hi:[1,0]
	v_pk_add_f32 v[8:9], v[8:9], v[8:9] op_sel:[0,1] op_sel_hi:[1,0]
	v_fmamk_f32 v5, v42, 0xbc000000, v5
	v_mov_b32_e32 v7, v30
	v_mov_b32_e32 v9, v31
	v_fmac_f32_e32 v4, 0xbc000000, v42
	v_fmamk_f32 v3, v42, 0xbc000000, v3
	v_fmamk_f32 v2, v42, 0xbc000000, v2
	v_pk_add_f32 v[6:7], v[6:7], v[8:9]
	v_mul_f32_e32 v8, v5, v5
	v_mul_f32_e32 v14, v27, v27
	v_mul_f32_e32 v42, v2, v2
	v_mul_f32_e32 v43, v3, v3
	v_pk_fma_f32 v[8:9], v[4:5], v[4:5], v[8:9] op_sel_hi:[1,1,0]
	v_pk_fma_f32 v[14:15], v[26:27], v[26:27], v[14:15] op_sel_hi:[1,1,0]

.Lw3b51:
	v_mov_b32_e32 v9, v42
	v_mov_b32_e32 v15, v43
	v_pk_add_f32 v[8:9], v[8:9], v[14:15]
	s_nop 0
	v_pk_add_f32 v[6:7], v[6:7], v[8:9]
	s_nop 0
	v_add_f32_e32 v6, v6, v7
	ds_bpermute_b32 v7, v40, v6
	s_waitcnt lgkmcnt(0)
	v_add_f32_e32 v6, v6, v7
	ds_bpermute_b32 v7, v41, v6
	s_waitcnt lgkmcnt(0)
	v_add_f32_e32 v6, v6, v7
	v_fmamk_f32 v6, v6, 0x3c000000, v98
	v_mul_f32_e32 v7, 0x4b800000, v6
	v_cmp_gt_f32_e32 vcc, s28, v6
	s_nop 1
	v_cndmask_b32_e32 v6, v6, v7, vcc
	v_rsq_f32_e32 v14, v6
	ds_read_b128 v[6:9], v96 offset:512
	ds_read_b128 v[40:43], v96 offset:528
	ds_read_b128 v[44:47], v96 offset:1024

.Lw3b52:
	ds_read_b128 v[48:51], v96 offset:1040
	v_mul_f32_e32 v15, 0x45800000, v14
	v_cndmask_b32_e32 v30, v14, v15, vcc
	v_pk_mul_f32 v[14:15], v[30:31], v[28:29] op_sel_hi:[0,1]
	s_waitcnt lgkmcnt(1)
	v_pk_fma_f32 v[6:7], v[6:7], v[14:15], v[44:45]
	v_pk_mul_f32 v[28:29], v[30:31], v[38:39] op_sel_hi:[0,1]
	v_pk_mul_f32 v[14:15], v[6:7], v[6:7]
	v_pk_fma_f32 v[8:9], v[8:9], v[28:29], v[46:47]
	v_fmamk_f32 v14, v14, 0xbdd2d3e8, v99
	v_fmamk_f32 v15, v15, 0xbdd2d3e8, v99
	v_mul_f32_e32 v14, v6, v14
	v_mul_f32_e32 v15, v7, v15
	v_exp_f32_e32 v14, v14
	v_exp_f32_e32 v15, v15
	v_pk_mul_f32 v[28:29], v[8:9], v[8:9]
	v_add_f32_e32 v14, 1.0, v14
	v_add_f32_e32 v15, 1.0, v15
	v_rcp_f32_e32 v14, v14
	v_rcp_f32_e32 v15, v15

.Lw3b53:
	v_fmamk_f32 v28, v28, 0xbdd2d3e8, v99
	v_mul_f32_e32 v28, v8, v28
	v_exp_f32_e32 v28, v28
	v_pk_mul_f32 v[6:7], v[6:7], v[14:15]
	v_fmamk_f32 v14, v29, 0xbdd2d3e8, v99
	v_mul_f32_e32 v14, v9, v14
	v_exp_f32_e32 v29, v14
	v_pk_mul_f32 v[14:15], v[30:31], v[24:25] op_sel_hi:[0,1]
	s_waitcnt lgkmcnt(0)
	v_pk_fma_f32 v[14:15], v[40:41], v[14:15], v[48:49]
	v_cvt_pk_f16_f32 v6, v6, v7
	v_pk_mul_f32 v[24:25], v[14:15], v[14:15]
	v_add_f32_e32 v7, 1.0, v28
	v_fmamk_f32 v24, v24, 0xbdd2d3e8, v99
	v_mul_f32_e32 v24, v14, v24
	v_exp_f32_e32 v24, v24
	v_rcp_f32_e32 v28, v7
	v_add_f32_e32 v7, 1.0, v29
	v_rcp_f32_e32 v29, v7
	v_add_f32_e32 v7, 1.0, v24
	v_fmamk_f32 v24, v25, 0xbdd2d3e8, v99
	v_mul_f32_e32 v31, v15, v24

.Lw3b54:
	v_pk_mul_f32 v[24:25], v[30:31], v[36:37] op_sel_hi:[0,1]
	v_pk_fma_f32 v[24:25], v[42:43], v[24:25], v[50:51]
	v_exp_f32_e32 v31, v31
	v_pk_mul_f32 v[36:37], v[24:25], v[24:25]
	v_rcp_f32_e32 v38, v7
	v_fmamk_f32 v36, v36, 0xbdd2d3e8, v99
	v_fmamk_f32 v37, v37, 0xbdd2d3e8, v99
	v_mul_f32_e32 v36, v24, v36
	v_mul_f32_e32 v37, v25, v37
	v_exp_f32_e32 v36, v36
	v_exp_f32_e32 v37, v37
	v_add_f32_e32 v7, 1.0, v31
	v_mov_b32_e32 v31, v84
	v_add_f32_e32 v36, 1.0, v36
	v_add_f32_e32 v37, 1.0, v37
	v_rcp_f32_e32 v36, v36
	v_rcp_f32_e32 v37, v37
	v_rcp_f32_e32 v39, v7
	v_pk_mul_f32 v[8:9], v[8:9], v[28:29]
	v_pk_mul_f32 v[24:25], v[24:25], v[36:37]
	s_nop 0
	s_nop 0
	v_lshl_add_u32 v7, v31, 2, v101

.Lw3b55:
	v_add_u32_e32 v52, 0x420, v7
	v_add_u32_e32 v46, 0x428, v7
	v_add_u32_e32 v50, 0x430, v7
	ds_read2_b32 v[36:37], v7 offset0:138 offset1:139
	ds_read2_b32 v[40:41], v7 offset0:142 offset1:143
	ds_read2_b32 v[42:43], v7 offset0:140 offset1:141
	ds_read2_b32 v[44:45], v7 offset0:136 offset1:137
	v_add_u32_e32 v7, 0x438, v7
	ds_read2_b32 v[46:47], v46 offset1:1
	ds_read2_b32 v[48:49], v7 offset1:1
	ds_read2_b32 v[50:51], v50 offset1:1
	ds_read2_b32 v[52:53], v52 offset1:1
	v_cvt_pk_f16_f32 v7, v8, v9
	v_pk_mul_f32 v[8:9], v[14:15], v[38:39]
	s_nop 0
	v_cvt_pk_f16_f32 v8, v8, v9

.Lw3b56:
	v_pk_mul_f32 v[14:15], v[30:31], v[34:35] op_sel_hi:[0,1]
	s_waitcnt lgkmcnt(0)
	v_pk_fma_f32 v[14:15], v[44:45], v[14:15], v[52:53]
	v_pk_mul_f32 v[22:23], v[30:31], v[22:23] op_sel_hi:[0,1]
	v_pk_mul_f32 v[28:29], v[14:15], v[14:15]
	v_pk_fma_f32 v[22:23], v[36:37], v[22:23], v[46:47]
	v_fmamk_f32 v9, v28, 0xbdd2d3e8, v99
	v_mul_f32_e32 v9, v14, v9
	v_fmamk_f32 v28, v29, 0xbdd2d3e8, v99
	v_exp_f32_e32 v9, v9
	v_mul_f32_e32 v28, v15, v28
	v_exp_f32_e32 v29, v28
	v_pk_mul_f32 v[34:35], v[22:23], v[22:23]
	v_add_f32_e32 v9, 1.0, v9
	v_rcp_f32_e32 v28, v9
	v_add_f32_e32 v9, 1.0, v29
	v_rcp_f32_e32 v29, v9
	v_fmamk_f32 v9, v34, 0xbdd2d3e8, v99
	v_mul_f32_e32 v9, v22, v9
	v_exp_f32_e32 v34, v9
	v_cvt_pk_f16_f32 v9, v24, v25

.Lw3b57:
	v_fmamk_f32 v24, v35, 0xbdd2d3e8, v99
	v_pk_mul_f32 v[16:17], v[30:31], v[16:17] op_sel_hi:[0,1]
	v_mul_f32_e32 v24, v23, v24
	v_pk_fma_f32 v[16:17], v[42:43], v[16:17], v[50:51]
	v_pk_mul_f32 v[14:15], v[14:15], v[28:29]
	v_exp_f32_e32 v29, v24
	v_pk_mul_f32 v[24:25], v[16:17], v[16:17]
	v_cvt_pk_f16_f32 v14, v14, v15
	v_fmamk_f32 v24, v24, 0xbdd2d3e8, v99
	v_mul_f32_e32 v24, v16, v24
	v_exp_f32_e32 v24, v24
	v_add_f32_e32 v15, 1.0, v34
	v_rcp_f32_e32 v28, v15
	v_add_f32_e32 v15, 1.0, v29
	v_rcp_f32_e32 v29, v15
	v_add_f32_e32 v15, 1.0, v24
	v_fmamk_f32 v24, v25, 0xbdd2d3e8, v99
	v_mul_f32_e32 v34, v17, v24
	v_pk_mul_f32 v[24:25], v[30:31], v[32:33] op_sel_hi:[0,1]
	v_pk_fma_f32 v[24:25], v[40:41], v[24:25], v[48:49]
	v_exp_f32_e32 v35, v34

.Lw3b58:
	v_pk_mul_f32 v[32:33], v[24:25], v[24:25]
	v_rcp_f32_e32 v34, v15
	v_fmamk_f32 v32, v32, 0xbdd2d3e8, v99
	v_fmamk_f32 v33, v33, 0xbdd2d3e8, v99
	v_mul_f32_e32 v32, v24, v32
	v_mul_f32_e32 v33, v25, v33
	v_exp_f32_e32 v32, v32
	v_exp_f32_e32 v33, v33
	v_add_f32_e32 v15, 1.0, v35
	v_rcp_f32_e32 v35, v15
	v_add_f32_e32 v32, 1.0, v32
	v_add_f32_e32 v33, 1.0, v33
	v_rcp_f32_e32 v32, v32
	v_rcp_f32_e32 v33, v33
	v_pk_mul_f32 v[22:23], v[22:23], v[28:29]
	v_pk_mul_f32 v[16:17], v[16:17], v[34:35]
	v_pk_mul_f32 v[24:25], v[24:25], v[32:33]
	s_nop 0
	v_cvt_pk_f16_f32 v16, v16, v17
	v_lshl_add_u32 v15, v31, 2, v101
	v_add_u32_e32 v48, 0x440, v15
	v_add_u32_e32 v42, 0x448, v15

.Lw3b59:
	v_add_u32_e32 v46, 0x450, v15
	ds_read2_b32 v[32:33], v15 offset0:146 offset1:147
	ds_read2_b32 v[36:37], v15 offset0:150 offset1:151
	ds_read2_b32 v[38:39], v15 offset0:148 offset1:149
	ds_read2_b32 v[40:41], v15 offset0:144 offset1:145
	v_add_u32_e32 v15, 0x458, v15
	ds_read2_b32 v[42:43], v42 offset1:1
	ds_read2_b32 v[44:45], v15 offset1:1
	ds_read2_b32 v[46:47], v46 offset1:1
	ds_read2_b32 v[48:49], v48 offset1:1
	v_cvt_pk_f16_f32 v15, v22, v23
	v_pk_mul_f32 v[12:13], v[30:31], v[12:13] op_sel_hi:[0,1]
	s_waitcnt lgkmcnt(0)
	v_pk_fma_f32 v[12:13], v[40:41], v[12:13], v[48:49]
	v_pk_mul_f32 v[18:19], v[30:31], v[18:19] op_sel_hi:[0,1]
	v_pk_mul_f32 v[22:23], v[12:13], v[12:13]

.Lw3b60:
	v_pk_fma_f32 v[28:29], v[32:33], v[18:19], v[42:43]
	v_fmamk_f32 v17, v22, 0xbdd2d3e8, v99
	v_mul_f32_e32 v17, v12, v17
	v_fmamk_f32 v22, v23, 0xbdd2d3e8, v99
	v_exp_f32_e32 v17, v17
	v_mul_f32_e32 v22, v13, v22
	v_exp_f32_e32 v23, v22
	v_pk_mul_f32 v[18:19], v[28:29], v[28:29]
	v_add_f32_e32 v17, 1.0, v17
	v_rcp_f32_e32 v22, v17
	v_add_f32_e32 v17, 1.0, v23
	v_rcp_f32_e32 v23, v17
	v_fmamk_f32 v17, v18, 0xbdd2d3e8, v99
	v_pk_mul_f32 v[10:11], v[30:31], v[10:11] op_sel_hi:[0,1]
	v_mul_f32_e32 v17, v28, v17
	v_pk_mul_f32 v[12:13], v[12:13], v[22:23]
	v_pk_fma_f32 v[10:11], v[36:37], v[10:11], v[44:45]
	v_cvt_pk_f16_f32 v18, v12, v13
	v_fmamk_f32 v12, v19, 0xbdd2d3e8, v99
	v_mul_f32_e32 v12, v29, v12

.Lw3b61:
	v_exp_f32_e32 v19, v12
	v_pk_mul_f32 v[12:13], v[30:31], v[20:21] op_sel_hi:[0,1]
	v_pk_fma_f32 v[12:13], v[38:39], v[12:13], v[46:47]
	v_exp_f32_e32 v32, v17
	v_pk_mul_f32 v[20:21], v[12:13], v[12:13]
	v_add_f32_e32 v19, 1.0, v19
	v_fmamk_f32 v20, v20, 0xbdd2d3e8, v99
	v_mul_f32_e32 v20, v12, v20
	v_exp_f32_e32 v20, v20
	v_rcp_f32_e32 v23, v19
	v_cvt_pk_f16_f32 v17, v24, v25
	v_add_f32_e32 v22, 1.0, v32
	v_add_f32_e32 v19, 1.0, v20
	v_fmamk_f32 v20, v21, 0xbdd2d3e8, v99
	v_mul_f32_e32 v24, v13, v20
	v_pk_mul_f32 v[20:21], v[10:11], v[10:11]
	v_exp_f32_e32 v25, v24
	v_fmamk_f32 v20, v20, 0xbdd2d3e8, v99
	v_fmamk_f32 v21, v21, 0xbdd2d3e8, v99
	v_mul_f32_e32 v20, v10, v20
	v_mul_f32_e32 v21, v11, v21
	v_exp_f32_e32 v20, v20

.Lw3b62:
	v_exp_f32_e32 v21, v21
	v_rcp_f32_e32 v24, v19
	v_add_f32_e32 v19, 1.0, v25
	v_add_f32_e32 v20, 1.0, v20
	v_add_f32_e32 v21, 1.0, v21
	v_rcp_f32_e32 v20, v20
	v_rcp_f32_e32 v21, v21
	v_rcp_f32_e32 v25, v19
	v_rcp_f32_e32 v22, v22
	v_pk_mul_f32 v[10:11], v[10:11], v[20:21]
	s_nop 0
	v_pk_mul_f32 v[12:13], v[12:13], v[24:25]
	v_lshl_add_u32 v19, v31, 2, v101
	v_add_u32_e32 v21, 0x468, v19
	ds_read2_b32 v[32:33], v19 offset0:154 offset1:155
	ds_read2_b32 v[34:35], v19 offset0:158 offset1:159
	ds_read2_b32 v[36:37], v19 offset0:156 offset1:157
	ds_read2_b32 v[38:39], v19 offset0:152 offset1:153
	v_add_u32_e32 v20, 0x460, v19
	v_add_u32_e32 v31, 0x470, v19
	v_add_u32_e32 v19, 0x478, v19

.Lw3b63:
	ds_read2_b32 v[40:41], v21 offset1:1
	ds_read2_b32 v[42:43], v19 offset1:1
	ds_read2_b32 v[44:45], v31 offset1:1
	ds_read2_b32 v[46:47], v20 offset1:1
	v_pk_mul_f32 v[20:21], v[28:29], v[22:23]
	s_nop 0
	v_cvt_pk_f16_f32 v19, v20, v21
	v_cvt_pk_f16_f32 v20, v12, v13
	v_pk_mul_f32 v[4:5], v[30:31], v[4:5] op_sel_hi:[0,1]
	s_waitcnt lgkmcnt(0)
	v_pk_fma_f32 v[4:5], v[38:39], v[4:5], v[46:47]
	v_cvt_pk_f16_f32 v21, v10, v11
	v_pk_mul_f32 v[12:13], v[4:5], v[4:5]
	v_pk_mul_f32 v[10:11], v[30:31], v[26:27] op_sel_hi:[0,1]
	v_fmamk_f32 v12, v12, 0xbdd2d3e8, v99
	v_fmamk_f32 v13, v13, 0xbdd2d3e8, v99

.Lw3b64:
	v_mul_f32_e32 v12, v4, v12
	v_mul_f32_e32 v13, v5, v13
	v_exp_f32_e32 v12, v12
	v_exp_f32_e32 v13, v13
	v_pk_fma_f32 v[10:11], v[32:33], v[10:11], v[40:41]
	v_pk_mul_f32 v[0:1], v[30:31], v[0:1] op_sel_hi:[0,1]
	v_add_f32_e32 v12, 1.0, v12
	v_add_f32_e32 v13, 1.0, v13
	v_rcp_f32_e32 v12, v12
	v_rcp_f32_e32 v13, v13
	v_pk_fma_f32 v[0:1], v[36:37], v[0:1], v[44:45]
	v_pk_mul_f32 v[2:3], v[30:31], v[2:3] op_sel_hi:[0,1]
	v_pk_fma_f32 v[2:3], v[34:35], v[2:3], v[42:43]
	v_pk_mul_f32 v[4:5], v[4:5], v[12:13]
	v_pk_mul_f32 v[12:13], v[10:11], v[10:11]
	v_cvt_pk_f16_f32 v24, v4, v5
	v_fmamk_f32 v12, v12, 0xbdd2d3e8, v99
	v_fmamk_f32 v13, v13, 0xbdd2d3e8, v99
	v_mul_f32_e32 v12, v10, v12
	v_mul_f32_e32 v13, v11, v13
	v_exp_f32_e32 v12, v12

.Lw3b65:
	v_exp_f32_e32 v13, v13
	v_add_f32_e32 v4, 1.0, v12
	v_add_f32_e32 v5, 1.0, v13
	v_pk_mul_f32 v[12:13], v[0:1], v[0:1]
	v_rcp_f32_e32 v4, v4
	v_fmamk_f32 v12, v12, 0xbdd2d3e8, v99
	v_fmamk_f32 v13, v13, 0xbdd2d3e8, v99
	v_mul_f32_e32 v12, v0, v12
	v_mul_f32_e32 v13, v1, v13
	v_rcp_f32_e32 v5, v5
	v_exp_f32_e32 v12, v12
	v_exp_f32_e32 v13, v13
	v_pk_mul_f32 v[4:5], v[10:11], v[4:5]
	v_add_f32_e32 v10, 1.0, v12
	v_add_f32_e32 v11, 1.0, v13
	v_pk_mul_f32 v[12:13], v[2:3], v[2:3]
	v_rcp_f32_e32 v10, v10
	v_fmamk_f32 v12, v12, 0xbdd2d3e8, v99
	v_fmamk_f32 v13, v13, 0xbdd2d3e8, v99
	v_mul_f32_e32 v12, v2, v12
	v_mul_f32_e32 v13, v3, v13
	v_exp_f32_e32 v12, v12
	v_exp_f32_e32 v13, v13
	v_rcp_f32_e32 v11, v11

.Lw3b66:
	v_cvt_pk_f16_f32 v25, v4, v5
	v_add_f32_e32 v12, 1.0, v12
	v_add_f32_e32 v13, 1.0, v13
	v_rcp_f32_e32 v12, v12
	v_rcp_f32_e32 v13, v13
	v_pk_mul_f32 v[0:1], v[0:1], v[10:11]
	s_nop 0
	v_cvt_pk_f16_f32 v26, v0, v1
	v_pk_mul_f32 v[0:1], v[2:3], v[12:13]
	s_nop 0
	v_cvt_pk_f16_f32 v27, v0, v1
	ds_read_b128 v[0:3], v96 offset:1536
	ds_read_b128 v[10:13], v96 offset:1552
	ds_read_b128 v[30:33], v96 offset:1568
	ds_read_b128 v[34:37], v96 offset:1584
	ds_read_b128 v[38:41], v96 offset:1600
	ds_read_b128 v[42:45], v96 offset:1616
	ds_read_b128 v[46:49], v96 offset:1632
	ds_read_b128 v[50:53], v96 offset:1648

.Lw3b67:
	v_mov_b32_e32 v4, v77
	s_nop 0
	v_lshl_add_u32 v28, v4, 4, v102
	ds_read_b128 v[54:57], v28
	ds_read_b128 v[58:61], v28 offset:1024
	ds_read_b128 v[62:65], v28 offset:2048
	ds_read_b128 v[66:69], v28 offset:3072
	ds_read_b128 v[104:107], v28 offset:4096
	ds_read_b128 v[108:111], v28 offset:5120
	ds_read_b128 v[112:115], v28 offset:6144
	ds_read_b128 v[116:119], v28 offset:7168
	s_waitcnt lgkmcnt(7)
	v_mfma_f32_16x16x32_f16 v[0:3], v[54:57], v[6:9], v[0:3]
	s_waitcnt lgkmcnt(6)
	v_mfma_f32_16x16x32_f16 v[10:13], v[58:61], v[6:9], v[10:13]
	s_waitcnt lgkmcnt(5)
	v_mfma_f32_16x16x32_f16 v[30:33], v[62:65], v[6:9], v[30:33]
	s_waitcnt lgkmcnt(4)

.Lw3b68:
	v_mfma_f32_16x16x32_f16 v[34:37], v[66:69], v[6:9], v[34:37]
	ds_read_b128 v[54:57], v28 offset:8192
	ds_read_b128 v[58:61], v28 offset:9216
	ds_read_b128 v[62:65], v28 offset:10240
	ds_read_b128 v[66:69], v28 offset:11264
	s_waitcnt lgkmcnt(7)
	v_mfma_f32_16x16x32_f16 v[38:41], v[104:107], v[6:9], v[38:41]
	s_waitcnt lgkmcnt(6)
	v_mfma_f32_16x16x32_f16 v[42:45], v[108:111], v[6:9], v[42:45]
	s_waitcnt lgkmcnt(5)
	v_mfma_f32_16x16x32_f16 v[46:49], v[112:115], v[6:9], v[46:49]
	s_waitcnt lgkmcnt(4)
	v_mfma_f32_16x16x32_f16 v[4:7], v[116:119], v[6:9], v[50:53]
	s_nop 2
	ds_read_b128 v[50:53], v28 offset:12288
	ds_read_b128 v[104:107], v28 offset:13312
	ds_read_b128 v[108:111], v28 offset:14336
	ds_read_b128 v[112:115], v28 offset:15360

.Lw3b69:
	s_waitcnt lgkmcnt(7)
	v_mfma_f32_16x16x32_f16 v[0:3], v[54:57], v[14:17], v[0:3]
	s_waitcnt lgkmcnt(6)
	v_mfma_f32_16x16x32_f16 v[8:11], v[58:61], v[14:17], v[10:13]
	s_waitcnt lgkmcnt(5)
	v_mfma_f32_16x16x32_f16 v[30:33], v[62:65], v[14:17], v[30:33]
	s_waitcnt lgkmcnt(4)
	v_mfma_f32_16x16x32_f16 v[34:37], v[66:69], v[14:17], v[34:37]
	ds_read_b128 v[54:57], v28 offset:16384
	ds_read_b128 v[58:61], v28 offset:17408
	ds_read_b128 v[62:65], v28 offset:18432
	ds_read_b128 v[66:69], v28 offset:19456
	s_waitcnt lgkmcnt(7)
	v_mfma_f32_16x16x32_f16 v[38:41], v[50:53], v[14:17], v[38:41]
	s_waitcnt lgkmcnt(6)
	v_mfma_f32_16x16x32_f16 v[42:45], v[104:107], v[14:17], v[42:45]
	s_waitcnt lgkmcnt(5)
	v_mfma_f32_16x16x32_f16 v[46:49], v[108:111], v[14:17], v[46:49]
	s_waitcnt lgkmcnt(4)
	v_mfma_f32_16x16x32_f16 v[4:7], v[112:115], v[14:17], v[4:7]

.Lw3b70:
	ds_read_b128 v[12:15], v28 offset:20480
	ds_read_b128 v[50:53], v28 offset:21504
	ds_read_b128 v[104:107], v28 offset:22528
	ds_read_b128 v[108:111], v28 offset:23552
	s_waitcnt lgkmcnt(7)
	v_mfma_f32_16x16x32_f16 v[0:3], v[54:57], v[18:21], v[0:3]
	s_waitcnt lgkmcnt(6)
	v_mfma_f32_16x16x32_f16 v[8:11], v[58:61], v[18:21], v[8:11]
	s_waitcnt lgkmcnt(5)
	v_mfma_f32_16x16x32_f16 v[30:33], v[62:65], v[18:21], v[30:33]
	s_waitcnt lgkmcnt(4)
	v_mfma_f32_16x16x32_f16 v[34:37], v[66:69], v[18:21], v[34:37]
	ds_read_b128 v[54:57], v28 offset:24576
	ds_read_b128 v[58:61], v28 offset:25600
	ds_read_b128 v[62:65], v28 offset:26624
	ds_read_b128 v[66:69], v28 offset:27648
	s_waitcnt lgkmcnt(7)
	v_mfma_f32_16x16x32_f16 v[12:15], v[12:15], v[18:21], v[38:41]

.Lw3b71:
	s_waitcnt lgkmcnt(6)
	v_mfma_f32_16x16x32_f16 v[38:41], v[50:53], v[18:21], v[42:45]
	s_waitcnt lgkmcnt(5)
	v_mfma_f32_16x16x32_f16 v[42:45], v[104:107], v[18:21], v[46:49]
	s_waitcnt lgkmcnt(4)
	v_mfma_f32_16x16x32_f16 v[46:49], v[108:111], v[18:21], v[4:7]
	s_nop 2
	ds_read_b128 v[4:7], v28 offset:28672
	ds_read_b128 v[50:53], v28 offset:29696
	ds_read_b128 v[104:107], v28 offset:30720
	ds_read_b128 v[108:111], v28 offset:31744
	s_waitcnt lgkmcnt(7)
	v_mfma_f32_16x16x32_f16 v[54:57], v[54:57], v[24:27], v[0:3]
	s_waitcnt lgkmcnt(6)
	v_mfma_f32_16x16x32_f16 v[58:61], v[58:61], v[24:27], v[8:11]
	s_waitcnt lgkmcnt(5)
	v_mfma_f32_16x16x32_f16 v[20:23], v[62:65], v[24:27], v[30:33]
	s_waitcnt lgkmcnt(4)
	v_mfma_f32_16x16x32_f16 v[16:19], v[66:69], v[24:27], v[34:37]

.Lw3b72:
	s_waitcnt lgkmcnt(0)
	v_mfma_f32_16x16x32_f16 v[0:3], v[108:111], v[24:27], v[46:49]
	v_mfma_f32_16x16x32_f16 v[12:15], v[4:7], v[24:27], v[12:15]
	v_mfma_f32_16x16x32_f16 v[8:11], v[50:53], v[24:27], v[38:41]
	v_mfma_f32_16x16x32_f16 v[4:7], v[104:107], v[24:27], v[42:45]
	v_mul_f32_e32 v24, v54, v54
	v_fmamk_f32 v24, v24, 0xbdd2d3e8, v99
	v_mul_f32_e32 v24, v54, v24
	v_exp_f32_e32 v24, v24
	v_mul_f32_e32 v25, v55, v55
	v_mul_f32_e32 v26, v56, v56
	v_fmamk_f32 v25, v25, 0xbdd2d3e8, v99
	v_fmamk_f32 v26, v26, 0xbdd2d3e8, v99
	v_mul_f32_e32 v25, v55, v25
	v_add_f32_e32 v24, 1.0, v24
	v_mul_f32_e32 v26, v56, v26
	v_rcp_f32_e32 v24, v24
	v_exp_f32_e32 v25, v25
	v_exp_f32_e32 v26, v26
	v_mul_f32_e32 v30, v57, v57
	v_mul_f32_e32 v31, v58, v58
	v_fmamk_f32 v30, v30, 0xbdd2d3e8, v99
	v_fmamk_f32 v31, v31, 0xbdd2d3e8, v99

.Lw3b73:
	v_fma_mixlo_f16 v29, v54, v24, 0
	v_add_f32_e32 v24, 1.0, v25
	v_add_f32_e32 v25, 1.0, v26
	v_mul_f32_e32 v30, v57, v30
	v_mul_f32_e32 v31, v58, v31
	v_rcp_f32_e32 v24, v24
	v_rcp_f32_e32 v25, v25
	v_exp_f32_e32 v30, v30
	v_exp_f32_e32 v31, v31
	v_mov_b32_e32 v26, v55
	v_mov_b32_e32 v27, v56
	v_pk_mul_f32 v[24:25], v[26:27], v[24:25]
	v_add_f32_e32 v26, 1.0, v30
	v_add_f32_e32 v27, 1.0, v31
	v_rcp_f32_e32 v26, v26
	v_rcp_f32_e32 v27, v27
	v_cvt_pk_f16_f32 v25, v24, v25
	v_pk_mov_b32 v[30:31], v[56:57], v[58:59] op_sel:[1,0]
	v_pack_b32_f16 v24, v29, v25
	v_pk_mul_f32 v[26:27], v[30:31], v[26:27]
	v_mul_f32_e32 v29, v59, v59
	v_mul_f32_e32 v30, v60, v60
	v_fmamk_f32 v29, v29, 0xbdd2d3e8, v99

.Lw3b74:
	v_fmamk_f32 v30, v30, 0xbdd2d3e8, v99
	v_mul_f32_e32 v29, v59, v29
	v_mul_f32_e32 v30, v60, v30
	v_exp_f32_e32 v29, v29
	v_exp_f32_e32 v30, v30
	v_cvt_pk_f16_f32 v32, v26, v27
	v_mov_b32_e32 v31, v60
	v_add_f32_e32 v26, 1.0, v29
	v_add_f32_e32 v27, 1.0, v30
	v_rcp_f32_e32 v26, v26
	v_rcp_f32_e32 v27, v27
	v_mov_b32_e32 v30, v59
	v_alignbit_b32 v25, v32, v25, 16
	v_mul_f32_e32 v34, v20, v20
	v_pk_mul_f32 v[26:27], v[30:31], v[26:27]
	v_fmamk_f32 v34, v34, 0xbdd2d3e8, v99
	v_cvt_pk_f16_f32 v27, v26, v27
	v_mul_f32_e32 v26, v61, v61
	v_fmamk_f32 v26, v26, 0xbdd2d3e8, v99
	v_mul_f32_e32 v26, v61, v26
	v_exp_f32_e32 v29, v26
	v_alignbit_b32 v26, v27, v32, 16
	ds_read_b128 v[30:33], v28 offset:32768

.Lw3b75:
	v_mul_f32_e32 v34, v20, v34
	v_add_f32_e32 v29, 1.0, v29
	v_rcp_f32_e32 v29, v29
	v_lshrrev_b32_e32 v27, 16, v27
	v_exp_f32_e32 v38, v34
	ds_read_b128 v[34:37], v28 offset:33792
	v_fma_mixhi_f16 v27, v61, v29, 0
	v_add_f32_e32 v29, 1.0, v38
	s_waitcnt lgkmcnt(1)
	v_mfma_f32_16x16x32_f16 v[24:27], v[30:33], v[24:27], 0
	v_mul_f32_e32 v30, v21, v21
	v_fmamk_f32 v30, v30, 0xbdd2d3e8, v99
	v_mul_f32_e32 v31, v22, v22
	v_mul_f32_e32 v30, v21, v30
	v_fmamk_f32 v31, v31, 0xbdd2d3e8, v99
	v_rcp_f32_e32 v29, v29
	v_exp_f32_e32 v30, v30
	v_mul_f32_e32 v31, v22, v31
	v_exp_f32_e32 v31, v31
	v_fma_mixlo_f16 v29, v20, v29, 0
	v_add_f32_e32 v20, 1.0, v30
	v_rcp_f32_e32 v30, v20
	v_add_f32_e32 v20, 1.0, v31
	v_rcp_f32_e32 v31, v20

.Lw3b76:
	v_mov_b32_e32 v20, v21
	v_mov_b32_e32 v21, v22
	v_mul_f32_e32 v22, v23, v23
	v_fmamk_f32 v22, v22, 0xbdd2d3e8, v99
	v_mul_f32_e32 v32, v16, v16
	v_mul_f32_e32 v22, v23, v22
	v_fmamk_f32 v32, v32, 0xbdd2d3e8, v99
	v_exp_f32_e32 v22, v22
	v_mul_f32_e32 v32, v16, v32
	v_exp_f32_e32 v32, v32
	v_pk_mul_f32 v[20:21], v[20:21], v[30:31]
	v_add_f32_e32 v22, 1.0, v22
	v_rcp_f32_e32 v30, v22
	v_add_f32_e32 v22, 1.0, v32
	v_rcp_f32_e32 v31, v22
	v_pk_mov_b32 v[22:23], v[22:23], v[16:17] op_sel:[1,0]
	v_cvt_pk_f16_f32 v21, v20, v21
	v_mul_f32_e32 v16, v17, v17
	v_pk_mul_f32 v[22:23], v[22:23], v[30:31]
	v_pack_b32_f16 v20, v29, v21
	v_cvt_pk_f16_f32 v29, v22, v23
	v_fmamk_f32 v16, v16, 0xbdd2d3e8, v99

.Lw3b77:
	v_mul_f32_e32 v22, v18, v18
	v_mul_f32_e32 v16, v17, v16
	v_fmamk_f32 v22, v22, 0xbdd2d3e8, v99
	v_exp_f32_e32 v16, v16
	v_mul_f32_e32 v22, v18, v22
	v_exp_f32_e32 v23, v22
	v_alignbit_b32 v21, v29, v21, 16
	v_add_f32_e32 v16, 1.0, v16
	v_rcp_f32_e32 v22, v16
	v_add_f32_e32 v16, 1.0, v23
	v_rcp_f32_e32 v23, v16
	v_mul_f32_e32 v16, v19, v19
	v_fmamk_f32 v16, v16, 0xbdd2d3e8, v99
	v_mul_f32_e32 v16, v19, v16
	v_exp_f32_e32 v30, v16
	v_mov_b32_e32 v16, v17
	v_mov_b32_e32 v17, v18
	v_pk_mul_f32 v[16:17], v[16:17], v[22:23]
	v_add_f32_e32 v18, 1.0, v30
	v_rcp_f32_e32 v18, v18
	v_cvt_pk_f16_f32 v16, v16, v17
	v_lshrrev_b32_e32 v23, 16, v16
	v_alignbit_b32 v22, v16, v29, 16
	v_fma_mixhi_f16 v23, v19, v18, 0

.Lw3b78:
	s_waitcnt lgkmcnt(0)
	s_nop 0
	v_mfma_f32_16x16x32_f16 v[16:19], v[34:37], v[20:23], v[24:27]
	v_mul_f32_e32 v20, v12, v12
	v_fmamk_f32 v20, v20, 0xbdd2d3e8, v99
	v_mul_f32_e32 v20, v12, v20
	v_exp_f32_e32 v20, v20
	v_mul_f32_e32 v21, v13, v13
	v_fmamk_f32 v21, v21, 0xbdd2d3e8, v99
	v_mul_f32_e32 v22, v14, v14
	v_mul_f32_e32 v21, v13, v21
	v_add_f32_e32 v20, 1.0, v20
	v_fmamk_f32 v22, v22, 0xbdd2d3e8, v99
	v_rcp_f32_e32 v20, v20
	v_exp_f32_e32 v21, v21
	v_mul_f32_e32 v22, v14, v22
	v_exp_f32_e32 v22, v22
	v_fma_mixlo_f16 v23, v12, v20, 0
	v_add_f32_e32 v12, 1.0, v21
	v_rcp_f32_e32 v20, v12
	v_add_f32_e32 v12, 1.0, v22
	v_rcp_f32_e32 v21, v12
	v_mov_b32_e32 v12, v13
	v_mov_b32_e32 v13, v14
	v_mul_f32_e32 v14, v15, v15
	v_fmamk_f32 v14, v14, 0xbdd2d3e8, v99

.Lw3b79:
	v_mul_f32_e32 v22, v8, v8
	v_mul_f32_e32 v14, v15, v14
	v_fmamk_f32 v22, v22, 0xbdd2d3e8, v99
	v_exp_f32_e32 v14, v14
	v_mul_f32_e32 v22, v8, v22
	v_exp_f32_e32 v22, v22
	v_pk_mul_f32 v[12:13], v[12:13], v[20:21]
	v_add_f32_e32 v14, 1.0, v14
	v_rcp_f32_e32 v20, v14
	v_add_f32_e32 v14, 1.0, v22
	v_rcp_f32_e32 v21, v14
	v_pk_mov_b32 v[14:15], v[14:15], v[8:9] op_sel:[1,0]
	v_mul_f32_e32 v8, v9, v9
	v_fmamk_f32 v8, v8, 0xbdd2d3e8, v99
	v_pk_mul_f32 v[14:15], v[14:15], v[20:21]
	v_mul_f32_e32 v20, v10, v10
	v_mul_f32_e32 v8, v9, v8
	v_fmamk_f32 v20, v20, 0xbdd2d3e8, v99
	v_exp_f32_e32 v8, v8
	v_mul_f32_e32 v20, v10, v20
	v_exp_f32_e32 v20, v20
	v_cvt_pk_f16_f32 v21, v14, v15
	v_add_f32_e32 v8, 1.0, v8

.Lw3b80:
	v_rcp_f32_e32 v14, v8
	v_add_f32_e32 v8, 1.0, v20
	v_rcp_f32_e32 v15, v8
	v_mov_b32_e32 v8, v9
	v_mov_b32_e32 v9, v10
	v_cvt_pk_f16_f32 v13, v12, v13
	v_pk_mul_f32 v[8:9], v[8:9], v[14:15]
	v_pack_b32_f16 v12, v23, v13
	v_cvt_pk_f16_f32 v8, v8, v9
	v_mul_f32_e32 v9, v11, v11
	v_fmamk_f32 v9, v9, 0xbdd2d3e8, v99
	v_mul_f32_e32 v9, v11, v9
	v_exp_f32_e32 v9, v9
	v_alignbit_b32 v13, v21, v13, 16
	v_alignbit_b32 v14, v8, v21, 16
	ds_read_b128 v[20:23], v28 offset:34816
	v_lshrrev_b32_e32 v15, 16, v8
	v_add_f32_e32 v8, 1.0, v9
	v_rcp_f32_e32 v8, v8
	v_mul_f32_e32 v9, v4, v4
	v_fmamk_f32 v9, v9, 0xbdd2d3e8, v99
	v_mul_f32_e32 v9, v4, v9

.Lw3b81:
	v_exp_f32_e32 v24, v9
	v_fma_mixhi_f16 v15, v11, v8, 0
	ds_read_b128 v[8:11], v28 offset:35840
	s_waitcnt lgkmcnt(1)
	v_mfma_f32_16x16x32_f16 v[12:15], v[20:23], v[12:15], v[16:19]
	s_nop 2
	v_mul_f32_e32 v17, v5, v5
	v_fmamk_f32 v17, v17, 0xbdd2d3e8, v99
	v_mul_f32_e32 v18, v6, v6
	v_add_f32_e32 v16, 1.0, v24
	v_mul_f32_e32 v17, v5, v17
	v_fmamk_f32 v18, v18, 0xbdd2d3e8, v99
	v_rcp_f32_e32 v16, v16
	v_exp_f32_e32 v17, v17
	v_mul_f32_e32 v18, v6, v18
	v_exp_f32_e32 v18, v18
	v_fma_mixlo_f16 v19, v4, v16, 0
	v_add_f32_e32 v4, 1.0, v17
	v_rcp_f32_e32 v16, v4
	v_add_f32_e32 v4, 1.0, v18
	v_rcp_f32_e32 v17, v4
	v_mov_b32_e32 v4, v5
	v_mov_b32_e32 v5, v6
	v_mul_f32_e32 v6, v7, v7
	v_fmamk_f32 v6, v6, 0xbdd2d3e8, v99

.Lw3b82:
	v_mul_f32_e32 v18, v0, v0
	v_mul_f32_e32 v6, v7, v6
	v_fmamk_f32 v18, v18, 0xbdd2d3e8, v99
	v_exp_f32_e32 v6, v6
	v_mul_f32_e32 v18, v0, v18
	v_exp_f32_e32 v18, v18
	v_pk_mul_f32 v[4:5], v[4:5], v[16:17]
	v_add_f32_e32 v6, 1.0, v6
	v_rcp_f32_e32 v16, v6
	v_add_f32_e32 v6, 1.0, v18
	v_rcp_f32_e32 v17, v6
	v_pk_mov_b32 v[6:7], v[6:7], v[0:1] op_sel:[1,0]
	v_mul_f32_e32 v0, v1, v1
	v_fmamk_f32 v0, v0, 0xbdd2d3e8, v99
	v_pk_mul_f32 v[6:7], v[6:7], v[16:17]
	v_mul_f32_e32 v0, v1, v0
	v_cvt_pk_f16_f32 v16, v6, v7
	v_mul_f32_e32 v6, v2, v2
	v_fmamk_f32 v6, v6, 0xbdd2d3e8, v99
	v_exp_f32_e32 v0, v0
	v_mul_f32_e32 v6, v2, v6
	v_exp_f32_e32 v7, v6
	v_cvt_pk_f16_f32 v5, v4, v5

.Lw3b83:
	v_add_f32_e32 v0, 1.0, v0
	v_rcp_f32_e32 v6, v0
	v_add_f32_e32 v0, 1.0, v7
	v_rcp_f32_e32 v7, v0
	v_mul_f32_e32 v0, v3, v3
	v_fmamk_f32 v0, v0, 0xbdd2d3e8, v99
	v_mul_f32_e32 v0, v3, v0
	v_exp_f32_e32 v17, v0
	v_mov_b32_e32 v0, v1
	v_mov_b32_e32 v1, v2
	v_pk_mul_f32 v[0:1], v[0:1], v[6:7]
	v_add_f32_e32 v2, 1.0, v17
	v_rcp_f32_e32 v2, v2
	v_cvt_pk_f16_f32 v0, v0, v1
	v_lshrrev_b32_e32 v7, 16, v0
	v_pack_b32_f16 v4, v19, v5
	v_alignbit_b32 v5, v16, v5, 16
	v_alignbit_b32 v6, v0, v16, 16
	v_fma_mixhi_f16 v7, v3, v2, 0
	s_waitcnt lgkmcnt(0)
	s_nop 0
	v_mfma_f32_16x16x32_f16 v[0:3], v[8:11], v[4:7], v[12:15]

.Lw3b84:
	s_and_saveexec_b64 s[14:15], s[4:5]
	s_xor_b64 s[14:15], exec, s[14:15]
	s_cbranch_execz .LBB3_9
	s_load_dwordx2 s[20:21], s[16:17], 0x0
	s_nop 3
	v_or_b32_e32 v2, s10, v80
	v_ashrrev_i32_e32 v3, 31, v2
	v_lshl_add_u64 v[2:3], v[2:3], 3, s[6:7]
	s_waitcnt lgkmcnt(0)
	v_pk_add_f32 v[0:1], v[0:1], s[20:21]
	global_store_dwordx2 v[2:3], v[0:1], off
	s_branch .LBB3_9
